# speedup vs baseline: 1.0423x; 1.0423x over previous
_Z4k_k2ILb0EEvPKDF16_S1_PKfS3_S3_S1_S1_PfS3_S3_S1_PDF16_PKiS4_S4_:
	s_load_dwordx2 s[24:25], s[0:1], 0x58
	s_load_dwordx8 s[4:11], s[0:1], 0x38
	s_load_dwordx4 s[20:23], s[0:1], 0x0
	s_load_dwordx8 s[12:19], s[0:1], 0x18
	s_load_dwordx2 s[54:55], s[0:1], 0x10
	s_lshl_b32 s3, s2, 5
	s_and_b32 s3, s3, 0xe0
	s_lshr_b32 s26, s2, 3
	s_or_b32 s3, s3, s26
	s_movk_i32 s26, 0x100
	s_lshl_b32 s28, s3, 5
	v_cmp_gt_u32_e32 vcc, s26, v0
	v_mov_b32_e32 v67, 0
	v_lshlrev_b32_e32 v66, 4, v0
	s_lshl_b32 s0, s3, 1
	s_and_b32 s26, s0, 0xffffffe
	s_mov_b32 s27, 0
	s_waitcnt lgkmcnt(0)
	v_lshl_add_u64 v[2:3], s[16:17], 0, v[66:67]
	s_lshl_b64 s[0:1], s[26:27], 13
	s_or_b32 s26, s26, 1
	v_lshl_add_u64 v[4:5], v[2:3], 0, s[0:1]
	s_lshl_b64 s[0:1], s[26:27], 13
	v_lshl_add_u64 v[2:3], v[2:3], 0, s[0:1]
	global_load_dwordx4 v[68:71], v[4:5], off
	global_load_dwordx4 v[72:75], v[2:3], off
	v_lshl_add_u64 v[2:3], s[12:13], 0, v[66:67]
	s_movk_i32 s29, 0x2000
	v_add_co_u32_e32 v4, vcc, s29, v2
	s_movk_i32 s52, 0x4000
	s_nop 0
	v_addc_co_u32_e32 v5, vcc, 0, v3, vcc
	v_add_co_u32_e32 v18, vcc, s52, v2
	s_movk_i32 s33, 0x6000
	s_nop 0
	v_addc_co_u32_e32 v19, vcc, 0, v3, vcc
	s_lshl_b32 s26, s3, 2
	global_load_dwordx4 v[14:17], v66, s[12:13]
	global_load_dwordx4 v[10:13], v[4:5], off
	global_load_dwordx4 v[6:9], v[18:19], off
	v_add_co_u32_e32 v18, vcc, s33, v2
	s_add_u32 s0, s24, 0x800000
	s_nop 0
	v_addc_co_u32_e32 v19, vcc, 0, v3, vcc
	s_addc_u32 s1, s25, 0
	s_lshl_b64 s[12:13], s[26:27], 13
	v_lshlrev_b32_e32 v20, 2, v0
	global_load_dwordx4 v[2:5], v[18:19], off
	global_load_dword v1, v20, s[14:15]
	v_or_b32_e32 v18, s12, v66
	v_mov_b32_e32 v19, s13
	s_or_b32 s12, s26, 1
	s_mov_b32 s13, s27
	s_lshl_b64 s[12:13], s[12:13], 13
	v_lshl_add_u64 v[76:77], s[22:23], 0, v[18:19]
	v_lshl_add_u64 v[78:79], s[20:21], 0, v[18:19]
	v_lshl_add_u64 v[80:81], s[0:1], 0, v[18:19]
	v_or_b32_e32 v18, s12, v66
	v_mov_b32_e32 v19, s13
	s_or_b32 s12, s26, 2
	s_mov_b32 s13, s27
	s_lshl_b64 s[12:13], s[12:13], 13
	s_or_b32 s26, s26, 3
	v_lshl_add_u64 v[82:83], s[22:23], 0, v[18:19]
	v_lshl_add_u64 v[84:85], s[20:21], 0, v[18:19]
	v_lshl_add_u64 v[86:87], s[0:1], 0, v[18:19]
	v_or_b32_e32 v18, s12, v66
	v_mov_b32_e32 v19, s13
	s_lshl_b64 s[12:13], s[26:27], 13
	v_lshl_add_u64 v[88:89], s[22:23], 0, v[18:19]
	v_lshl_add_u64 v[90:91], s[20:21], 0, v[18:19]
	v_lshl_add_u64 v[92:93], s[0:1], 0, v[18:19]
	v_or_b32_e32 v18, s12, v66
	v_mov_b32_e32 v19, s13
	v_lshl_add_u64 v[94:95], s[22:23], 0, v[18:19]
	v_lshl_add_u64 v[96:97], s[20:21], 0, v[18:19]
	v_lshl_add_u64 v[98:99], s[0:1], 0, v[18:19]
	global_load_dwordx4 v[62:65], v[76:77], off
	global_load_dwordx4 v[54:57], v[78:79], off
	global_load_dwordx4 v[58:61], v[80:81], off
	v_mov_b64_e32 v[212:213], v[82:83]
	v_mov_b64_e32 v[214:215], v[84:85]
	v_mov_b64_e32 v[216:217], v[86:87]
	v_mov_b64_e32 v[218:219], v[88:89]
	v_mov_b64_e32 v[220:221], v[90:91]
	v_mov_b64_e32 v[222:223], v[92:93]
	v_mov_b64_e32 v[224:225], v[94:95]
	v_mov_b64_e32 v[226:227], v[96:97]
	v_mov_b64_e32 v[228:229], v[98:99]
	s_lshl_b32 s30, s28, 7
	s_add_u32 s54, s54, s30
	s_addc_u32 s55, s55, 0
	s_load_dwordx16 s[36:51], s[54:55], 0x0
	s_load_dwordx16 s[72:87], s[54:55], 0x40
	s_load_dwordx16 s[56:71], s[54:55], 0x80
	s_load_dwordx8 s[88:95], s[54:55], 0xc0
	s_load_dwordx4 s[96:99], s[54:55], 0xe0
	s_load_dwordx4 s[20:23], s[54:55], 0xf0
	v_lshrrev_b32_e32 v196, 6, v0
	s_nop 1
	v_readfirstlane_b32 s16, v196
	s_nop 3
	s_lshl_b32 s16, s16, 9
	s_add_u32 s16, s54, s16
	s_addc_u32 s17, s55, 0
	s_load_dword s30, s[16:17], 0x0
	s_load_dword s30, s[16:17], 0x40
	s_load_dword s30, s[16:17], 0x80
	s_load_dword s30, s[16:17], 0xc0
	s_load_dword s30, s[16:17], 0x100
	s_load_dword s30, s[16:17], 0x140
	s_load_dword s30, s[16:17], 0x180
	s_load_dword s30, s[16:17], 0x1c0
	s_barrier
	s_waitcnt vmcnt(9)
	v_cvt_f32_f16_e32 v134, v68
	v_cvt_f32_f16_sdwa v135, v68 dst_sel:DWORD dst_unused:UNUSED_PAD src0_sel:WORD_1
	v_cvt_f32_f16_e32 v136, v69
	v_cvt_f32_f16_sdwa v137, v69 dst_sel:DWORD dst_unused:UNUSED_PAD src0_sel:WORD_1
	v_cvt_f32_f16_e32 v138, v70
	v_cvt_f32_f16_sdwa v139, v70 dst_sel:DWORD dst_unused:UNUSED_PAD src0_sel:WORD_1
	v_cvt_f32_f16_e32 v140, v71
	v_cvt_f32_f16_sdwa v141, v71 dst_sel:DWORD dst_unused:UNUSED_PAD src0_sel:WORD_1
	s_waitcnt vmcnt(8)
	v_cvt_f32_f16_e32 v142, v72
	v_cvt_f32_f16_sdwa v143, v72 dst_sel:DWORD dst_unused:UNUSED_PAD src0_sel:WORD_1
	v_cvt_f32_f16_e32 v144, v73
	v_cvt_f32_f16_sdwa v145, v73 dst_sel:DWORD dst_unused:UNUSED_PAD src0_sel:WORD_1
	v_cvt_f32_f16_e32 v146, v74
	v_cvt_f32_f16_sdwa v147, v74 dst_sel:DWORD dst_unused:UNUSED_PAD src0_sel:WORD_1
	v_cvt_f32_f16_e32 v148, v75
	v_cvt_f32_f16_sdwa v149, v75 dst_sel:DWORD dst_unused:UNUSED_PAD src0_sel:WORD_1
	s_waitcnt lgkmcnt(0)
	v_lshlrev_b32_e32 v68, 1, v0
	s_waitcnt vmcnt(2)
	v_cvt_f32_f16_e32 v150, v62
	s_waitcnt vmcnt(1)
	v_cvt_f32_f16_e32 v69, v54
	v_pk_mul_f32 v[154:155], v[150:151], v[14:15] op_sel_hi:[0,1]
	v_exp_f32_e32 v154, v154
	v_exp_f32_e32 v155, v155
	v_pk_mul_f32 v[156:157], v[150:151], v[16:17] op_sel_hi:[0,1]
	v_exp_f32_e32 v156, v156
	v_exp_f32_e32 v157, v157
	v_mul_f32_e32 v152, v150, v69
	v_pk_mul_f32 v[134:135], v[154:155], v[134:135]
	v_pk_fma_f32 v[134:135], v[152:153], s[36:37], v[134:135] op_sel_hi:[0, 1, 1]
	v_pk_fma_f32 v[70:71], s[72:73], v[134:135], 0 op_sel_hi:[1, 1, 0]
	v_pk_mul_f32 v[86:87], v[156:157], v[136:137]
	s_nop 0
	v_pk_fma_f32 v[136:137], v[152:153], s[38:39], v[86:87] op_sel_hi:[0, 1, 1]
	v_pk_mul_f32 v[72:73], v[150:151], v[10:11] op_sel_hi:[0,1]
	v_exp_f32_e32 v72, v72
	v_exp_f32_e32 v73, v73
	v_pk_mul_f32 v[86:87], v[150:151], v[12:13] op_sel_hi:[0,1]
	v_exp_f32_e32 v86, v86
	v_exp_f32_e32 v87, v87
	v_pk_mul_f32 v[72:73], v[72:73], v[138:139]
	v_pk_fma_f32 v[70:71], s[74:75], v[136:137], v[70:71]
	v_pk_fma_f32 v[138:139], v[152:153], s[40:41], v[72:73] op_sel_hi:[0, 1, 1]
	v_pk_mul_f32 v[72:73], v[86:87], v[140:141]
	v_pk_mul_f32 v[74:75], v[150:151], v[8:9] op_sel_hi:[0,1]
	v_pk_fma_f32 v[140:141], v[152:153], s[42:43], v[72:73] op_sel_hi:[0, 1, 1]
	v_pk_mul_f32 v[72:73], v[150:151], v[6:7] op_sel_hi:[0,1]
	v_exp_f32_e32 v72, v72
	v_exp_f32_e32 v73, v73
	v_exp_f32_e32 v74, v74
	v_exp_f32_e32 v75, v75
	v_pk_fma_f32 v[70:71], s[76:77], v[138:139], v[70:71]
	v_pk_mul_f32 v[72:73], v[72:73], v[142:143]
	v_pk_fma_f32 v[70:71], s[78:79], v[140:141], v[70:71]
	v_pk_fma_f32 v[142:143], v[152:153], s[44:45], v[72:73] op_sel_hi:[0, 1, 1]
	v_pk_mul_f32 v[72:73], v[74:75], v[144:145]
	v_pk_mul_f32 v[74:75], v[150:151], v[4:5] op_sel_hi:[0,1]
	v_pk_fma_f32 v[144:145], v[152:153], s[46:47], v[72:73] op_sel_hi:[0, 1, 1]
	v_pk_mul_f32 v[72:73], v[150:151], v[2:3] op_sel_hi:[0,1]
	v_exp_f32_e32 v72, v72
	v_exp_f32_e32 v73, v73
	v_exp_f32_e32 v74, v74
	v_exp_f32_e32 v75, v75
	v_pk_fma_f32 v[70:71], s[80:81], v[142:143], v[70:71]
	v_pk_mul_f32 v[72:73], v[72:73], v[146:147]
	v_pk_fma_f32 v[70:71], s[82:83], v[144:145], v[70:71]
	v_pk_fma_f32 v[146:147], v[152:153], s[48:49], v[72:73] op_sel_hi:[0, 1, 1]
	v_pk_mul_f32 v[72:73], v[74:75], v[148:149]
	v_pk_fma_f32 v[70:71], s[84:85], v[146:147], v[70:71]
	v_pk_fma_f32 v[148:149], v[152:153], s[50:51], v[72:73] op_sel_hi:[0, 1, 1]
	v_pk_fma_f32 v[70:71], s[86:87], v[148:149], v[70:71]
	s_nop 0
	v_add_f32_e32 v69, v70, v71
	v_fma_mix_f32 v69, v1, v54, v69 op_sel_hi:[0,1,0]
	s_waitcnt vmcnt(0)
	v_fma_mixlo_f16 v69, v69, v58, 0 op_sel_hi:[0,1,0]
	ds_write_b16 v68, v69 offset:4096
	global_load_dwordx4 v[50:53], v[212:213], off
	global_load_dwordx4 v[42:45], v[214:215], off
	global_load_dwordx4 v[46:49], v[216:217], off
	global_load_dwordx4 v[38:41], v[218:219], off
	global_load_dwordx4 v[30:33], v[220:221], off
	global_load_dwordx4 v[34:37], v[222:223], off
	global_load_dwordx4 v[26:29], v[224:225], off
	global_load_dwordx4 v[18:21], v[226:227], off
	global_load_dwordx4 v[22:25], v[228:229], off
	s_waitcnt lgkmcnt(0)
	s_load_dwordx16 s[36:51], s[54:55], 0x100
	s_load_dwordx16 s[72:87], s[54:55], 0x140
	v_cvt_f32_f16_sdwa v62, v62 dst_sel:DWORD dst_unused:UNUSED_PAD src0_sel:WORD_1
	v_cvt_f32_f16_sdwa v69, v54 dst_sel:DWORD dst_unused:UNUSED_PAD src0_sel:WORD_1
	v_pk_mul_f32 v[152:153], v[62:63], v[14:15] op_sel_hi:[0,1]
	v_exp_f32_e32 v152, v152
	v_exp_f32_e32 v153, v153
	v_pk_mul_f32 v[154:155], v[62:63], v[16:17] op_sel_hi:[0,1]
	v_exp_f32_e32 v154, v154
	v_exp_f32_e32 v155, v155
	v_mul_f32_e32 v150, v62, v69
	v_pk_mul_f32 v[134:135], v[152:153], v[134:135]
	v_pk_fma_f32 v[134:135], v[150:151], s[56:57], v[134:135] op_sel_hi:[0, 1, 1]
	v_pk_fma_f32 v[102:103], s[88:89], v[134:135], 0 op_sel_hi:[1, 1, 0]
	v_pk_mul_f32 v[118:119], v[154:155], v[136:137]
	s_nop 0
	v_pk_fma_f32 v[136:137], v[150:151], s[58:59], v[118:119] op_sel_hi:[0, 1, 1]
	v_pk_mul_f32 v[104:105], v[62:63], v[10:11] op_sel_hi:[0,1]
	v_exp_f32_e32 v104, v104
	v_exp_f32_e32 v105, v105
	v_pk_mul_f32 v[118:119], v[62:63], v[12:13] op_sel_hi:[0,1]
	v_exp_f32_e32 v118, v118
	v_exp_f32_e32 v119, v119
	v_pk_mul_f32 v[104:105], v[104:105], v[138:139]
	v_pk_fma_f32 v[102:103], s[90:91], v[136:137], v[102:103]
	v_pk_fma_f32 v[138:139], v[150:151], s[60:61], v[104:105] op_sel_hi:[0, 1, 1]
	v_pk_mul_f32 v[104:105], v[118:119], v[140:141]
	v_pk_mul_f32 v[106:107], v[62:63], v[8:9] op_sel_hi:[0,1]
	v_pk_fma_f32 v[140:141], v[150:151], s[62:63], v[104:105] op_sel_hi:[0, 1, 1]
	v_pk_mul_f32 v[104:105], v[62:63], v[6:7] op_sel_hi:[0,1]
	v_exp_f32_e32 v104, v104
	v_exp_f32_e32 v105, v105
	v_exp_f32_e32 v106, v106
	v_exp_f32_e32 v107, v107
	v_pk_fma_f32 v[102:103], s[92:93], v[138:139], v[102:103]
	v_pk_mul_f32 v[104:105], v[104:105], v[142:143]
	v_pk_fma_f32 v[102:103], s[94:95], v[140:141], v[102:103]
	v_pk_fma_f32 v[142:143], v[150:151], s[64:65], v[104:105] op_sel_hi:[0, 1, 1]
	v_pk_mul_f32 v[104:105], v[106:107], v[144:145]
	v_pk_mul_f32 v[106:107], v[62:63], v[4:5] op_sel_hi:[0,1]
	v_pk_fma_f32 v[144:145], v[150:151], s[66:67], v[104:105] op_sel_hi:[0, 1, 1]
	v_pk_mul_f32 v[104:105], v[62:63], v[2:3] op_sel_hi:[0,1]
	v_exp_f32_e32 v104, v104
	v_exp_f32_e32 v105, v105
	v_exp_f32_e32 v106, v106
	v_exp_f32_e32 v107, v107
	v_pk_fma_f32 v[102:103], s[96:97], v[142:143], v[102:103]
	v_pk_mul_f32 v[104:105], v[104:105], v[146:147]
	v_pk_fma_f32 v[102:103], s[98:99], v[144:145], v[102:103]
	v_pk_fma_f32 v[146:147], v[150:151], s[68:69], v[104:105] op_sel_hi:[0, 1, 1]
	v_pk_mul_f32 v[104:105], v[106:107], v[148:149]
	v_pk_fma_f32 v[102:103], s[20:21], v[146:147], v[102:103]
	v_pk_fma_f32 v[148:149], v[150:151], s[70:71], v[104:105] op_sel_hi:[0, 1, 1]
	v_pk_fma_f32 v[102:103], s[22:23], v[148:149], v[102:103]
	s_nop 0
	v_add_f32_e32 v62, v102, v103
	v_fma_mix_f32 v54, v1, v54, v62 op_sel:[0,1,0] op_sel_hi:[0,1,0]
	v_fma_mixlo_f16 v54, v54, v58, 0 op_sel:[0,1,0] op_sel_hi:[0,1,0]
	ds_write_b16 v68, v54 offset:5136
	s_waitcnt lgkmcnt(0)
	s_load_dwordx16 s[56:71], s[54:55], 0x180
	s_load_dwordx8 s[88:95], s[54:55], 0x1c0
	s_load_dwordx4 s[96:99], s[54:55], 0x1e0
	s_load_dwordx4 s[20:23], s[54:55], 0x1f0
	v_cvt_f32_f16_e32 v54, v63
	v_cvt_f32_f16_e32 v58, v55
	v_pk_mul_f32 v[150:151], v[54:55], v[14:15] op_sel_hi:[0,1]
	v_exp_f32_e32 v150, v150
	v_exp_f32_e32 v151, v151
	v_pk_mul_f32 v[152:153], v[54:55], v[16:17] op_sel_hi:[0,1]
	v_exp_f32_e32 v152, v152
	v_exp_f32_e32 v153, v153
	v_mul_f32_e32 v58, v54, v58
	v_pk_mul_f32 v[134:135], v[150:151], v[134:135]
	v_pk_fma_f32 v[134:135], v[58:59], s[36:37], v[134:135] op_sel_hi:[0, 1, 1]
	v_pk_fma_f32 v[70:71], s[72:73], v[134:135], 0 op_sel_hi:[1, 1, 0]
	v_pk_mul_f32 v[86:87], v[152:153], v[136:137]
	s_nop 0
	v_pk_fma_f32 v[136:137], v[58:59], s[38:39], v[86:87] op_sel_hi:[0, 1, 1]
	v_pk_mul_f32 v[72:73], v[54:55], v[10:11] op_sel_hi:[0,1]
	v_exp_f32_e32 v72, v72
	v_exp_f32_e32 v73, v73
	v_pk_mul_f32 v[86:87], v[54:55], v[12:13] op_sel_hi:[0,1]
	v_exp_f32_e32 v86, v86
	v_exp_f32_e32 v87, v87
	v_pk_mul_f32 v[72:73], v[72:73], v[138:139]
	v_pk_fma_f32 v[70:71], s[74:75], v[136:137], v[70:71]
	v_pk_fma_f32 v[138:139], v[58:59], s[40:41], v[72:73] op_sel_hi:[0, 1, 1]
	v_pk_mul_f32 v[72:73], v[86:87], v[140:141]
	v_pk_mul_f32 v[74:75], v[54:55], v[8:9] op_sel_hi:[0,1]
	v_pk_fma_f32 v[140:141], v[58:59], s[42:43], v[72:73] op_sel_hi:[0, 1, 1]
	v_pk_mul_f32 v[72:73], v[54:55], v[6:7] op_sel_hi:[0,1]
	v_exp_f32_e32 v72, v72
	v_exp_f32_e32 v73, v73
	v_exp_f32_e32 v74, v74
	v_exp_f32_e32 v75, v75
	v_pk_fma_f32 v[70:71], s[76:77], v[138:139], v[70:71]
	v_pk_mul_f32 v[72:73], v[72:73], v[142:143]
	v_pk_fma_f32 v[70:71], s[78:79], v[140:141], v[70:71]
	v_pk_fma_f32 v[142:143], v[58:59], s[44:45], v[72:73] op_sel_hi:[0, 1, 1]
	v_pk_mul_f32 v[72:73], v[74:75], v[144:145]
	v_pk_mul_f32 v[74:75], v[54:55], v[4:5] op_sel_hi:[0,1]
	v_pk_fma_f32 v[144:145], v[58:59], s[46:47], v[72:73] op_sel_hi:[0, 1, 1]
	v_pk_mul_f32 v[72:73], v[54:55], v[2:3] op_sel_hi:[0,1]
	v_exp_f32_e32 v72, v72
	v_exp_f32_e32 v73, v73
	v_exp_f32_e32 v74, v74
	v_exp_f32_e32 v75, v75
	v_pk_fma_f32 v[70:71], s[80:81], v[142:143], v[70:71]
	v_pk_mul_f32 v[72:73], v[72:73], v[146:147]
	v_pk_fma_f32 v[70:71], s[82:83], v[144:145], v[70:71]
	v_pk_fma_f32 v[146:147], v[58:59], s[48:49], v[72:73] op_sel_hi:[0, 1, 1]
	v_pk_mul_f32 v[72:73], v[74:75], v[148:149]
	v_pk_fma_f32 v[70:71], s[84:85], v[146:147], v[70:71]
	v_pk_fma_f32 v[148:149], v[58:59], s[50:51], v[72:73] op_sel_hi:[0, 1, 1]
	v_pk_fma_f32 v[70:71], s[86:87], v[148:149], v[70:71]
	s_nop 0
	v_add_f32_e32 v54, v70, v71
	v_fma_mix_f32 v54, v1, v55, v54 op_sel_hi:[0,1,0]
	v_fma_mixlo_f16 v54, v54, v59, 0 op_sel_hi:[0,1,0]
	ds_write_b16 v68, v54 offset:6176
	s_waitcnt lgkmcnt(0)
	s_load_dwordx16 s[36:51], s[54:55], 0x200
	s_load_dwordx16 s[72:87], s[54:55], 0x240
	v_cvt_f32_f16_sdwa v54, v63 dst_sel:DWORD dst_unused:UNUSED_PAD src0_sel:WORD_1
	v_cvt_f32_f16_sdwa v58, v55 dst_sel:DWORD dst_unused:UNUSED_PAD src0_sel:WORD_1
	v_pk_mul_f32 v[62:63], v[54:55], v[14:15] op_sel_hi:[0,1]
	v_exp_f32_e32 v62, v62
	v_exp_f32_e32 v63, v63
	v_pk_mul_f32 v[150:151], v[54:55], v[16:17] op_sel_hi:[0,1]
	v_exp_f32_e32 v150, v150
	v_exp_f32_e32 v151, v151
	v_mul_f32_e32 v58, v54, v58
	v_pk_mul_f32 v[62:63], v[62:63], v[134:135]
	v_pk_fma_f32 v[62:63], v[58:59], s[56:57], v[62:63] op_sel_hi:[0, 1, 1]
	v_pk_fma_f32 v[102:103], s[88:89], v[62:63], 0 op_sel_hi:[1, 1, 0]
	v_pk_mul_f32 v[118:119], v[150:151], v[136:137]
	s_nop 0
	v_pk_fma_f32 v[134:135], v[58:59], s[58:59], v[118:119] op_sel_hi:[0, 1, 1]
	v_pk_mul_f32 v[104:105], v[54:55], v[10:11] op_sel_hi:[0,1]
	v_exp_f32_e32 v104, v104
	v_exp_f32_e32 v105, v105
	v_pk_mul_f32 v[118:119], v[54:55], v[12:13] op_sel_hi:[0,1]
	v_exp_f32_e32 v118, v118
	v_exp_f32_e32 v119, v119
	v_pk_mul_f32 v[104:105], v[104:105], v[138:139]
	v_pk_fma_f32 v[102:103], s[90:91], v[134:135], v[102:103]
	v_pk_fma_f32 v[136:137], v[58:59], s[60:61], v[104:105] op_sel_hi:[0, 1, 1]
	v_pk_mul_f32 v[104:105], v[118:119], v[140:141]
	v_pk_mul_f32 v[106:107], v[54:55], v[8:9] op_sel_hi:[0,1]
	v_pk_fma_f32 v[138:139], v[58:59], s[62:63], v[104:105] op_sel_hi:[0, 1, 1]
	v_pk_mul_f32 v[104:105], v[54:55], v[6:7] op_sel_hi:[0,1]
	v_exp_f32_e32 v104, v104
	v_exp_f32_e32 v105, v105
	v_exp_f32_e32 v106, v106
	v_exp_f32_e32 v107, v107
	v_pk_fma_f32 v[102:103], s[92:93], v[136:137], v[102:103]
	v_pk_mul_f32 v[104:105], v[104:105], v[142:143]
	v_pk_fma_f32 v[102:103], s[94:95], v[138:139], v[102:103]
	v_pk_fma_f32 v[140:141], v[58:59], s[64:65], v[104:105] op_sel_hi:[0, 1, 1]
	v_pk_mul_f32 v[104:105], v[106:107], v[144:145]
	v_pk_mul_f32 v[106:107], v[54:55], v[4:5] op_sel_hi:[0,1]
	v_pk_fma_f32 v[142:143], v[58:59], s[66:67], v[104:105] op_sel_hi:[0, 1, 1]
	v_pk_mul_f32 v[104:105], v[54:55], v[2:3] op_sel_hi:[0,1]
	v_exp_f32_e32 v104, v104
	v_exp_f32_e32 v105, v105
	v_exp_f32_e32 v106, v106
	v_exp_f32_e32 v107, v107
	v_pk_fma_f32 v[102:103], s[96:97], v[140:141], v[102:103]
	v_pk_mul_f32 v[104:105], v[104:105], v[146:147]
	v_pk_fma_f32 v[102:103], s[98:99], v[142:143], v[102:103]
	v_pk_fma_f32 v[144:145], v[58:59], s[68:69], v[104:105] op_sel_hi:[0, 1, 1]
	v_pk_mul_f32 v[104:105], v[106:107], v[148:149]
	v_pk_fma_f32 v[102:103], s[20:21], v[144:145], v[102:103]
	v_pk_fma_f32 v[146:147], v[58:59], s[70:71], v[104:105] op_sel_hi:[0, 1, 1]
	v_pk_fma_f32 v[102:103], s[22:23], v[146:147], v[102:103]
	s_nop 0
	v_add_f32_e32 v54, v102, v103
	v_fma_mix_f32 v54, v1, v55, v54 op_sel:[0,1,0] op_sel_hi:[0,1,0]
	v_fma_mixlo_f16 v54, v54, v59, 0 op_sel:[0,1,0] op_sel_hi:[0,1,0]
	ds_write_b16 v68, v54 offset:7216
	s_waitcnt lgkmcnt(0)
	s_load_dwordx16 s[56:71], s[54:55], 0x280
	s_load_dwordx8 s[88:95], s[54:55], 0x2c0
	s_load_dwordx4 s[96:99], s[54:55], 0x2e0
	s_load_dwordx4 s[20:23], s[54:55], 0x2f0
	v_cvt_f32_f16_e32 v54, v64
	v_cvt_f32_f16_e32 v55, v56
	v_pk_mul_f32 v[148:149], v[54:55], v[14:15] op_sel_hi:[0,1]
	v_exp_f32_e32 v148, v148
	v_exp_f32_e32 v149, v149
	v_pk_mul_f32 v[150:151], v[54:55], v[16:17] op_sel_hi:[0,1]
	v_exp_f32_e32 v150, v150
	v_exp_f32_e32 v151, v151
	v_mul_f32_e32 v58, v54, v55
	v_pk_mul_f32 v[62:63], v[148:149], v[62:63]
	v_pk_fma_f32 v[62:63], v[58:59], s[36:37], v[62:63] op_sel_hi:[0, 1, 1]
	v_pk_fma_f32 v[70:71], s[72:73], v[62:63], 0 op_sel_hi:[1, 1, 0]
	v_pk_mul_f32 v[86:87], v[150:151], v[134:135]
	s_nop 0
	v_pk_fma_f32 v[134:135], v[58:59], s[38:39], v[86:87] op_sel_hi:[0, 1, 1]
	v_pk_mul_f32 v[72:73], v[54:55], v[10:11] op_sel_hi:[0,1]
	v_exp_f32_e32 v72, v72
	v_exp_f32_e32 v73, v73
	v_pk_mul_f32 v[86:87], v[54:55], v[12:13] op_sel_hi:[0,1]
	v_exp_f32_e32 v86, v86
	v_exp_f32_e32 v87, v87
	v_pk_mul_f32 v[72:73], v[72:73], v[136:137]
	v_pk_fma_f32 v[70:71], s[74:75], v[134:135], v[70:71]
	v_pk_fma_f32 v[136:137], v[58:59], s[40:41], v[72:73] op_sel_hi:[0, 1, 1]
	v_pk_mul_f32 v[72:73], v[86:87], v[138:139]
	v_pk_mul_f32 v[74:75], v[54:55], v[8:9] op_sel_hi:[0,1]
	v_pk_fma_f32 v[138:139], v[58:59], s[42:43], v[72:73] op_sel_hi:[0, 1, 1]
	v_pk_mul_f32 v[72:73], v[54:55], v[6:7] op_sel_hi:[0,1]
	v_exp_f32_e32 v72, v72
	v_exp_f32_e32 v73, v73
	v_exp_f32_e32 v74, v74
	v_exp_f32_e32 v75, v75
	v_pk_fma_f32 v[70:71], s[76:77], v[136:137], v[70:71]
	v_pk_mul_f32 v[72:73], v[72:73], v[140:141]
	v_pk_fma_f32 v[70:71], s[78:79], v[138:139], v[70:71]
	v_pk_fma_f32 v[140:141], v[58:59], s[44:45], v[72:73] op_sel_hi:[0, 1, 1]
	v_pk_mul_f32 v[72:73], v[74:75], v[142:143]
	v_pk_fma_f32 v[70:71], s[80:81], v[140:141], v[70:71]
	v_pk_fma_f32 v[142:143], v[58:59], s[46:47], v[72:73] op_sel_hi:[0, 1, 1]
	v_pk_mul_f32 v[72:73], v[54:55], v[2:3] op_sel_hi:[0,1]
	v_exp_f32_e32 v72, v72
	v_exp_f32_e32 v73, v73
	v_pk_mul_f32 v[54:55], v[54:55], v[4:5] op_sel_hi:[0,1]
	v_exp_f32_e32 v54, v54
	v_exp_f32_e32 v55, v55
	v_pk_mul_f32 v[72:73], v[72:73], v[144:145]
	v_pk_fma_f32 v[70:71], s[82:83], v[142:143], v[70:71]
	v_pk_fma_f32 v[144:145], v[58:59], s[48:49], v[72:73] op_sel_hi:[0, 1, 1]
	v_pk_mul_f32 v[54:55], v[54:55], v[146:147]
	v_pk_fma_f32 v[70:71], s[84:85], v[144:145], v[70:71]
	v_pk_fma_f32 v[54:55], v[58:59], s[50:51], v[54:55] op_sel_hi:[0, 1, 1]
	v_pk_fma_f32 v[58:59], s[86:87], v[54:55], v[70:71]
	s_nop 0
	v_add_f32_e32 v58, v58, v59
	v_fma_mix_f32 v58, v1, v56, v58 op_sel_hi:[0,1,0]
	v_fma_mixlo_f16 v58, v58, v60, 0 op_sel_hi:[0,1,0]
	ds_write_b16 v68, v58 offset:8256
	s_waitcnt lgkmcnt(0)
	s_load_dwordx16 s[36:51], s[54:55], 0x300
	s_load_dwordx16 s[72:87], s[54:55], 0x340
	v_cvt_f32_f16_sdwa v58, v64 dst_sel:DWORD dst_unused:UNUSED_PAD src0_sel:WORD_1
	v_cvt_f32_f16_sdwa v59, v56 dst_sel:DWORD dst_unused:UNUSED_PAD src0_sel:WORD_1
	v_pk_mul_f32 v[146:147], v[58:59], v[14:15] op_sel_hi:[0,1]
	v_exp_f32_e32 v146, v146
	v_exp_f32_e32 v147, v147
	v_pk_mul_f32 v[148:149], v[58:59], v[16:17] op_sel_hi:[0,1]
	v_exp_f32_e32 v148, v148
	v_exp_f32_e32 v149, v149
	v_mul_f32_e32 v64, v58, v59
	v_pk_mul_f32 v[62:63], v[146:147], v[62:63]
	v_pk_fma_f32 v[62:63], v[64:65], s[56:57], v[62:63] op_sel_hi:[0, 1, 1]
	v_pk_fma_f32 v[102:103], s[88:89], v[62:63], 0 op_sel_hi:[1, 1, 0]
	v_pk_mul_f32 v[118:119], v[148:149], v[134:135]
	s_nop 0
	v_pk_fma_f32 v[134:135], v[64:65], s[58:59], v[118:119] op_sel_hi:[0, 1, 1]
	v_pk_mul_f32 v[104:105], v[58:59], v[10:11] op_sel_hi:[0,1]
	v_exp_f32_e32 v104, v104
	v_exp_f32_e32 v105, v105
	v_pk_mul_f32 v[118:119], v[58:59], v[12:13] op_sel_hi:[0,1]
	v_exp_f32_e32 v118, v118
	v_exp_f32_e32 v119, v119
	v_pk_mul_f32 v[104:105], v[104:105], v[136:137]
	v_pk_fma_f32 v[102:103], s[90:91], v[134:135], v[102:103]
	v_pk_fma_f32 v[136:137], v[64:65], s[60:61], v[104:105] op_sel_hi:[0, 1, 1]
	v_pk_mul_f32 v[104:105], v[118:119], v[138:139]
	v_pk_mul_f32 v[106:107], v[58:59], v[8:9] op_sel_hi:[0,1]
	v_pk_fma_f32 v[138:139], v[64:65], s[62:63], v[104:105] op_sel_hi:[0, 1, 1]
	v_pk_mul_f32 v[104:105], v[58:59], v[6:7] op_sel_hi:[0,1]
	v_exp_f32_e32 v104, v104
	v_exp_f32_e32 v105, v105
	v_exp_f32_e32 v106, v106
	v_exp_f32_e32 v107, v107
	v_pk_fma_f32 v[102:103], s[92:93], v[136:137], v[102:103]
	v_pk_mul_f32 v[104:105], v[104:105], v[140:141]
	v_pk_fma_f32 v[102:103], s[94:95], v[138:139], v[102:103]
	v_pk_fma_f32 v[140:141], v[64:65], s[64:65], v[104:105] op_sel_hi:[0, 1, 1]
	v_pk_mul_f32 v[104:105], v[106:107], v[142:143]
	v_pk_fma_f32 v[102:103], s[96:97], v[140:141], v[102:103]
	v_pk_fma_f32 v[142:143], v[64:65], s[66:67], v[104:105] op_sel_hi:[0, 1, 1]
	v_pk_mul_f32 v[104:105], v[58:59], v[2:3] op_sel_hi:[0,1]
	v_exp_f32_e32 v104, v104
	v_exp_f32_e32 v105, v105
	v_pk_mul_f32 v[58:59], v[58:59], v[4:5] op_sel_hi:[0,1]
	v_exp_f32_e32 v58, v58
	v_exp_f32_e32 v59, v59
	v_pk_mul_f32 v[104:105], v[104:105], v[144:145]
	v_pk_fma_f32 v[102:103], s[98:99], v[142:143], v[102:103]
	v_pk_fma_f32 v[144:145], v[64:65], s[68:69], v[104:105] op_sel_hi:[0, 1, 1]
	v_pk_mul_f32 v[54:55], v[58:59], v[54:55]
	v_pk_fma_f32 v[102:103], s[20:21], v[144:145], v[102:103]
	v_pk_fma_f32 v[54:55], v[64:65], s[70:71], v[54:55] op_sel_hi:[0, 1, 1]
	v_pk_fma_f32 v[58:59], s[22:23], v[54:55], v[102:103]
	s_nop 0
	v_add_f32_e32 v58, v58, v59
	v_fma_mix_f32 v56, v1, v56, v58 op_sel:[0,1,0] op_sel_hi:[0,1,0]
	v_fma_mixlo_f16 v56, v56, v60, 0 op_sel:[0,1,0] op_sel_hi:[0,1,0]
	ds_write_b16 v68, v56 offset:9296
	s_waitcnt lgkmcnt(0)
	s_load_dwordx16 s[56:71], s[54:55], 0x380
	s_load_dwordx8 s[88:95], s[54:55], 0x3c0
	s_load_dwordx4 s[96:99], s[54:55], 0x3e0
	s_load_dwordx4 s[20:23], s[54:55], 0x3f0
	v_cvt_f32_f16_e32 v56, v65
	v_cvt_f32_f16_e32 v58, v57
	v_pk_mul_f32 v[146:147], v[56:57], v[14:15] op_sel_hi:[0,1]
	v_exp_f32_e32 v146, v146
	v_exp_f32_e32 v147, v147
	v_pk_mul_f32 v[148:149], v[56:57], v[16:17] op_sel_hi:[0,1]
	v_exp_f32_e32 v148, v148
	v_exp_f32_e32 v149, v149
	v_mul_f32_e32 v58, v56, v58
	v_pk_mul_f32 v[62:63], v[146:147], v[62:63]
	v_pk_fma_f32 v[62:63], v[58:59], s[36:37], v[62:63] op_sel_hi:[0, 1, 1]
	v_pk_fma_f32 v[70:71], s[72:73], v[62:63], 0 op_sel_hi:[1, 1, 0]
	v_pk_mul_f32 v[86:87], v[148:149], v[134:135]
	s_nop 0
	v_pk_fma_f32 v[134:135], v[58:59], s[38:39], v[86:87] op_sel_hi:[0, 1, 1]
	v_pk_mul_f32 v[72:73], v[56:57], v[10:11] op_sel_hi:[0,1]
	v_exp_f32_e32 v72, v72
	v_exp_f32_e32 v73, v73
	v_pk_mul_f32 v[86:87], v[56:57], v[12:13] op_sel_hi:[0,1]
	v_exp_f32_e32 v86, v86
	v_exp_f32_e32 v87, v87
	v_pk_mul_f32 v[72:73], v[72:73], v[136:137]
	v_pk_fma_f32 v[70:71], s[74:75], v[134:135], v[70:71]
	v_pk_fma_f32 v[136:137], v[58:59], s[40:41], v[72:73] op_sel_hi:[0, 1, 1]
	v_pk_mul_f32 v[72:73], v[86:87], v[138:139]
	v_pk_mul_f32 v[74:75], v[56:57], v[8:9] op_sel_hi:[0,1]
	v_pk_fma_f32 v[138:139], v[58:59], s[42:43], v[72:73] op_sel_hi:[0, 1, 1]
	v_pk_mul_f32 v[72:73], v[56:57], v[6:7] op_sel_hi:[0,1]
	v_exp_f32_e32 v72, v72
	v_exp_f32_e32 v73, v73
	v_exp_f32_e32 v74, v74
	v_exp_f32_e32 v75, v75
	v_pk_fma_f32 v[70:71], s[76:77], v[136:137], v[70:71]
	v_pk_mul_f32 v[72:73], v[72:73], v[140:141]
	v_pk_fma_f32 v[70:71], s[78:79], v[138:139], v[70:71]
	v_pk_fma_f32 v[140:141], v[58:59], s[44:45], v[72:73] op_sel_hi:[0, 1, 1]
	v_pk_mul_f32 v[72:73], v[74:75], v[142:143]
	v_pk_mul_f32 v[74:75], v[56:57], v[4:5] op_sel_hi:[0,1]
	v_pk_fma_f32 v[142:143], v[58:59], s[46:47], v[72:73] op_sel_hi:[0, 1, 1]
	v_pk_mul_f32 v[72:73], v[56:57], v[2:3] op_sel_hi:[0,1]
	v_exp_f32_e32 v72, v72
	v_exp_f32_e32 v73, v73
	v_exp_f32_e32 v74, v74
	v_exp_f32_e32 v75, v75
	v_pk_fma_f32 v[70:71], s[80:81], v[140:141], v[70:71]
	v_pk_mul_f32 v[72:73], v[72:73], v[144:145]
	v_pk_fma_f32 v[70:71], s[82:83], v[142:143], v[70:71]
	v_pk_fma_f32 v[144:145], v[58:59], s[48:49], v[72:73] op_sel_hi:[0, 1, 1]
	v_pk_mul_f32 v[54:55], v[74:75], v[54:55]
	v_pk_fma_f32 v[70:71], s[84:85], v[144:145], v[70:71]
	v_pk_fma_f32 v[54:55], v[58:59], s[50:51], v[54:55] op_sel_hi:[0, 1, 1]
	v_pk_fma_f32 v[58:59], s[86:87], v[54:55], v[70:71]
	s_nop 0
	v_add_f32_e32 v56, v58, v59
	v_fma_mix_f32 v56, v1, v57, v56 op_sel_hi:[0,1,0]
	v_fma_mixlo_f16 v56, v56, v61, 0 op_sel_hi:[0,1,0]
	ds_write_b16 v68, v56 offset:10336
	s_waitcnt lgkmcnt(0)
	s_load_dwordx16 s[36:51], s[54:55], 0x400
	s_load_dwordx16 s[72:87], s[54:55], 0x440
	v_cvt_f32_f16_sdwa v56, v65 dst_sel:DWORD dst_unused:UNUSED_PAD src0_sel:WORD_1
	v_cvt_f32_f16_sdwa v58, v57 dst_sel:DWORD dst_unused:UNUSED_PAD src0_sel:WORD_1
	v_pk_mul_f32 v[64:65], v[56:57], v[14:15] op_sel_hi:[0,1]
	v_pk_mul_f32 v[146:147], v[56:57], v[16:17] op_sel_hi:[0,1]
	v_exp_f32_e32 v64, v64
	v_exp_f32_e32 v65, v65
	v_exp_f32_e32 v146, v146
	v_exp_f32_e32 v147, v147
	v_mul_f32_e32 v58, v56, v58
	v_pk_mul_f32 v[62:63], v[64:65], v[62:63]
	v_pk_mul_f32 v[64:65], v[146:147], v[134:135]
	v_pk_fma_f32 v[134:135], v[58:59], s[58:59], v[64:65] op_sel_hi:[0, 1, 1]
	v_pk_mul_f32 v[64:65], v[56:57], v[10:11] op_sel_hi:[0,1]
	v_pk_fma_f32 v[148:149], v[58:59], s[56:57], v[62:63] op_sel_hi:[0, 1, 1]
	v_exp_f32_e32 v64, v64
	v_exp_f32_e32 v65, v65
	v_pk_mul_f32 v[102:103], v[56:57], v[12:13] op_sel_hi:[0,1]
	v_exp_f32_e32 v102, v102
	v_exp_f32_e32 v103, v103
	v_pk_fma_f32 v[62:63], s[88:89], v[148:149], 0 op_sel_hi:[1, 1, 0]
	v_pk_mul_f32 v[64:65], v[64:65], v[136:137]
	v_pk_fma_f32 v[62:63], s[90:91], v[134:135], v[62:63]
	v_pk_fma_f32 v[136:137], v[58:59], s[60:61], v[64:65] op_sel_hi:[0, 1, 1]
	v_pk_mul_f32 v[64:65], v[102:103], v[138:139]
	v_pk_fma_f32 v[62:63], s[92:93], v[136:137], v[62:63]
	v_pk_fma_f32 v[122:123], v[58:59], s[62:63], v[64:65] op_sel_hi:[0, 1, 1]
	v_pk_mul_f32 v[64:65], v[56:57], v[6:7] op_sel_hi:[0,1]
	v_exp_f32_e32 v64, v64
	v_exp_f32_e32 v65, v65
	v_pk_mul_f32 v[102:103], v[56:57], v[8:9] op_sel_hi:[0,1]
	v_exp_f32_e32 v102, v102
	v_exp_f32_e32 v103, v103
	v_pk_mul_f32 v[64:65], v[64:65], v[140:141]
	v_pk_fma_f32 v[62:63], s[94:95], v[122:123], v[62:63]
	v_pk_fma_f32 v[124:125], v[58:59], s[64:65], v[64:65] op_sel_hi:[0, 1, 1]
	v_pk_mul_f32 v[64:65], v[102:103], v[142:143]
	v_pk_fma_f32 v[62:63], s[96:97], v[124:125], v[62:63]
	v_pk_fma_f32 v[126:127], v[58:59], s[66:67], v[64:65] op_sel_hi:[0, 1, 1]
	v_pk_mul_f32 v[64:65], v[56:57], v[2:3] op_sel_hi:[0,1]
	v_exp_f32_e32 v64, v64
	v_exp_f32_e32 v65, v65
	v_pk_mul_f32 v[102:103], v[56:57], v[4:5] op_sel_hi:[0,1]
	v_exp_f32_e32 v102, v102
	v_exp_f32_e32 v103, v103
	v_pk_mul_f32 v[64:65], v[64:65], v[144:145]
	v_pk_fma_f32 v[62:63], s[98:99], v[126:127], v[62:63]
	v_pk_fma_f32 v[128:129], v[58:59], s[68:69], v[64:65] op_sel_hi:[0, 1, 1]
	v_pk_mul_f32 v[54:55], v[102:103], v[54:55]
	v_pk_fma_f32 v[62:63], s[20:21], v[128:129], v[62:63]
	v_pk_fma_f32 v[130:131], v[58:59], s[70:71], v[54:55] op_sel_hi:[0, 1, 1]
	v_pk_fma_f32 v[54:55], s[22:23], v[130:131], v[62:63]
	s_nop 0
	v_add_f32_e32 v54, v54, v55
	v_fma_mix_f32 v54, v1, v57, v54 op_sel:[0,1,0] op_sel_hi:[0,1,0]
	v_fma_mixlo_f16 v54, v54, v61, 0 op_sel:[0,1,0] op_sel_hi:[0,1,0]
	ds_write_b16 v68, v54 offset:11376
	s_waitcnt lgkmcnt(0)
	s_load_dwordx16 s[56:71], s[54:55], 0x480
	s_load_dwordx8 s[88:95], s[54:55], 0x4c0
	s_load_dwordx4 s[96:99], s[54:55], 0x4e0
	s_load_dwordx4 s[20:23], s[54:55], 0x4f0
	s_waitcnt vmcnt(8)
	v_cvt_f32_f16_e32 v132, v50
	s_waitcnt vmcnt(7)
	v_cvt_f32_f16_e32 v69, v42
	v_pk_mul_f32 v[140:141], v[132:133], v[14:15] op_sel_hi:[0,1]
	v_exp_f32_e32 v140, v140
	v_exp_f32_e32 v141, v141
	v_pk_mul_f32 v[142:143], v[132:133], v[16:17] op_sel_hi:[0,1]
	v_exp_f32_e32 v142, v142
	v_exp_f32_e32 v143, v143
	v_mul_f32_e32 v138, v132, v69
	v_pk_mul_f32 v[140:141], v[140:141], v[148:149]
	v_pk_fma_f32 v[140:141], v[138:139], s[36:37], v[140:141] op_sel_hi:[0, 1, 1]
	v_pk_fma_f32 v[70:71], s[72:73], v[140:141], 0 op_sel_hi:[1, 1, 0]
	v_pk_mul_f32 v[86:87], v[142:143], v[134:135]
	s_nop 0
	v_pk_fma_f32 v[134:135], v[138:139], s[38:39], v[86:87] op_sel_hi:[0, 1, 1]
	v_pk_mul_f32 v[72:73], v[132:133], v[10:11] op_sel_hi:[0,1]
	v_exp_f32_e32 v72, v72
	v_exp_f32_e32 v73, v73
	v_pk_mul_f32 v[86:87], v[132:133], v[12:13] op_sel_hi:[0,1]
	v_exp_f32_e32 v86, v86
	v_exp_f32_e32 v87, v87
	v_pk_mul_f32 v[72:73], v[72:73], v[136:137]
	v_pk_fma_f32 v[70:71], s[74:75], v[134:135], v[70:71]
	v_pk_fma_f32 v[136:137], v[138:139], s[40:41], v[72:73] op_sel_hi:[0, 1, 1]
	v_pk_mul_f32 v[72:73], v[86:87], v[122:123]
	v_pk_mul_f32 v[74:75], v[132:133], v[8:9] op_sel_hi:[0,1]
	v_pk_fma_f32 v[122:123], v[138:139], s[42:43], v[72:73] op_sel_hi:[0, 1, 1]
	v_pk_mul_f32 v[72:73], v[132:133], v[6:7] op_sel_hi:[0,1]
	v_exp_f32_e32 v72, v72
	v_exp_f32_e32 v73, v73
	v_exp_f32_e32 v74, v74
	v_exp_f32_e32 v75, v75
	v_pk_fma_f32 v[70:71], s[76:77], v[136:137], v[70:71]
	v_pk_mul_f32 v[72:73], v[72:73], v[124:125]
	v_pk_fma_f32 v[70:71], s[78:79], v[122:123], v[70:71]
	v_pk_fma_f32 v[124:125], v[138:139], s[44:45], v[72:73] op_sel_hi:[0, 1, 1]
	v_pk_mul_f32 v[72:73], v[74:75], v[126:127]
	v_pk_mul_f32 v[74:75], v[132:133], v[4:5] op_sel_hi:[0,1]
	v_pk_fma_f32 v[126:127], v[138:139], s[46:47], v[72:73] op_sel_hi:[0, 1, 1]
	v_pk_mul_f32 v[72:73], v[132:133], v[2:3] op_sel_hi:[0,1]
	v_exp_f32_e32 v72, v72
	v_exp_f32_e32 v73, v73
	v_exp_f32_e32 v74, v74
	v_exp_f32_e32 v75, v75
	v_pk_fma_f32 v[70:71], s[80:81], v[124:125], v[70:71]
	v_pk_mul_f32 v[72:73], v[72:73], v[128:129]
	v_pk_fma_f32 v[70:71], s[82:83], v[126:127], v[70:71]
	v_pk_fma_f32 v[128:129], v[138:139], s[48:49], v[72:73] op_sel_hi:[0, 1, 1]
	v_pk_mul_f32 v[72:73], v[74:75], v[130:131]
	v_pk_fma_f32 v[70:71], s[84:85], v[128:129], v[70:71]
	v_pk_fma_f32 v[130:131], v[138:139], s[50:51], v[72:73] op_sel_hi:[0, 1, 1]
	v_pk_fma_f32 v[70:71], s[86:87], v[130:131], v[70:71]
	s_nop 0
	v_add_f32_e32 v69, v70, v71
	v_fma_mix_f32 v69, v1, v42, v69 op_sel_hi:[0,1,0]
	s_waitcnt vmcnt(6)
	v_fma_mixlo_f16 v69, v69, v46, 0 op_sel_hi:[0,1,0]
	ds_write_b16 v68, v69 offset:12416
	s_waitcnt lgkmcnt(0)
	s_load_dwordx16 s[36:51], s[54:55], 0x500
	s_load_dwordx16 s[72:87], s[54:55], 0x540
	v_cvt_f32_f16_sdwa v50, v50 dst_sel:DWORD dst_unused:UNUSED_PAD src0_sel:WORD_1
	v_cvt_f32_f16_sdwa v69, v42 dst_sel:DWORD dst_unused:UNUSED_PAD src0_sel:WORD_1
	v_pk_mul_f32 v[138:139], v[50:51], v[14:15] op_sel_hi:[0,1]
	v_exp_f32_e32 v138, v138
	v_exp_f32_e32 v139, v139
	v_pk_mul_f32 v[142:143], v[50:51], v[16:17] op_sel_hi:[0,1]
	v_exp_f32_e32 v142, v142
	v_exp_f32_e32 v143, v143
	v_mul_f32_e32 v132, v50, v69
	v_pk_mul_f32 v[138:139], v[138:139], v[140:141]
	v_pk_fma_f32 v[138:139], v[132:133], s[56:57], v[138:139] op_sel_hi:[0, 1, 1]
	v_pk_fma_f32 v[54:55], s[88:89], v[138:139], 0 op_sel_hi:[1, 1, 0]
	v_pk_mul_f32 v[106:107], v[142:143], v[134:135]
	s_nop 0
	v_pk_fma_f32 v[134:135], v[132:133], s[58:59], v[106:107] op_sel_hi:[0, 1, 1]
	v_pk_mul_f32 v[56:57], v[50:51], v[10:11] op_sel_hi:[0,1]
	v_exp_f32_e32 v56, v56
	v_exp_f32_e32 v57, v57
	v_pk_mul_f32 v[106:107], v[50:51], v[12:13] op_sel_hi:[0,1]
	v_exp_f32_e32 v106, v106
	v_exp_f32_e32 v107, v107
	v_pk_mul_f32 v[56:57], v[56:57], v[136:137]
	v_pk_fma_f32 v[54:55], s[90:91], v[134:135], v[54:55]
	v_pk_fma_f32 v[136:137], v[132:133], s[60:61], v[56:57] op_sel_hi:[0, 1, 1]
	v_pk_mul_f32 v[56:57], v[106:107], v[122:123]
	v_pk_mul_f32 v[58:59], v[50:51], v[8:9] op_sel_hi:[0,1]
	v_pk_fma_f32 v[122:123], v[132:133], s[62:63], v[56:57] op_sel_hi:[0, 1, 1]
	v_pk_mul_f32 v[56:57], v[50:51], v[6:7] op_sel_hi:[0,1]
	v_exp_f32_e32 v56, v56
	v_exp_f32_e32 v57, v57
	v_exp_f32_e32 v58, v58
	v_exp_f32_e32 v59, v59
	v_pk_fma_f32 v[54:55], s[92:93], v[136:137], v[54:55]
	v_pk_mul_f32 v[56:57], v[56:57], v[124:125]
	v_pk_fma_f32 v[54:55], s[94:95], v[122:123], v[54:55]
	v_pk_fma_f32 v[124:125], v[132:133], s[64:65], v[56:57] op_sel_hi:[0, 1, 1]
	v_pk_mul_f32 v[56:57], v[58:59], v[126:127]
	v_pk_mul_f32 v[58:59], v[50:51], v[4:5] op_sel_hi:[0,1]
	v_pk_fma_f32 v[126:127], v[132:133], s[66:67], v[56:57] op_sel_hi:[0, 1, 1]
	v_pk_mul_f32 v[56:57], v[50:51], v[2:3] op_sel_hi:[0,1]
	v_exp_f32_e32 v56, v56
	v_exp_f32_e32 v57, v57
	v_exp_f32_e32 v58, v58
	v_exp_f32_e32 v59, v59
	v_pk_fma_f32 v[54:55], s[96:97], v[124:125], v[54:55]
	v_pk_mul_f32 v[56:57], v[56:57], v[128:129]
	v_pk_fma_f32 v[54:55], s[98:99], v[126:127], v[54:55]
	v_pk_fma_f32 v[128:129], v[132:133], s[68:69], v[56:57] op_sel_hi:[0, 1, 1]
	v_pk_mul_f32 v[56:57], v[58:59], v[130:131]
	v_pk_fma_f32 v[54:55], s[20:21], v[128:129], v[54:55]
	v_pk_fma_f32 v[130:131], v[132:133], s[70:71], v[56:57] op_sel_hi:[0, 1, 1]
	v_pk_fma_f32 v[54:55], s[22:23], v[130:131], v[54:55]
	s_nop 0
	v_add_f32_e32 v50, v54, v55
	v_fma_mix_f32 v42, v1, v42, v50 op_sel:[0,1,0] op_sel_hi:[0,1,0]
	v_fma_mixlo_f16 v42, v42, v46, 0 op_sel:[0,1,0] op_sel_hi:[0,1,0]
	ds_write_b16 v68, v42 offset:13456
	s_waitcnt lgkmcnt(0)
	s_load_dwordx16 s[56:71], s[54:55], 0x580
	s_load_dwordx8 s[88:95], s[54:55], 0x5c0
	s_load_dwordx4 s[96:99], s[54:55], 0x5e0
	s_load_dwordx4 s[20:23], s[54:55], 0x5f0
	v_cvt_f32_f16_e32 v42, v51
	v_cvt_f32_f16_e32 v46, v43
	v_pk_mul_f32 v[132:133], v[42:43], v[14:15] op_sel_hi:[0,1]
	v_exp_f32_e32 v132, v132
	v_exp_f32_e32 v133, v133
	v_pk_mul_f32 v[140:141], v[42:43], v[16:17] op_sel_hi:[0,1]
	v_exp_f32_e32 v140, v140
	v_exp_f32_e32 v141, v141
	v_mul_f32_e32 v46, v42, v46
	v_pk_mul_f32 v[132:133], v[132:133], v[138:139]
	v_pk_fma_f32 v[132:133], v[46:47], s[36:37], v[132:133] op_sel_hi:[0, 1, 1]
	v_pk_fma_f32 v[70:71], s[72:73], v[132:133], 0 op_sel_hi:[1, 1, 0]
	v_pk_mul_f32 v[86:87], v[140:141], v[134:135]
	s_nop 0
	v_pk_fma_f32 v[134:135], v[46:47], s[38:39], v[86:87] op_sel_hi:[0, 1, 1]
	v_pk_mul_f32 v[72:73], v[42:43], v[10:11] op_sel_hi:[0,1]
	v_exp_f32_e32 v72, v72
	v_exp_f32_e32 v73, v73
	v_pk_mul_f32 v[86:87], v[42:43], v[12:13] op_sel_hi:[0,1]
	v_exp_f32_e32 v86, v86
	v_exp_f32_e32 v87, v87
	v_pk_mul_f32 v[72:73], v[72:73], v[136:137]
	v_pk_fma_f32 v[70:71], s[74:75], v[134:135], v[70:71]
	v_pk_fma_f32 v[136:137], v[46:47], s[40:41], v[72:73] op_sel_hi:[0, 1, 1]
	v_pk_mul_f32 v[72:73], v[86:87], v[122:123]
	v_pk_mul_f32 v[74:75], v[42:43], v[8:9] op_sel_hi:[0,1]
	v_pk_fma_f32 v[122:123], v[46:47], s[42:43], v[72:73] op_sel_hi:[0, 1, 1]
	v_pk_mul_f32 v[72:73], v[42:43], v[6:7] op_sel_hi:[0,1]
	v_exp_f32_e32 v72, v72
	v_exp_f32_e32 v73, v73
	v_exp_f32_e32 v74, v74
	v_exp_f32_e32 v75, v75
	v_pk_fma_f32 v[70:71], s[76:77], v[136:137], v[70:71]
	v_pk_mul_f32 v[72:73], v[72:73], v[124:125]
	v_pk_fma_f32 v[70:71], s[78:79], v[122:123], v[70:71]
	v_pk_fma_f32 v[124:125], v[46:47], s[44:45], v[72:73] op_sel_hi:[0, 1, 1]
	v_pk_mul_f32 v[72:73], v[74:75], v[126:127]
	v_pk_mul_f32 v[74:75], v[42:43], v[4:5] op_sel_hi:[0,1]
	v_pk_fma_f32 v[126:127], v[46:47], s[46:47], v[72:73] op_sel_hi:[0, 1, 1]
	v_pk_mul_f32 v[72:73], v[42:43], v[2:3] op_sel_hi:[0,1]
	v_exp_f32_e32 v72, v72
	v_exp_f32_e32 v73, v73
	v_exp_f32_e32 v74, v74
	v_exp_f32_e32 v75, v75
	v_pk_fma_f32 v[70:71], s[80:81], v[124:125], v[70:71]
	v_pk_mul_f32 v[72:73], v[72:73], v[128:129]
	v_pk_fma_f32 v[70:71], s[82:83], v[126:127], v[70:71]
	v_pk_fma_f32 v[128:129], v[46:47], s[48:49], v[72:73] op_sel_hi:[0, 1, 1]
	v_pk_mul_f32 v[72:73], v[74:75], v[130:131]
	v_pk_fma_f32 v[70:71], s[84:85], v[128:129], v[70:71]
	v_pk_fma_f32 v[130:131], v[46:47], s[50:51], v[72:73] op_sel_hi:[0, 1, 1]
	v_pk_fma_f32 v[70:71], s[86:87], v[130:131], v[70:71]
	s_nop 0
	v_add_f32_e32 v42, v70, v71
	v_fma_mix_f32 v42, v1, v43, v42 op_sel_hi:[0,1,0]
	v_fma_mixlo_f16 v42, v42, v47, 0 op_sel_hi:[0,1,0]
	ds_write_b16 v68, v42 offset:14496
	s_waitcnt lgkmcnt(0)
	s_load_dwordx16 s[36:51], s[54:55], 0x600
	s_load_dwordx16 s[72:87], s[54:55], 0x640
	v_cvt_f32_f16_sdwa v42, v51 dst_sel:DWORD dst_unused:UNUSED_PAD src0_sel:WORD_1
	v_cvt_f32_f16_sdwa v46, v43 dst_sel:DWORD dst_unused:UNUSED_PAD src0_sel:WORD_1
	v_pk_mul_f32 v[50:51], v[42:43], v[14:15] op_sel_hi:[0,1]
	v_exp_f32_e32 v50, v50
	v_exp_f32_e32 v51, v51
	v_pk_mul_f32 v[138:139], v[42:43], v[16:17] op_sel_hi:[0,1]
	v_exp_f32_e32 v138, v138
	v_exp_f32_e32 v139, v139
	v_mul_f32_e32 v46, v42, v46
	v_pk_mul_f32 v[50:51], v[50:51], v[132:133]
	v_pk_fma_f32 v[50:51], v[46:47], s[56:57], v[50:51] op_sel_hi:[0, 1, 1]
	v_pk_fma_f32 v[54:55], s[88:89], v[50:51], 0 op_sel_hi:[1, 1, 0]
	v_pk_mul_f32 v[106:107], v[138:139], v[134:135]
	s_nop 0
	v_pk_fma_f32 v[132:133], v[46:47], s[58:59], v[106:107] op_sel_hi:[0, 1, 1]
	v_pk_mul_f32 v[56:57], v[42:43], v[10:11] op_sel_hi:[0,1]
	v_exp_f32_e32 v56, v56
	v_exp_f32_e32 v57, v57
	v_pk_mul_f32 v[106:107], v[42:43], v[12:13] op_sel_hi:[0,1]
	v_exp_f32_e32 v106, v106
	v_exp_f32_e32 v107, v107
	v_pk_mul_f32 v[56:57], v[56:57], v[136:137]
	v_pk_fma_f32 v[54:55], s[90:91], v[132:133], v[54:55]
	v_pk_fma_f32 v[134:135], v[46:47], s[60:61], v[56:57] op_sel_hi:[0, 1, 1]
	v_pk_mul_f32 v[56:57], v[106:107], v[122:123]
	v_pk_mul_f32 v[58:59], v[42:43], v[8:9] op_sel_hi:[0,1]
	v_pk_fma_f32 v[122:123], v[46:47], s[62:63], v[56:57] op_sel_hi:[0, 1, 1]
	v_pk_mul_f32 v[56:57], v[42:43], v[6:7] op_sel_hi:[0,1]
	v_exp_f32_e32 v56, v56
	v_exp_f32_e32 v57, v57
	v_exp_f32_e32 v58, v58
	v_exp_f32_e32 v59, v59
	v_pk_fma_f32 v[54:55], s[92:93], v[134:135], v[54:55]
	v_pk_mul_f32 v[56:57], v[56:57], v[124:125]
	v_pk_fma_f32 v[54:55], s[94:95], v[122:123], v[54:55]
	v_pk_fma_f32 v[124:125], v[46:47], s[64:65], v[56:57] op_sel_hi:[0, 1, 1]
	v_pk_mul_f32 v[56:57], v[58:59], v[126:127]
	v_pk_mul_f32 v[58:59], v[42:43], v[4:5] op_sel_hi:[0,1]
	v_pk_fma_f32 v[126:127], v[46:47], s[66:67], v[56:57] op_sel_hi:[0, 1, 1]
	v_pk_mul_f32 v[56:57], v[42:43], v[2:3] op_sel_hi:[0,1]
	v_exp_f32_e32 v56, v56
	v_exp_f32_e32 v57, v57
	v_exp_f32_e32 v58, v58
	v_exp_f32_e32 v59, v59
	v_pk_fma_f32 v[54:55], s[96:97], v[124:125], v[54:55]
	v_pk_mul_f32 v[56:57], v[56:57], v[128:129]
	v_pk_fma_f32 v[54:55], s[98:99], v[126:127], v[54:55]
	v_pk_fma_f32 v[128:129], v[46:47], s[68:69], v[56:57] op_sel_hi:[0, 1, 1]
	v_pk_mul_f32 v[56:57], v[58:59], v[130:131]
	v_pk_fma_f32 v[54:55], s[20:21], v[128:129], v[54:55]
	v_pk_fma_f32 v[130:131], v[46:47], s[70:71], v[56:57] op_sel_hi:[0, 1, 1]
	v_pk_fma_f32 v[54:55], s[22:23], v[130:131], v[54:55]
	s_nop 0
	v_add_f32_e32 v42, v54, v55
	v_fma_mix_f32 v42, v1, v43, v42 op_sel:[0,1,0] op_sel_hi:[0,1,0]
	v_fma_mixlo_f16 v42, v42, v47, 0 op_sel:[0,1,0] op_sel_hi:[0,1,0]
	ds_write_b16 v68, v42 offset:15536
	s_waitcnt lgkmcnt(0)
	s_load_dwordx16 s[56:71], s[54:55], 0x680
	s_load_dwordx8 s[88:95], s[54:55], 0x6c0
	s_load_dwordx4 s[96:99], s[54:55], 0x6e0
	s_load_dwordx4 s[20:23], s[54:55], 0x6f0
	v_cvt_f32_f16_e32 v42, v52
	v_cvt_f32_f16_e32 v43, v44
	v_pk_mul_f32 v[136:137], v[42:43], v[14:15] op_sel_hi:[0,1]
	v_exp_f32_e32 v136, v136
	v_exp_f32_e32 v137, v137
	v_pk_mul_f32 v[138:139], v[42:43], v[16:17] op_sel_hi:[0,1]
	v_exp_f32_e32 v138, v138
	v_exp_f32_e32 v139, v139
	v_mul_f32_e32 v46, v42, v43
	v_pk_mul_f32 v[50:51], v[136:137], v[50:51]
	v_pk_fma_f32 v[50:51], v[46:47], s[36:37], v[50:51] op_sel_hi:[0, 1, 1]
	v_pk_fma_f32 v[70:71], s[72:73], v[50:51], 0 op_sel_hi:[1, 1, 0]
	v_pk_mul_f32 v[86:87], v[138:139], v[132:133]
	s_nop 0
	v_pk_fma_f32 v[132:133], v[46:47], s[38:39], v[86:87] op_sel_hi:[0, 1, 1]
	v_pk_mul_f32 v[72:73], v[42:43], v[10:11] op_sel_hi:[0,1]
	v_exp_f32_e32 v72, v72
	v_exp_f32_e32 v73, v73
	v_pk_mul_f32 v[86:87], v[42:43], v[12:13] op_sel_hi:[0,1]
	v_exp_f32_e32 v86, v86
	v_exp_f32_e32 v87, v87
	v_pk_mul_f32 v[72:73], v[72:73], v[134:135]
	v_pk_fma_f32 v[70:71], s[74:75], v[132:133], v[70:71]
	v_pk_fma_f32 v[134:135], v[46:47], s[40:41], v[72:73] op_sel_hi:[0, 1, 1]
	v_pk_mul_f32 v[72:73], v[86:87], v[122:123]
	v_pk_mul_f32 v[74:75], v[42:43], v[8:9] op_sel_hi:[0,1]
	v_pk_fma_f32 v[122:123], v[46:47], s[42:43], v[72:73] op_sel_hi:[0, 1, 1]
	v_pk_mul_f32 v[72:73], v[42:43], v[6:7] op_sel_hi:[0,1]
	v_exp_f32_e32 v72, v72
	v_exp_f32_e32 v73, v73
	v_exp_f32_e32 v74, v74
	v_exp_f32_e32 v75, v75
	v_pk_fma_f32 v[70:71], s[76:77], v[134:135], v[70:71]
	v_pk_mul_f32 v[72:73], v[72:73], v[124:125]
	v_pk_fma_f32 v[70:71], s[78:79], v[122:123], v[70:71]
	v_pk_fma_f32 v[124:125], v[46:47], s[44:45], v[72:73] op_sel_hi:[0, 1, 1]
	v_pk_mul_f32 v[72:73], v[74:75], v[126:127]
	v_pk_fma_f32 v[70:71], s[80:81], v[124:125], v[70:71]
	v_pk_fma_f32 v[126:127], v[46:47], s[46:47], v[72:73] op_sel_hi:[0, 1, 1]
	v_pk_mul_f32 v[72:73], v[42:43], v[2:3] op_sel_hi:[0,1]
	v_exp_f32_e32 v72, v72
	v_exp_f32_e32 v73, v73
	v_pk_mul_f32 v[42:43], v[42:43], v[4:5] op_sel_hi:[0,1]
	v_exp_f32_e32 v42, v42
	v_exp_f32_e32 v43, v43
	v_pk_mul_f32 v[72:73], v[72:73], v[128:129]
	v_pk_fma_f32 v[70:71], s[82:83], v[126:127], v[70:71]
	v_pk_fma_f32 v[128:129], v[46:47], s[48:49], v[72:73] op_sel_hi:[0, 1, 1]
	v_pk_mul_f32 v[42:43], v[42:43], v[130:131]
	v_pk_fma_f32 v[70:71], s[84:85], v[128:129], v[70:71]
	v_pk_fma_f32 v[42:43], v[46:47], s[50:51], v[42:43] op_sel_hi:[0, 1, 1]
	v_pk_fma_f32 v[46:47], s[86:87], v[42:43], v[70:71]
	s_nop 0
	v_add_f32_e32 v46, v46, v47
	v_fma_mix_f32 v46, v1, v44, v46 op_sel_hi:[0,1,0]
	v_fma_mixlo_f16 v46, v46, v48, 0 op_sel_hi:[0,1,0]
	ds_write_b16 v68, v46 offset:16576
	s_waitcnt lgkmcnt(0)
	s_load_dwordx16 s[36:51], s[54:55], 0x700
	s_load_dwordx16 s[72:87], s[54:55], 0x740
	v_cvt_f32_f16_sdwa v46, v52 dst_sel:DWORD dst_unused:UNUSED_PAD src0_sel:WORD_1
	v_cvt_f32_f16_sdwa v47, v44 dst_sel:DWORD dst_unused:UNUSED_PAD src0_sel:WORD_1
	v_pk_mul_f32 v[130:131], v[46:47], v[14:15] op_sel_hi:[0,1]
	v_exp_f32_e32 v130, v130
	v_exp_f32_e32 v131, v131
	v_pk_mul_f32 v[136:137], v[46:47], v[16:17] op_sel_hi:[0,1]
	v_exp_f32_e32 v136, v136
	v_exp_f32_e32 v137, v137
	v_mul_f32_e32 v52, v46, v47
	v_pk_mul_f32 v[50:51], v[130:131], v[50:51]
	v_pk_fma_f32 v[50:51], v[52:53], s[56:57], v[50:51] op_sel_hi:[0, 1, 1]
	v_pk_fma_f32 v[54:55], s[88:89], v[50:51], 0 op_sel_hi:[1, 1, 0]
	v_pk_mul_f32 v[106:107], v[136:137], v[132:133]
	s_nop 0
	v_pk_fma_f32 v[130:131], v[52:53], s[58:59], v[106:107] op_sel_hi:[0, 1, 1]
	v_pk_mul_f32 v[56:57], v[46:47], v[10:11] op_sel_hi:[0,1]
	v_exp_f32_e32 v56, v56
	v_exp_f32_e32 v57, v57
	v_pk_mul_f32 v[106:107], v[46:47], v[12:13] op_sel_hi:[0,1]
	v_exp_f32_e32 v106, v106
	v_exp_f32_e32 v107, v107
	v_pk_mul_f32 v[56:57], v[56:57], v[134:135]
	v_pk_fma_f32 v[54:55], s[90:91], v[130:131], v[54:55]
	v_pk_fma_f32 v[132:133], v[52:53], s[60:61], v[56:57] op_sel_hi:[0, 1, 1]
	v_pk_mul_f32 v[56:57], v[106:107], v[122:123]
	v_pk_mul_f32 v[58:59], v[46:47], v[8:9] op_sel_hi:[0,1]
	v_pk_fma_f32 v[122:123], v[52:53], s[62:63], v[56:57] op_sel_hi:[0, 1, 1]
	v_pk_mul_f32 v[56:57], v[46:47], v[6:7] op_sel_hi:[0,1]
	v_exp_f32_e32 v56, v56
	v_exp_f32_e32 v57, v57
	v_exp_f32_e32 v58, v58
	v_exp_f32_e32 v59, v59
	v_pk_fma_f32 v[54:55], s[92:93], v[132:133], v[54:55]
	v_pk_mul_f32 v[56:57], v[56:57], v[124:125]
	v_pk_fma_f32 v[54:55], s[94:95], v[122:123], v[54:55]
	v_pk_fma_f32 v[124:125], v[52:53], s[64:65], v[56:57] op_sel_hi:[0, 1, 1]
	v_pk_mul_f32 v[56:57], v[58:59], v[126:127]
	v_pk_fma_f32 v[54:55], s[96:97], v[124:125], v[54:55]
	v_pk_fma_f32 v[126:127], v[52:53], s[66:67], v[56:57] op_sel_hi:[0, 1, 1]
	v_pk_mul_f32 v[56:57], v[46:47], v[2:3] op_sel_hi:[0,1]
	v_exp_f32_e32 v56, v56
	v_exp_f32_e32 v57, v57
	v_pk_mul_f32 v[46:47], v[46:47], v[4:5] op_sel_hi:[0,1]
	v_exp_f32_e32 v46, v46
	v_exp_f32_e32 v47, v47
	v_pk_mul_f32 v[56:57], v[56:57], v[128:129]
	v_pk_fma_f32 v[54:55], s[98:99], v[126:127], v[54:55]
	v_pk_fma_f32 v[128:129], v[52:53], s[68:69], v[56:57] op_sel_hi:[0, 1, 1]
	v_pk_mul_f32 v[42:43], v[46:47], v[42:43]
	v_pk_fma_f32 v[54:55], s[20:21], v[128:129], v[54:55]
	v_pk_fma_f32 v[42:43], v[52:53], s[70:71], v[42:43] op_sel_hi:[0, 1, 1]
	v_pk_fma_f32 v[46:47], s[22:23], v[42:43], v[54:55]
	s_nop 0
	v_add_f32_e32 v46, v46, v47
	v_fma_mix_f32 v44, v1, v44, v46 op_sel:[0,1,0] op_sel_hi:[0,1,0]
	v_fma_mixlo_f16 v44, v44, v48, 0 op_sel:[0,1,0] op_sel_hi:[0,1,0]
	ds_write_b16 v68, v44 offset:17616
	s_waitcnt lgkmcnt(0)
	s_load_dwordx16 s[56:71], s[54:55], 0x780
	s_load_dwordx8 s[88:95], s[54:55], 0x7c0
	s_load_dwordx4 s[96:99], s[54:55], 0x7e0
	s_load_dwordx4 s[20:23], s[54:55], 0x7f0
	v_cvt_f32_f16_e32 v44, v53
	v_cvt_f32_f16_e32 v46, v45
	v_pk_mul_f32 v[134:135], v[44:45], v[14:15] op_sel_hi:[0,1]
	v_exp_f32_e32 v134, v134
	v_exp_f32_e32 v135, v135
	v_pk_mul_f32 v[136:137], v[44:45], v[16:17] op_sel_hi:[0,1]
	v_exp_f32_e32 v136, v136
	v_exp_f32_e32 v137, v137
	v_mul_f32_e32 v46, v44, v46
	v_pk_mul_f32 v[50:51], v[134:135], v[50:51]
	v_pk_fma_f32 v[50:51], v[46:47], s[36:37], v[50:51] op_sel_hi:[0, 1, 1]
	v_pk_fma_f32 v[70:71], s[72:73], v[50:51], 0 op_sel_hi:[1, 1, 0]
	v_pk_mul_f32 v[86:87], v[136:137], v[130:131]
	s_nop 0
	v_pk_fma_f32 v[130:131], v[46:47], s[38:39], v[86:87] op_sel_hi:[0, 1, 1]
	v_pk_mul_f32 v[72:73], v[44:45], v[10:11] op_sel_hi:[0,1]
	v_exp_f32_e32 v72, v72
	v_exp_f32_e32 v73, v73
	v_pk_mul_f32 v[86:87], v[44:45], v[12:13] op_sel_hi:[0,1]
	v_exp_f32_e32 v86, v86
	v_exp_f32_e32 v87, v87
	v_pk_mul_f32 v[72:73], v[72:73], v[132:133]
	v_pk_fma_f32 v[70:71], s[74:75], v[130:131], v[70:71]
	v_pk_fma_f32 v[132:133], v[46:47], s[40:41], v[72:73] op_sel_hi:[0, 1, 1]
	v_pk_mul_f32 v[72:73], v[86:87], v[122:123]
	v_pk_mul_f32 v[74:75], v[44:45], v[8:9] op_sel_hi:[0,1]
	v_pk_fma_f32 v[122:123], v[46:47], s[42:43], v[72:73] op_sel_hi:[0, 1, 1]
	v_pk_mul_f32 v[72:73], v[44:45], v[6:7] op_sel_hi:[0,1]
	v_exp_f32_e32 v72, v72
	v_exp_f32_e32 v73, v73
	v_exp_f32_e32 v74, v74
	v_exp_f32_e32 v75, v75
	v_pk_fma_f32 v[70:71], s[76:77], v[132:133], v[70:71]
	v_pk_mul_f32 v[72:73], v[72:73], v[124:125]
	v_pk_fma_f32 v[70:71], s[78:79], v[122:123], v[70:71]
	v_pk_fma_f32 v[124:125], v[46:47], s[44:45], v[72:73] op_sel_hi:[0, 1, 1]
	v_pk_mul_f32 v[72:73], v[74:75], v[126:127]
	v_pk_mul_f32 v[74:75], v[44:45], v[4:5] op_sel_hi:[0,1]
	v_pk_fma_f32 v[126:127], v[46:47], s[46:47], v[72:73] op_sel_hi:[0, 1, 1]
	v_pk_mul_f32 v[72:73], v[44:45], v[2:3] op_sel_hi:[0,1]
	v_exp_f32_e32 v72, v72
	v_exp_f32_e32 v73, v73
	v_exp_f32_e32 v74, v74
	v_exp_f32_e32 v75, v75
	v_pk_fma_f32 v[70:71], s[80:81], v[124:125], v[70:71]
	v_pk_mul_f32 v[72:73], v[72:73], v[128:129]
	v_pk_fma_f32 v[70:71], s[82:83], v[126:127], v[70:71]
	v_pk_fma_f32 v[128:129], v[46:47], s[48:49], v[72:73] op_sel_hi:[0, 1, 1]
	v_pk_mul_f32 v[42:43], v[74:75], v[42:43]
	v_pk_fma_f32 v[70:71], s[84:85], v[128:129], v[70:71]
	v_pk_fma_f32 v[42:43], v[46:47], s[50:51], v[42:43] op_sel_hi:[0, 1, 1]
	v_pk_fma_f32 v[46:47], s[86:87], v[42:43], v[70:71]
	s_nop 0
	v_add_f32_e32 v44, v46, v47
	v_fma_mix_f32 v44, v1, v45, v44 op_sel_hi:[0,1,0]
	v_fma_mixlo_f16 v44, v44, v49, 0 op_sel_hi:[0,1,0]
	ds_write_b16 v68, v44 offset:18656
	s_waitcnt lgkmcnt(0)
	s_load_dwordx16 s[36:51], s[54:55], 0x800
	s_load_dwordx16 s[72:87], s[54:55], 0x840
	v_cvt_f32_f16_sdwa v44, v53 dst_sel:DWORD dst_unused:UNUSED_PAD src0_sel:WORD_1
	v_cvt_f32_f16_sdwa v46, v45 dst_sel:DWORD dst_unused:UNUSED_PAD src0_sel:WORD_1
	v_pk_mul_f32 v[52:53], v[44:45], v[14:15] op_sel_hi:[0,1]
	v_pk_mul_f32 v[134:135], v[44:45], v[16:17] op_sel_hi:[0,1]
	v_exp_f32_e32 v52, v52
	v_exp_f32_e32 v53, v53
	v_exp_f32_e32 v134, v134
	v_exp_f32_e32 v135, v135
	v_mul_f32_e32 v46, v44, v46
	v_pk_mul_f32 v[50:51], v[52:53], v[50:51]
	v_pk_mul_f32 v[52:53], v[134:135], v[130:131]
	v_pk_fma_f32 v[130:131], v[46:47], s[58:59], v[52:53] op_sel_hi:[0, 1, 1]
	v_pk_mul_f32 v[52:53], v[44:45], v[10:11] op_sel_hi:[0,1]
	v_pk_fma_f32 v[136:137], v[46:47], s[56:57], v[50:51] op_sel_hi:[0, 1, 1]
	v_exp_f32_e32 v52, v52
	v_exp_f32_e32 v53, v53
	v_pk_mul_f32 v[54:55], v[44:45], v[12:13] op_sel_hi:[0,1]
	v_exp_f32_e32 v54, v54
	v_exp_f32_e32 v55, v55
	v_pk_fma_f32 v[50:51], s[88:89], v[136:137], 0 op_sel_hi:[1, 1, 0]
	v_pk_mul_f32 v[52:53], v[52:53], v[132:133]
	v_pk_fma_f32 v[50:51], s[90:91], v[130:131], v[50:51]
	v_pk_fma_f32 v[132:133], v[46:47], s[60:61], v[52:53] op_sel_hi:[0, 1, 1]
	v_pk_mul_f32 v[52:53], v[54:55], v[122:123]
	v_pk_fma_f32 v[50:51], s[92:93], v[132:133], v[50:51]
	v_pk_fma_f32 v[110:111], v[46:47], s[62:63], v[52:53] op_sel_hi:[0, 1, 1]
	v_pk_mul_f32 v[52:53], v[44:45], v[6:7] op_sel_hi:[0,1]
	v_exp_f32_e32 v52, v52
	v_exp_f32_e32 v53, v53
	v_pk_mul_f32 v[54:55], v[44:45], v[8:9] op_sel_hi:[0,1]
	v_exp_f32_e32 v54, v54
	v_exp_f32_e32 v55, v55
	v_pk_mul_f32 v[52:53], v[52:53], v[124:125]
	v_pk_fma_f32 v[50:51], s[94:95], v[110:111], v[50:51]
	v_pk_fma_f32 v[112:113], v[46:47], s[64:65], v[52:53] op_sel_hi:[0, 1, 1]
	v_pk_mul_f32 v[52:53], v[54:55], v[126:127]
	v_pk_fma_f32 v[50:51], s[96:97], v[112:113], v[50:51]
	v_pk_fma_f32 v[114:115], v[46:47], s[66:67], v[52:53] op_sel_hi:[0, 1, 1]
	v_pk_mul_f32 v[52:53], v[44:45], v[2:3] op_sel_hi:[0,1]
	v_exp_f32_e32 v52, v52
	v_exp_f32_e32 v53, v53
	v_pk_mul_f32 v[54:55], v[44:45], v[4:5] op_sel_hi:[0,1]
	v_exp_f32_e32 v54, v54
	v_exp_f32_e32 v55, v55
	v_pk_mul_f32 v[52:53], v[52:53], v[128:129]
	v_pk_fma_f32 v[50:51], s[98:99], v[114:115], v[50:51]
	v_pk_fma_f32 v[116:117], v[46:47], s[68:69], v[52:53] op_sel_hi:[0, 1, 1]
	v_pk_mul_f32 v[42:43], v[54:55], v[42:43]
	v_pk_fma_f32 v[50:51], s[20:21], v[116:117], v[50:51]
	v_pk_fma_f32 v[118:119], v[46:47], s[70:71], v[42:43] op_sel_hi:[0, 1, 1]
	v_pk_fma_f32 v[42:43], s[22:23], v[118:119], v[50:51]
	s_nop 0
	v_add_f32_e32 v42, v42, v43
	v_fma_mix_f32 v42, v1, v45, v42 op_sel:[0,1,0] op_sel_hi:[0,1,0]
	v_fma_mixlo_f16 v42, v42, v49, 0 op_sel:[0,1,0] op_sel_hi:[0,1,0]
	ds_write_b16 v68, v42 offset:19696
	s_waitcnt lgkmcnt(0)
	s_load_dwordx16 s[56:71], s[54:55], 0x880
	s_load_dwordx8 s[88:95], s[54:55], 0x8c0
	s_load_dwordx4 s[96:99], s[54:55], 0x8e0
	s_load_dwordx4 s[20:23], s[54:55], 0x8f0
	s_waitcnt vmcnt(5)
	v_cvt_f32_f16_e32 v120, v38
	s_waitcnt vmcnt(4)
	v_cvt_f32_f16_e32 v69, v30
	v_pk_mul_f32 v[124:125], v[120:121], v[14:15] op_sel_hi:[0,1]
	v_exp_f32_e32 v124, v124
	v_exp_f32_e32 v125, v125
	v_pk_mul_f32 v[126:127], v[120:121], v[16:17] op_sel_hi:[0,1]
	v_exp_f32_e32 v126, v126
	v_exp_f32_e32 v127, v127
	v_mul_f32_e32 v122, v120, v69
	v_pk_mul_f32 v[124:125], v[124:125], v[136:137]
	v_pk_fma_f32 v[124:125], v[122:123], s[36:37], v[124:125] op_sel_hi:[0, 1, 1]
	v_pk_fma_f32 v[70:71], s[72:73], v[124:125], 0 op_sel_hi:[1, 1, 0]
	v_pk_mul_f32 v[86:87], v[126:127], v[130:131]
	s_nop 0
	v_pk_fma_f32 v[126:127], v[122:123], s[38:39], v[86:87] op_sel_hi:[0, 1, 1]
	v_pk_mul_f32 v[72:73], v[120:121], v[10:11] op_sel_hi:[0,1]
	v_exp_f32_e32 v72, v72
	v_exp_f32_e32 v73, v73
	v_pk_mul_f32 v[86:87], v[120:121], v[12:13] op_sel_hi:[0,1]
	v_exp_f32_e32 v86, v86
	v_exp_f32_e32 v87, v87
	v_pk_mul_f32 v[72:73], v[72:73], v[132:133]
	v_pk_fma_f32 v[70:71], s[74:75], v[126:127], v[70:71]
	v_pk_fma_f32 v[128:129], v[122:123], s[40:41], v[72:73] op_sel_hi:[0, 1, 1]
	v_pk_mul_f32 v[72:73], v[86:87], v[110:111]
	v_pk_mul_f32 v[74:75], v[120:121], v[8:9] op_sel_hi:[0,1]
	v_pk_fma_f32 v[110:111], v[122:123], s[42:43], v[72:73] op_sel_hi:[0, 1, 1]
	v_pk_mul_f32 v[72:73], v[120:121], v[6:7] op_sel_hi:[0,1]
	v_exp_f32_e32 v72, v72
	v_exp_f32_e32 v73, v73
	v_exp_f32_e32 v74, v74
	v_exp_f32_e32 v75, v75
	v_pk_fma_f32 v[70:71], s[76:77], v[128:129], v[70:71]
	v_pk_mul_f32 v[72:73], v[72:73], v[112:113]
	v_pk_fma_f32 v[70:71], s[78:79], v[110:111], v[70:71]
	v_pk_fma_f32 v[112:113], v[122:123], s[44:45], v[72:73] op_sel_hi:[0, 1, 1]
	v_pk_mul_f32 v[72:73], v[74:75], v[114:115]
	v_pk_mul_f32 v[74:75], v[120:121], v[4:5] op_sel_hi:[0,1]
	v_pk_fma_f32 v[114:115], v[122:123], s[46:47], v[72:73] op_sel_hi:[0, 1, 1]
	v_pk_mul_f32 v[72:73], v[120:121], v[2:3] op_sel_hi:[0,1]
	v_exp_f32_e32 v72, v72
	v_exp_f32_e32 v73, v73
	v_exp_f32_e32 v74, v74
	v_exp_f32_e32 v75, v75
	v_pk_fma_f32 v[70:71], s[80:81], v[112:113], v[70:71]
	v_pk_mul_f32 v[72:73], v[72:73], v[116:117]
	v_pk_fma_f32 v[70:71], s[82:83], v[114:115], v[70:71]
	v_pk_fma_f32 v[116:117], v[122:123], s[48:49], v[72:73] op_sel_hi:[0, 1, 1]
	v_pk_mul_f32 v[72:73], v[74:75], v[118:119]
	v_pk_fma_f32 v[70:71], s[84:85], v[116:117], v[70:71]
	v_pk_fma_f32 v[118:119], v[122:123], s[50:51], v[72:73] op_sel_hi:[0, 1, 1]
	v_pk_fma_f32 v[70:71], s[86:87], v[118:119], v[70:71]
	s_nop 0
	v_add_f32_e32 v69, v70, v71
	v_fma_mix_f32 v69, v1, v30, v69 op_sel_hi:[0,1,0]
	s_waitcnt vmcnt(3)
	v_fma_mixlo_f16 v69, v69, v34, 0 op_sel_hi:[0,1,0]
	ds_write_b16 v68, v69 offset:20736
	s_waitcnt lgkmcnt(0)
	s_load_dwordx16 s[36:51], s[54:55], 0x900
	s_load_dwordx16 s[72:87], s[54:55], 0x940
	v_cvt_f32_f16_sdwa v38, v38 dst_sel:DWORD dst_unused:UNUSED_PAD src0_sel:WORD_1
	v_cvt_f32_f16_sdwa v69, v30 dst_sel:DWORD dst_unused:UNUSED_PAD src0_sel:WORD_1
	v_pk_mul_f32 v[122:123], v[38:39], v[14:15] op_sel_hi:[0,1]
	v_exp_f32_e32 v122, v122
	v_exp_f32_e32 v123, v123
	v_pk_mul_f32 v[130:131], v[38:39], v[16:17] op_sel_hi:[0,1]
	v_exp_f32_e32 v130, v130
	v_exp_f32_e32 v131, v131
	v_mul_f32_e32 v120, v38, v69
	v_pk_mul_f32 v[122:123], v[122:123], v[124:125]
	v_pk_fma_f32 v[122:123], v[120:121], s[56:57], v[122:123] op_sel_hi:[0, 1, 1]
	v_pk_fma_f32 v[42:43], s[88:89], v[122:123], 0 op_sel_hi:[1, 1, 0]
	v_pk_mul_f32 v[58:59], v[130:131], v[126:127]
	s_nop 0
	v_pk_fma_f32 v[124:125], v[120:121], s[58:59], v[58:59] op_sel_hi:[0, 1, 1]
	v_pk_mul_f32 v[44:45], v[38:39], v[10:11] op_sel_hi:[0,1]
	v_exp_f32_e32 v44, v44
	v_exp_f32_e32 v45, v45
	v_pk_mul_f32 v[58:59], v[38:39], v[12:13] op_sel_hi:[0,1]
	v_exp_f32_e32 v58, v58
	v_exp_f32_e32 v59, v59
	v_pk_mul_f32 v[44:45], v[44:45], v[128:129]
	v_pk_fma_f32 v[42:43], s[90:91], v[124:125], v[42:43]
	v_pk_fma_f32 v[126:127], v[120:121], s[60:61], v[44:45] op_sel_hi:[0, 1, 1]
	v_pk_mul_f32 v[44:45], v[58:59], v[110:111]
	v_pk_mul_f32 v[46:47], v[38:39], v[8:9] op_sel_hi:[0,1]
	v_pk_fma_f32 v[110:111], v[120:121], s[62:63], v[44:45] op_sel_hi:[0, 1, 1]
	v_pk_mul_f32 v[44:45], v[38:39], v[6:7] op_sel_hi:[0,1]
	v_exp_f32_e32 v44, v44
	v_exp_f32_e32 v45, v45
	v_exp_f32_e32 v46, v46
	v_exp_f32_e32 v47, v47
	v_pk_fma_f32 v[42:43], s[92:93], v[126:127], v[42:43]
	v_pk_mul_f32 v[44:45], v[44:45], v[112:113]
	v_pk_fma_f32 v[42:43], s[94:95], v[110:111], v[42:43]
	v_pk_fma_f32 v[112:113], v[120:121], s[64:65], v[44:45] op_sel_hi:[0, 1, 1]
	v_pk_mul_f32 v[44:45], v[46:47], v[114:115]
	v_pk_mul_f32 v[46:47], v[38:39], v[4:5] op_sel_hi:[0,1]
	v_pk_fma_f32 v[114:115], v[120:121], s[66:67], v[44:45] op_sel_hi:[0, 1, 1]
	v_pk_mul_f32 v[44:45], v[38:39], v[2:3] op_sel_hi:[0,1]
	v_exp_f32_e32 v44, v44
	v_exp_f32_e32 v45, v45
	v_exp_f32_e32 v46, v46
	v_exp_f32_e32 v47, v47
	v_pk_fma_f32 v[42:43], s[96:97], v[112:113], v[42:43]
	v_pk_mul_f32 v[44:45], v[44:45], v[116:117]
	v_pk_fma_f32 v[42:43], s[98:99], v[114:115], v[42:43]
	v_pk_fma_f32 v[116:117], v[120:121], s[68:69], v[44:45] op_sel_hi:[0, 1, 1]
	v_pk_mul_f32 v[44:45], v[46:47], v[118:119]
	v_pk_fma_f32 v[42:43], s[20:21], v[116:117], v[42:43]
	v_pk_fma_f32 v[118:119], v[120:121], s[70:71], v[44:45] op_sel_hi:[0, 1, 1]
	v_pk_fma_f32 v[42:43], s[22:23], v[118:119], v[42:43]
	s_nop 0
	v_add_f32_e32 v38, v42, v43
	v_fma_mix_f32 v30, v1, v30, v38 op_sel:[0,1,0] op_sel_hi:[0,1,0]
	v_fma_mixlo_f16 v30, v30, v34, 0 op_sel:[0,1,0] op_sel_hi:[0,1,0]
	ds_write_b16 v68, v30 offset:21776
	s_waitcnt lgkmcnt(0)
	s_load_dwordx16 s[56:71], s[54:55], 0x980
	s_load_dwordx8 s[88:95], s[54:55], 0x9c0
	s_load_dwordx4 s[96:99], s[54:55], 0x9e0
	s_load_dwordx4 s[20:23], s[54:55], 0x9f0
	v_cvt_f32_f16_e32 v30, v39
	v_cvt_f32_f16_e32 v34, v31
	v_pk_mul_f32 v[120:121], v[30:31], v[14:15] op_sel_hi:[0,1]
	v_exp_f32_e32 v120, v120
	v_exp_f32_e32 v121, v121
	v_pk_mul_f32 v[128:129], v[30:31], v[16:17] op_sel_hi:[0,1]
	v_exp_f32_e32 v128, v128
	v_exp_f32_e32 v129, v129
	v_mul_f32_e32 v34, v30, v34
	v_pk_mul_f32 v[120:121], v[120:121], v[122:123]
	v_pk_fma_f32 v[120:121], v[34:35], s[36:37], v[120:121] op_sel_hi:[0, 1, 1]
	v_pk_fma_f32 v[70:71], s[72:73], v[120:121], 0 op_sel_hi:[1, 1, 0]
	v_pk_mul_f32 v[86:87], v[128:129], v[124:125]
	s_nop 0
	v_pk_fma_f32 v[122:123], v[34:35], s[38:39], v[86:87] op_sel_hi:[0, 1, 1]
	v_pk_mul_f32 v[72:73], v[30:31], v[10:11] op_sel_hi:[0,1]
	v_exp_f32_e32 v72, v72
	v_exp_f32_e32 v73, v73
	v_pk_mul_f32 v[86:87], v[30:31], v[12:13] op_sel_hi:[0,1]
	v_exp_f32_e32 v86, v86
	v_exp_f32_e32 v87, v87
	v_pk_mul_f32 v[72:73], v[72:73], v[126:127]
	v_pk_fma_f32 v[70:71], s[74:75], v[122:123], v[70:71]
	v_pk_fma_f32 v[124:125], v[34:35], s[40:41], v[72:73] op_sel_hi:[0, 1, 1]
	v_pk_mul_f32 v[72:73], v[86:87], v[110:111]
	v_pk_mul_f32 v[74:75], v[30:31], v[8:9] op_sel_hi:[0,1]
	v_pk_fma_f32 v[110:111], v[34:35], s[42:43], v[72:73] op_sel_hi:[0, 1, 1]
	v_pk_mul_f32 v[72:73], v[30:31], v[6:7] op_sel_hi:[0,1]
	v_exp_f32_e32 v72, v72
	v_exp_f32_e32 v73, v73
	v_exp_f32_e32 v74, v74
	v_exp_f32_e32 v75, v75
	v_pk_fma_f32 v[70:71], s[76:77], v[124:125], v[70:71]
	v_pk_mul_f32 v[72:73], v[72:73], v[112:113]
	v_pk_fma_f32 v[70:71], s[78:79], v[110:111], v[70:71]
	v_pk_fma_f32 v[112:113], v[34:35], s[44:45], v[72:73] op_sel_hi:[0, 1, 1]
	v_pk_mul_f32 v[72:73], v[74:75], v[114:115]
	v_pk_mul_f32 v[74:75], v[30:31], v[4:5] op_sel_hi:[0,1]
	v_pk_fma_f32 v[114:115], v[34:35], s[46:47], v[72:73] op_sel_hi:[0, 1, 1]
	v_pk_mul_f32 v[72:73], v[30:31], v[2:3] op_sel_hi:[0,1]
	v_exp_f32_e32 v72, v72
	v_exp_f32_e32 v73, v73
	v_exp_f32_e32 v74, v74
	v_exp_f32_e32 v75, v75
	v_pk_fma_f32 v[70:71], s[80:81], v[112:113], v[70:71]
	v_pk_mul_f32 v[72:73], v[72:73], v[116:117]
	v_pk_fma_f32 v[70:71], s[82:83], v[114:115], v[70:71]
	v_pk_fma_f32 v[116:117], v[34:35], s[48:49], v[72:73] op_sel_hi:[0, 1, 1]
	v_pk_mul_f32 v[72:73], v[74:75], v[118:119]
	v_pk_fma_f32 v[70:71], s[84:85], v[116:117], v[70:71]
	v_pk_fma_f32 v[118:119], v[34:35], s[50:51], v[72:73] op_sel_hi:[0, 1, 1]
	v_pk_fma_f32 v[70:71], s[86:87], v[118:119], v[70:71]
	s_nop 0
	v_add_f32_e32 v30, v70, v71
	v_fma_mix_f32 v30, v1, v31, v30 op_sel_hi:[0,1,0]
	v_fma_mixlo_f16 v30, v30, v35, 0 op_sel_hi:[0,1,0]
	ds_write_b16 v68, v30 offset:22816
	s_waitcnt lgkmcnt(0)
	s_load_dwordx16 s[36:51], s[54:55], 0xa00
	s_load_dwordx16 s[72:87], s[54:55], 0xa40
	v_cvt_f32_f16_sdwa v30, v39 dst_sel:DWORD dst_unused:UNUSED_PAD src0_sel:WORD_1
	v_cvt_f32_f16_sdwa v34, v31 dst_sel:DWORD dst_unused:UNUSED_PAD src0_sel:WORD_1
	v_pk_mul_f32 v[38:39], v[30:31], v[14:15] op_sel_hi:[0,1]
	v_exp_f32_e32 v38, v38
	v_exp_f32_e32 v39, v39
	v_pk_mul_f32 v[126:127], v[30:31], v[16:17] op_sel_hi:[0,1]
	v_exp_f32_e32 v126, v126
	v_exp_f32_e32 v127, v127
	v_mul_f32_e32 v34, v30, v34
	v_pk_mul_f32 v[38:39], v[38:39], v[120:121]
	v_pk_fma_f32 v[38:39], v[34:35], s[56:57], v[38:39] op_sel_hi:[0, 1, 1]
	v_pk_fma_f32 v[42:43], s[88:89], v[38:39], 0 op_sel_hi:[1, 1, 0]
	v_pk_mul_f32 v[58:59], v[126:127], v[122:123]
	s_nop 0
	v_pk_fma_f32 v[120:121], v[34:35], s[58:59], v[58:59] op_sel_hi:[0, 1, 1]
	v_pk_mul_f32 v[44:45], v[30:31], v[10:11] op_sel_hi:[0,1]
	v_exp_f32_e32 v44, v44
	v_exp_f32_e32 v45, v45
	v_pk_mul_f32 v[58:59], v[30:31], v[12:13] op_sel_hi:[0,1]
	v_exp_f32_e32 v58, v58
	v_exp_f32_e32 v59, v59
	v_pk_mul_f32 v[44:45], v[44:45], v[124:125]
	v_pk_fma_f32 v[42:43], s[90:91], v[120:121], v[42:43]
	v_pk_fma_f32 v[122:123], v[34:35], s[60:61], v[44:45] op_sel_hi:[0, 1, 1]
	v_pk_mul_f32 v[44:45], v[58:59], v[110:111]
	v_pk_mul_f32 v[46:47], v[30:31], v[8:9] op_sel_hi:[0,1]
	v_pk_fma_f32 v[110:111], v[34:35], s[62:63], v[44:45] op_sel_hi:[0, 1, 1]
	v_pk_mul_f32 v[44:45], v[30:31], v[6:7] op_sel_hi:[0,1]
	v_exp_f32_e32 v44, v44
	v_exp_f32_e32 v45, v45
	v_exp_f32_e32 v46, v46
	v_exp_f32_e32 v47, v47
	v_pk_fma_f32 v[42:43], s[92:93], v[122:123], v[42:43]
	v_pk_mul_f32 v[44:45], v[44:45], v[112:113]
	v_pk_fma_f32 v[42:43], s[94:95], v[110:111], v[42:43]
	v_pk_fma_f32 v[112:113], v[34:35], s[64:65], v[44:45] op_sel_hi:[0, 1, 1]
	v_pk_mul_f32 v[44:45], v[46:47], v[114:115]
	v_pk_mul_f32 v[46:47], v[30:31], v[4:5] op_sel_hi:[0,1]
	v_pk_fma_f32 v[114:115], v[34:35], s[66:67], v[44:45] op_sel_hi:[0, 1, 1]
	v_pk_mul_f32 v[44:45], v[30:31], v[2:3] op_sel_hi:[0,1]
	v_exp_f32_e32 v44, v44
	v_exp_f32_e32 v45, v45
	v_exp_f32_e32 v46, v46
	v_exp_f32_e32 v47, v47
	v_pk_fma_f32 v[42:43], s[96:97], v[112:113], v[42:43]
	v_pk_mul_f32 v[44:45], v[44:45], v[116:117]
	v_pk_fma_f32 v[42:43], s[98:99], v[114:115], v[42:43]
	v_pk_fma_f32 v[116:117], v[34:35], s[68:69], v[44:45] op_sel_hi:[0, 1, 1]
	v_pk_mul_f32 v[44:45], v[46:47], v[118:119]
	v_pk_fma_f32 v[42:43], s[20:21], v[116:117], v[42:43]
	v_pk_fma_f32 v[118:119], v[34:35], s[70:71], v[44:45] op_sel_hi:[0, 1, 1]
	v_pk_fma_f32 v[42:43], s[22:23], v[118:119], v[42:43]
	s_nop 0
	v_add_f32_e32 v30, v42, v43
	v_fma_mix_f32 v30, v1, v31, v30 op_sel:[0,1,0] op_sel_hi:[0,1,0]
	v_fma_mixlo_f16 v30, v30, v35, 0 op_sel:[0,1,0] op_sel_hi:[0,1,0]
	ds_write_b16 v68, v30 offset:23856
	s_waitcnt lgkmcnt(0)
	s_load_dwordx16 s[56:71], s[54:55], 0xa80
	s_load_dwordx8 s[88:95], s[54:55], 0xac0
	s_load_dwordx4 s[96:99], s[54:55], 0xae0
	s_load_dwordx4 s[20:23], s[54:55], 0xaf0
	v_cvt_f32_f16_e32 v30, v40
	v_cvt_f32_f16_e32 v31, v32
	v_pk_mul_f32 v[124:125], v[30:31], v[14:15] op_sel_hi:[0,1]
	v_exp_f32_e32 v124, v124
	v_exp_f32_e32 v125, v125
	v_pk_mul_f32 v[126:127], v[30:31], v[16:17] op_sel_hi:[0,1]
	v_exp_f32_e32 v126, v126
	v_exp_f32_e32 v127, v127
	v_mul_f32_e32 v34, v30, v31
	v_pk_mul_f32 v[38:39], v[124:125], v[38:39]
	v_pk_fma_f32 v[38:39], v[34:35], s[36:37], v[38:39] op_sel_hi:[0, 1, 1]
	v_pk_fma_f32 v[70:71], s[72:73], v[38:39], 0 op_sel_hi:[1, 1, 0]
	v_pk_mul_f32 v[86:87], v[126:127], v[120:121]
	s_nop 0
	v_pk_fma_f32 v[120:121], v[34:35], s[38:39], v[86:87] op_sel_hi:[0, 1, 1]
	v_pk_mul_f32 v[72:73], v[30:31], v[10:11] op_sel_hi:[0,1]
	v_exp_f32_e32 v72, v72
	v_exp_f32_e32 v73, v73
	v_pk_mul_f32 v[86:87], v[30:31], v[12:13] op_sel_hi:[0,1]
	v_exp_f32_e32 v86, v86
	v_exp_f32_e32 v87, v87
	v_pk_mul_f32 v[72:73], v[72:73], v[122:123]
	v_pk_fma_f32 v[70:71], s[74:75], v[120:121], v[70:71]
	v_pk_fma_f32 v[122:123], v[34:35], s[40:41], v[72:73] op_sel_hi:[0, 1, 1]
	v_pk_mul_f32 v[72:73], v[86:87], v[110:111]
	v_pk_mul_f32 v[74:75], v[30:31], v[8:9] op_sel_hi:[0,1]
	v_pk_fma_f32 v[110:111], v[34:35], s[42:43], v[72:73] op_sel_hi:[0, 1, 1]
	v_pk_mul_f32 v[72:73], v[30:31], v[6:7] op_sel_hi:[0,1]
	v_exp_f32_e32 v72, v72
	v_exp_f32_e32 v73, v73
	v_exp_f32_e32 v74, v74
	v_exp_f32_e32 v75, v75
	v_pk_fma_f32 v[70:71], s[76:77], v[122:123], v[70:71]
	v_pk_mul_f32 v[72:73], v[72:73], v[112:113]
	v_pk_fma_f32 v[70:71], s[78:79], v[110:111], v[70:71]
	v_pk_fma_f32 v[112:113], v[34:35], s[44:45], v[72:73] op_sel_hi:[0, 1, 1]
	v_pk_mul_f32 v[72:73], v[74:75], v[114:115]
	v_pk_fma_f32 v[70:71], s[80:81], v[112:113], v[70:71]
	v_pk_fma_f32 v[114:115], v[34:35], s[46:47], v[72:73] op_sel_hi:[0, 1, 1]
	v_pk_mul_f32 v[72:73], v[30:31], v[2:3] op_sel_hi:[0,1]
	v_exp_f32_e32 v72, v72
	v_exp_f32_e32 v73, v73
	v_pk_mul_f32 v[30:31], v[30:31], v[4:5] op_sel_hi:[0,1]
	v_exp_f32_e32 v30, v30
	v_exp_f32_e32 v31, v31
	v_pk_mul_f32 v[72:73], v[72:73], v[116:117]
	v_pk_fma_f32 v[70:71], s[82:83], v[114:115], v[70:71]
	v_pk_fma_f32 v[116:117], v[34:35], s[48:49], v[72:73] op_sel_hi:[0, 1, 1]
	v_pk_mul_f32 v[30:31], v[30:31], v[118:119]
	v_pk_fma_f32 v[70:71], s[84:85], v[116:117], v[70:71]
	v_pk_fma_f32 v[30:31], v[34:35], s[50:51], v[30:31] op_sel_hi:[0, 1, 1]
	v_pk_fma_f32 v[34:35], s[86:87], v[30:31], v[70:71]
	s_nop 0
	v_add_f32_e32 v34, v34, v35
	v_fma_mix_f32 v34, v1, v32, v34 op_sel_hi:[0,1,0]
	v_fma_mixlo_f16 v34, v34, v36, 0 op_sel_hi:[0,1,0]
	ds_write_b16 v68, v34 offset:24896
	s_waitcnt lgkmcnt(0)
	s_load_dwordx16 s[36:51], s[54:55], 0xb00
	s_load_dwordx16 s[72:87], s[54:55], 0xb40
	v_cvt_f32_f16_sdwa v34, v40 dst_sel:DWORD dst_unused:UNUSED_PAD src0_sel:WORD_1
	v_cvt_f32_f16_sdwa v35, v32 dst_sel:DWORD dst_unused:UNUSED_PAD src0_sel:WORD_1
	v_pk_mul_f32 v[118:119], v[34:35], v[14:15] op_sel_hi:[0,1]
	v_exp_f32_e32 v118, v118
	v_exp_f32_e32 v119, v119
	v_pk_mul_f32 v[124:125], v[34:35], v[16:17] op_sel_hi:[0,1]
	v_exp_f32_e32 v124, v124
	v_exp_f32_e32 v125, v125
	v_mul_f32_e32 v40, v34, v35
	v_pk_mul_f32 v[38:39], v[118:119], v[38:39]
	v_pk_fma_f32 v[38:39], v[40:41], s[56:57], v[38:39] op_sel_hi:[0, 1, 1]
	v_pk_fma_f32 v[42:43], s[88:89], v[38:39], 0 op_sel_hi:[1, 1, 0]
	v_pk_mul_f32 v[58:59], v[124:125], v[120:121]
	s_nop 0
	v_pk_fma_f32 v[118:119], v[40:41], s[58:59], v[58:59] op_sel_hi:[0, 1, 1]
	v_pk_mul_f32 v[44:45], v[34:35], v[10:11] op_sel_hi:[0,1]
	v_exp_f32_e32 v44, v44
	v_exp_f32_e32 v45, v45
	v_pk_mul_f32 v[58:59], v[34:35], v[12:13] op_sel_hi:[0,1]
	v_exp_f32_e32 v58, v58
	v_exp_f32_e32 v59, v59
	v_pk_mul_f32 v[44:45], v[44:45], v[122:123]
	v_pk_fma_f32 v[42:43], s[90:91], v[118:119], v[42:43]
	v_pk_fma_f32 v[120:121], v[40:41], s[60:61], v[44:45] op_sel_hi:[0, 1, 1]
	v_pk_mul_f32 v[44:45], v[58:59], v[110:111]
	v_pk_mul_f32 v[46:47], v[34:35], v[8:9] op_sel_hi:[0,1]
	v_pk_fma_f32 v[110:111], v[40:41], s[62:63], v[44:45] op_sel_hi:[0, 1, 1]
	v_pk_mul_f32 v[44:45], v[34:35], v[6:7] op_sel_hi:[0,1]
	v_exp_f32_e32 v44, v44
	v_exp_f32_e32 v45, v45
	v_exp_f32_e32 v46, v46
	v_exp_f32_e32 v47, v47
	v_pk_fma_f32 v[42:43], s[92:93], v[120:121], v[42:43]
	v_pk_mul_f32 v[44:45], v[44:45], v[112:113]
	v_pk_fma_f32 v[42:43], s[94:95], v[110:111], v[42:43]
	v_pk_fma_f32 v[112:113], v[40:41], s[64:65], v[44:45] op_sel_hi:[0, 1, 1]
	v_pk_mul_f32 v[44:45], v[46:47], v[114:115]
	v_pk_fma_f32 v[42:43], s[96:97], v[112:113], v[42:43]
	v_pk_fma_f32 v[114:115], v[40:41], s[66:67], v[44:45] op_sel_hi:[0, 1, 1]
	v_pk_mul_f32 v[44:45], v[34:35], v[2:3] op_sel_hi:[0,1]
	v_exp_f32_e32 v44, v44
	v_exp_f32_e32 v45, v45
	v_pk_mul_f32 v[34:35], v[34:35], v[4:5] op_sel_hi:[0,1]
	v_exp_f32_e32 v34, v34
	v_exp_f32_e32 v35, v35
	v_pk_mul_f32 v[44:45], v[44:45], v[116:117]
	v_pk_fma_f32 v[42:43], s[98:99], v[114:115], v[42:43]
	v_pk_fma_f32 v[116:117], v[40:41], s[68:69], v[44:45] op_sel_hi:[0, 1, 1]
	v_pk_mul_f32 v[30:31], v[34:35], v[30:31]
	v_pk_fma_f32 v[42:43], s[20:21], v[116:117], v[42:43]
	v_pk_fma_f32 v[30:31], v[40:41], s[70:71], v[30:31] op_sel_hi:[0, 1, 1]
	v_pk_fma_f32 v[34:35], s[22:23], v[30:31], v[42:43]
	s_nop 0
	v_add_f32_e32 v34, v34, v35
	v_fma_mix_f32 v32, v1, v32, v34 op_sel:[0,1,0] op_sel_hi:[0,1,0]
	v_fma_mixlo_f16 v32, v32, v36, 0 op_sel:[0,1,0] op_sel_hi:[0,1,0]
	ds_write_b16 v68, v32 offset:25936
	s_waitcnt lgkmcnt(0)
	s_load_dwordx16 s[56:71], s[54:55], 0xb80
	s_load_dwordx8 s[88:95], s[54:55], 0xbc0
	s_load_dwordx4 s[96:99], s[54:55], 0xbe0
	s_load_dwordx4 s[20:23], s[54:55], 0xbf0
	v_cvt_f32_f16_e32 v32, v41
	v_cvt_f32_f16_e32 v34, v33
	v_pk_mul_f32 v[122:123], v[32:33], v[14:15] op_sel_hi:[0,1]
	v_exp_f32_e32 v122, v122
	v_exp_f32_e32 v123, v123
	v_pk_mul_f32 v[124:125], v[32:33], v[16:17] op_sel_hi:[0,1]
	v_exp_f32_e32 v124, v124
	v_exp_f32_e32 v125, v125
	v_mul_f32_e32 v34, v32, v34
	v_pk_mul_f32 v[38:39], v[122:123], v[38:39]
	v_pk_fma_f32 v[38:39], v[34:35], s[36:37], v[38:39] op_sel_hi:[0, 1, 1]
	v_pk_fma_f32 v[70:71], s[72:73], v[38:39], 0 op_sel_hi:[1, 1, 0]
	v_pk_mul_f32 v[86:87], v[124:125], v[118:119]
	s_nop 0
	v_pk_fma_f32 v[118:119], v[34:35], s[38:39], v[86:87] op_sel_hi:[0, 1, 1]
	v_pk_mul_f32 v[72:73], v[32:33], v[10:11] op_sel_hi:[0,1]
	v_exp_f32_e32 v72, v72
	v_exp_f32_e32 v73, v73
	v_pk_mul_f32 v[86:87], v[32:33], v[12:13] op_sel_hi:[0,1]
	v_exp_f32_e32 v86, v86
	v_exp_f32_e32 v87, v87
	v_pk_mul_f32 v[72:73], v[72:73], v[120:121]
	v_pk_fma_f32 v[70:71], s[74:75], v[118:119], v[70:71]
	v_pk_fma_f32 v[120:121], v[34:35], s[40:41], v[72:73] op_sel_hi:[0, 1, 1]
	v_pk_mul_f32 v[72:73], v[86:87], v[110:111]
	v_pk_mul_f32 v[74:75], v[32:33], v[8:9] op_sel_hi:[0,1]
	v_pk_fma_f32 v[110:111], v[34:35], s[42:43], v[72:73] op_sel_hi:[0, 1, 1]
	v_pk_mul_f32 v[72:73], v[32:33], v[6:7] op_sel_hi:[0,1]
	v_exp_f32_e32 v72, v72
	v_exp_f32_e32 v73, v73
	v_exp_f32_e32 v74, v74
	v_exp_f32_e32 v75, v75
	v_pk_fma_f32 v[70:71], s[76:77], v[120:121], v[70:71]
	v_pk_mul_f32 v[72:73], v[72:73], v[112:113]
	v_pk_fma_f32 v[70:71], s[78:79], v[110:111], v[70:71]
	v_pk_fma_f32 v[112:113], v[34:35], s[44:45], v[72:73] op_sel_hi:[0, 1, 1]
	v_pk_mul_f32 v[72:73], v[74:75], v[114:115]
	v_pk_mul_f32 v[74:75], v[32:33], v[4:5] op_sel_hi:[0,1]
	v_pk_fma_f32 v[114:115], v[34:35], s[46:47], v[72:73] op_sel_hi:[0, 1, 1]
	v_pk_mul_f32 v[72:73], v[32:33], v[2:3] op_sel_hi:[0,1]
	v_exp_f32_e32 v72, v72
	v_exp_f32_e32 v73, v73
	v_exp_f32_e32 v74, v74
	v_exp_f32_e32 v75, v75
	v_pk_fma_f32 v[70:71], s[80:81], v[112:113], v[70:71]
	v_pk_mul_f32 v[72:73], v[72:73], v[116:117]
	v_pk_fma_f32 v[70:71], s[82:83], v[114:115], v[70:71]
	v_pk_fma_f32 v[116:117], v[34:35], s[48:49], v[72:73] op_sel_hi:[0, 1, 1]
	v_pk_mul_f32 v[30:31], v[74:75], v[30:31]
	v_pk_fma_f32 v[70:71], s[84:85], v[116:117], v[70:71]
	v_pk_fma_f32 v[30:31], v[34:35], s[50:51], v[30:31] op_sel_hi:[0, 1, 1]
	v_pk_fma_f32 v[34:35], s[86:87], v[30:31], v[70:71]
	s_nop 0
	v_add_f32_e32 v32, v34, v35
	v_fma_mix_f32 v32, v1, v33, v32 op_sel_hi:[0,1,0]
	v_fma_mixlo_f16 v32, v32, v37, 0 op_sel_hi:[0,1,0]
	ds_write_b16 v68, v32 offset:26976
	s_waitcnt lgkmcnt(0)
	s_load_dwordx16 s[36:51], s[54:55], 0xc00
	s_load_dwordx16 s[72:87], s[54:55], 0xc40
	v_cvt_f32_f16_sdwa v32, v41 dst_sel:DWORD dst_unused:UNUSED_PAD src0_sel:WORD_1
	v_cvt_f32_f16_sdwa v34, v33 dst_sel:DWORD dst_unused:UNUSED_PAD src0_sel:WORD_1
	v_pk_mul_f32 v[40:41], v[32:33], v[14:15] op_sel_hi:[0,1]
	v_pk_mul_f32 v[122:123], v[32:33], v[16:17] op_sel_hi:[0,1]
	v_exp_f32_e32 v40, v40
	v_exp_f32_e32 v41, v41
	v_exp_f32_e32 v122, v122
	v_exp_f32_e32 v123, v123
	v_mul_f32_e32 v34, v32, v34
	v_pk_mul_f32 v[38:39], v[40:41], v[38:39]
	v_pk_mul_f32 v[40:41], v[122:123], v[118:119]
	v_pk_fma_f32 v[118:119], v[34:35], s[58:59], v[40:41] op_sel_hi:[0, 1, 1]
	v_pk_mul_f32 v[40:41], v[32:33], v[10:11] op_sel_hi:[0,1]
	v_pk_fma_f32 v[124:125], v[34:35], s[56:57], v[38:39] op_sel_hi:[0, 1, 1]
	v_exp_f32_e32 v40, v40
	v_exp_f32_e32 v41, v41
	v_pk_mul_f32 v[42:43], v[32:33], v[12:13] op_sel_hi:[0,1]
	v_exp_f32_e32 v42, v42
	v_exp_f32_e32 v43, v43
	v_pk_fma_f32 v[38:39], s[88:89], v[124:125], 0 op_sel_hi:[1, 1, 0]
	v_pk_mul_f32 v[40:41], v[40:41], v[120:121]
	v_pk_fma_f32 v[38:39], s[90:91], v[118:119], v[38:39]
	v_pk_fma_f32 v[120:121], v[34:35], s[60:61], v[40:41] op_sel_hi:[0, 1, 1]
	v_pk_mul_f32 v[40:41], v[42:43], v[110:111]
	v_pk_fma_f32 v[38:39], s[92:93], v[120:121], v[38:39]
	v_pk_fma_f32 v[62:63], v[34:35], s[62:63], v[40:41] op_sel_hi:[0, 1, 1]
	v_pk_mul_f32 v[40:41], v[32:33], v[6:7] op_sel_hi:[0,1]
	v_exp_f32_e32 v40, v40
	v_exp_f32_e32 v41, v41
	v_pk_mul_f32 v[42:43], v[32:33], v[8:9] op_sel_hi:[0,1]
	v_exp_f32_e32 v42, v42
	v_exp_f32_e32 v43, v43
	v_pk_mul_f32 v[40:41], v[40:41], v[112:113]
	v_pk_fma_f32 v[38:39], s[94:95], v[62:63], v[38:39]
	v_pk_fma_f32 v[64:65], v[34:35], s[64:65], v[40:41] op_sel_hi:[0, 1, 1]
	v_pk_mul_f32 v[40:41], v[42:43], v[114:115]
	v_pk_fma_f32 v[38:39], s[96:97], v[64:65], v[38:39]
	v_pk_fma_f32 v[102:103], v[34:35], s[66:67], v[40:41] op_sel_hi:[0, 1, 1]
	v_pk_mul_f32 v[40:41], v[32:33], v[2:3] op_sel_hi:[0,1]
	v_exp_f32_e32 v40, v40
	v_exp_f32_e32 v41, v41
	v_pk_mul_f32 v[42:43], v[32:33], v[4:5] op_sel_hi:[0,1]
	v_exp_f32_e32 v42, v42
	v_exp_f32_e32 v43, v43
	v_pk_mul_f32 v[40:41], v[40:41], v[116:117]
	v_pk_fma_f32 v[38:39], s[98:99], v[102:103], v[38:39]
	v_pk_fma_f32 v[104:105], v[34:35], s[68:69], v[40:41] op_sel_hi:[0, 1, 1]
	v_pk_mul_f32 v[30:31], v[42:43], v[30:31]
	v_pk_fma_f32 v[38:39], s[20:21], v[104:105], v[38:39]
	v_pk_fma_f32 v[106:107], v[34:35], s[70:71], v[30:31] op_sel_hi:[0, 1, 1]
	v_pk_fma_f32 v[30:31], s[22:23], v[106:107], v[38:39]
	s_nop 0
	v_add_f32_e32 v30, v30, v31
	v_fma_mix_f32 v30, v1, v33, v30 op_sel:[0,1,0] op_sel_hi:[0,1,0]
	v_fma_mixlo_f16 v30, v30, v37, 0 op_sel:[0,1,0] op_sel_hi:[0,1,0]
	ds_write_b16 v68, v30 offset:28016
	s_waitcnt lgkmcnt(0)
	s_load_dwordx16 s[56:71], s[54:55], 0xc80
	s_load_dwordx8 s[88:95], s[54:55], 0xcc0
	s_load_dwordx4 s[96:99], s[54:55], 0xce0
	s_load_dwordx4 s[20:23], s[54:55], 0xcf0
	s_waitcnt vmcnt(2)
	v_cvt_f32_f16_e32 v108, v26
	s_waitcnt vmcnt(1)
	v_cvt_f32_f16_e32 v69, v18
	v_pk_mul_f32 v[112:113], v[108:109], v[14:15] op_sel_hi:[0,1]
	v_exp_f32_e32 v112, v112
	v_exp_f32_e32 v113, v113
	v_pk_mul_f32 v[114:115], v[108:109], v[16:17] op_sel_hi:[0,1]
	v_exp_f32_e32 v114, v114
	v_exp_f32_e32 v115, v115
	v_mul_f32_e32 v110, v108, v69
	v_pk_mul_f32 v[112:113], v[112:113], v[124:125]
	v_pk_fma_f32 v[112:113], v[110:111], s[36:37], v[112:113] op_sel_hi:[0, 1, 1]
	v_pk_fma_f32 v[70:71], s[72:73], v[112:113], 0 op_sel_hi:[1, 1, 0]
	v_pk_mul_f32 v[86:87], v[114:115], v[118:119]
	s_nop 0
	v_pk_fma_f32 v[114:115], v[110:111], s[38:39], v[86:87] op_sel_hi:[0, 1, 1]
	v_pk_mul_f32 v[72:73], v[108:109], v[10:11] op_sel_hi:[0,1]
	v_exp_f32_e32 v72, v72
	v_exp_f32_e32 v73, v73
	v_pk_mul_f32 v[86:87], v[108:109], v[12:13] op_sel_hi:[0,1]
	v_exp_f32_e32 v86, v86
	v_exp_f32_e32 v87, v87
	v_pk_mul_f32 v[72:73], v[72:73], v[120:121]
	v_pk_fma_f32 v[70:71], s[74:75], v[114:115], v[70:71]
	v_pk_fma_f32 v[116:117], v[110:111], s[40:41], v[72:73] op_sel_hi:[0, 1, 1]
	v_pk_mul_f32 v[62:63], v[86:87], v[62:63]
	v_pk_fma_f32 v[70:71], s[76:77], v[116:117], v[70:71]
	v_pk_fma_f32 v[118:119], v[110:111], s[42:43], v[62:63] op_sel_hi:[0, 1, 1]
	v_pk_fma_f32 v[62:63], s[78:79], v[118:119], v[70:71]
	v_pk_mul_f32 v[70:71], v[108:109], v[6:7] op_sel_hi:[0,1]
	v_exp_f32_e32 v70, v70
	v_exp_f32_e32 v71, v71
	v_pk_mul_f32 v[72:73], v[108:109], v[8:9] op_sel_hi:[0,1]
	v_exp_f32_e32 v72, v72
	v_exp_f32_e32 v73, v73
	v_pk_mul_f32 v[64:65], v[70:71], v[64:65]
	v_pk_mul_f32 v[70:71], v[108:109], v[4:5] op_sel_hi:[0,1]
	v_pk_fma_f32 v[120:121], v[110:111], s[44:45], v[64:65] op_sel_hi:[0, 1, 1]
	v_pk_mul_f32 v[64:65], v[72:73], v[102:103]
	v_exp_f32_e32 v70, v70
	v_pk_fma_f32 v[102:103], v[110:111], s[46:47], v[64:65] op_sel_hi:[0, 1, 1]
	v_pk_mul_f32 v[64:65], v[108:109], v[2:3] op_sel_hi:[0,1]
	v_exp_f32_e32 v64, v64
	v_exp_f32_e32 v65, v65
	v_exp_f32_e32 v71, v71
	v_pk_fma_f32 v[62:63], s[80:81], v[120:121], v[62:63]
	v_pk_mul_f32 v[64:65], v[64:65], v[104:105]
	v_pk_fma_f32 v[62:63], s[82:83], v[102:103], v[62:63]
	v_pk_fma_f32 v[104:105], v[110:111], s[48:49], v[64:65] op_sel_hi:[0, 1, 1]
	v_pk_mul_f32 v[64:65], v[70:71], v[106:107]
	v_pk_fma_f32 v[62:63], s[84:85], v[104:105], v[62:63]
	v_pk_fma_f32 v[98:99], v[110:111], s[50:51], v[64:65] op_sel_hi:[0, 1, 1]
	v_pk_fma_f32 v[62:63], s[86:87], v[98:99], v[62:63]
	s_nop 0
	v_add_f32_e32 v62, v62, v63
	v_fma_mix_f32 v62, v1, v18, v62 op_sel_hi:[0,1,0]
	s_waitcnt vmcnt(0)
	v_fma_mixlo_f16 v62, v62, v22, 0 op_sel_hi:[0,1,0]
	ds_write_b16 v68, v62 offset:29056
	v_lshrrev_b32_e32 v196, 6, v0
	v_and_b32_e32 v197, 48, v0
	v_lshl_or_b32 v196, v196, 7, v197
	v_and_b32_e32 v197, 15, v0
	v_or_b32_e32 v197, s28, v197
	v_lshl_or_b32 v196, v197, 10, v196
	v_add_u32_e32 v197, 0x4000, v196
	global_load_dwordx4 v[180:183], v196, s[4:5]
	global_load_dwordx4 v[184:187], v196, s[4:5] offset:64
	global_load_dwordx4 v[188:191], v197, s[4:5]
	global_load_dwordx4 v[192:195], v197, s[4:5] offset:64
	v_and_b32_e32 v196, 63, v0
	v_lshlrev_b32_e32 v196, 4, v196
	global_load_dwordx4 v[204:207], v196, s[6:7]
	global_load_dwordx4 v[208:211], v196, s[8:9]
	s_waitcnt lgkmcnt(0)
	s_load_dwordx16 s[36:51], s[54:55], 0xd00
	s_load_dwordx16 s[72:87], s[54:55], 0xd40
	v_cvt_f32_f16_sdwa v26, v26 dst_sel:DWORD dst_unused:UNUSED_PAD src0_sel:WORD_1
	v_cvt_f32_f16_sdwa v69, v18 dst_sel:DWORD dst_unused:UNUSED_PAD src0_sel:WORD_1
	v_pk_mul_f32 v[106:107], v[26:27], v[14:15] op_sel_hi:[0,1]
	v_exp_f32_e32 v106, v106
	v_exp_f32_e32 v107, v107
	v_pk_mul_f32 v[108:109], v[26:27], v[16:17] op_sel_hi:[0,1]
	v_exp_f32_e32 v108, v108
	v_exp_f32_e32 v109, v109
	v_mul_f32_e32 v100, v26, v69
	v_pk_mul_f32 v[106:107], v[106:107], v[112:113]
	v_pk_fma_f32 v[106:107], v[100:101], s[56:57], v[106:107] op_sel_hi:[0, 1, 1]
	v_pk_fma_f32 v[30:31], s[88:89], v[106:107], 0 op_sel_hi:[1, 1, 0]
	v_pk_mul_f32 v[46:47], v[108:109], v[114:115]
	s_nop 0
	v_pk_fma_f32 v[108:109], v[100:101], s[58:59], v[46:47] op_sel_hi:[0, 1, 1]
	v_pk_mul_f32 v[32:33], v[26:27], v[10:11] op_sel_hi:[0,1]
	v_exp_f32_e32 v32, v32
	v_exp_f32_e32 v33, v33
	v_pk_mul_f32 v[46:47], v[26:27], v[12:13] op_sel_hi:[0,1]
	v_exp_f32_e32 v46, v46
	v_exp_f32_e32 v47, v47
	v_pk_mul_f32 v[32:33], v[32:33], v[116:117]
	v_pk_fma_f32 v[30:31], s[90:91], v[108:109], v[30:31]
	v_pk_fma_f32 v[110:111], v[100:101], s[60:61], v[32:33] op_sel_hi:[0, 1, 1]
	v_pk_mul_f32 v[32:33], v[46:47], v[118:119]
	v_pk_mul_f32 v[34:35], v[26:27], v[8:9] op_sel_hi:[0,1]
	v_pk_fma_f32 v[112:113], v[100:101], s[62:63], v[32:33] op_sel_hi:[0, 1, 1]
	v_pk_mul_f32 v[32:33], v[26:27], v[6:7] op_sel_hi:[0,1]
	v_exp_f32_e32 v32, v32
	v_exp_f32_e32 v33, v33
	v_exp_f32_e32 v34, v34
	v_exp_f32_e32 v35, v35
	v_pk_fma_f32 v[30:31], s[92:93], v[110:111], v[30:31]
	v_pk_mul_f32 v[32:33], v[32:33], v[120:121]
	v_pk_fma_f32 v[30:31], s[94:95], v[112:113], v[30:31]
	v_pk_fma_f32 v[114:115], v[100:101], s[64:65], v[32:33] op_sel_hi:[0, 1, 1]
	v_pk_mul_f32 v[32:33], v[34:35], v[102:103]
	v_pk_mul_f32 v[34:35], v[26:27], v[4:5] op_sel_hi:[0,1]
	v_pk_fma_f32 v[102:103], v[100:101], s[66:67], v[32:33] op_sel_hi:[0, 1, 1]
	v_pk_mul_f32 v[32:33], v[26:27], v[2:3] op_sel_hi:[0,1]
	v_exp_f32_e32 v32, v32
	v_exp_f32_e32 v33, v33
	v_exp_f32_e32 v34, v34
	v_exp_f32_e32 v35, v35
	v_pk_fma_f32 v[30:31], s[96:97], v[114:115], v[30:31]
	v_pk_mul_f32 v[32:33], v[32:33], v[104:105]
	v_pk_fma_f32 v[30:31], s[98:99], v[102:103], v[30:31]
	v_pk_fma_f32 v[104:105], v[100:101], s[68:69], v[32:33] op_sel_hi:[0, 1, 1]
	v_pk_mul_f32 v[32:33], v[34:35], v[98:99]
	v_pk_fma_f32 v[30:31], s[20:21], v[104:105], v[30:31]
	v_pk_fma_f32 v[98:99], v[100:101], s[70:71], v[32:33] op_sel_hi:[0, 1, 1]
	v_pk_fma_f32 v[30:31], s[22:23], v[98:99], v[30:31]
	s_nop 0
	v_add_f32_e32 v26, v30, v31
	v_fma_mix_f32 v18, v1, v18, v26 op_sel:[0,1,0] op_sel_hi:[0,1,0]
	v_fma_mixlo_f16 v18, v18, v22, 0 op_sel:[0,1,0] op_sel_hi:[0,1,0]
	ds_write_b16 v68, v18 offset:30096
	s_waitcnt lgkmcnt(0)
	s_load_dwordx16 s[56:71], s[54:55], 0xd80
	s_load_dwordx8 s[88:95], s[54:55], 0xdc0
	s_load_dwordx4 s[96:99], s[54:55], 0xde0
	s_load_dwordx4 s[20:23], s[54:55], 0xdf0
	v_cvt_f32_f16_e32 v18, v27
	v_cvt_f32_f16_e32 v22, v19
	v_pk_mul_f32 v[100:101], v[18:19], v[14:15] op_sel_hi:[0,1]
	v_exp_f32_e32 v100, v100
	v_exp_f32_e32 v101, v101
	v_pk_mul_f32 v[116:117], v[18:19], v[16:17] op_sel_hi:[0,1]
	v_exp_f32_e32 v116, v116
	v_exp_f32_e32 v117, v117
	v_mul_f32_e32 v22, v18, v22
	v_pk_mul_f32 v[100:101], v[100:101], v[106:107]
	v_pk_fma_f32 v[100:101], v[22:23], s[36:37], v[100:101] op_sel_hi:[0, 1, 1]
	v_pk_fma_f32 v[62:63], s[72:73], v[100:101], 0 op_sel_hi:[1, 1, 0]
	v_pk_mul_f32 v[82:83], v[116:117], v[108:109]
	s_nop 0
	v_pk_fma_f32 v[106:107], v[22:23], s[38:39], v[82:83] op_sel_hi:[0, 1, 1]
	v_pk_mul_f32 v[64:65], v[18:19], v[10:11] op_sel_hi:[0,1]
	v_exp_f32_e32 v64, v64
	v_exp_f32_e32 v65, v65
	v_pk_mul_f32 v[82:83], v[18:19], v[12:13] op_sel_hi:[0,1]
	v_exp_f32_e32 v82, v82
	v_exp_f32_e32 v83, v83
	v_pk_mul_f32 v[64:65], v[64:65], v[110:111]
	v_pk_fma_f32 v[62:63], s[74:75], v[106:107], v[62:63]
	v_pk_fma_f32 v[108:109], v[22:23], s[40:41], v[64:65] op_sel_hi:[0, 1, 1]
	v_pk_mul_f32 v[64:65], v[82:83], v[112:113]
	v_pk_mul_f32 v[70:71], v[18:19], v[8:9] op_sel_hi:[0,1]
	v_pk_fma_f32 v[110:111], v[22:23], s[42:43], v[64:65] op_sel_hi:[0, 1, 1]
	v_pk_mul_f32 v[64:65], v[18:19], v[6:7] op_sel_hi:[0,1]
	v_exp_f32_e32 v64, v64
	v_exp_f32_e32 v65, v65
	v_exp_f32_e32 v70, v70
	v_exp_f32_e32 v71, v71
	v_pk_fma_f32 v[62:63], s[76:77], v[108:109], v[62:63]
	v_pk_mul_f32 v[64:65], v[64:65], v[114:115]
	v_pk_fma_f32 v[62:63], s[78:79], v[110:111], v[62:63]
	v_pk_fma_f32 v[112:113], v[22:23], s[44:45], v[64:65] op_sel_hi:[0, 1, 1]
	v_pk_mul_f32 v[64:65], v[70:71], v[102:103]
	v_pk_mul_f32 v[70:71], v[18:19], v[4:5] op_sel_hi:[0,1]
	v_pk_fma_f32 v[102:103], v[22:23], s[46:47], v[64:65] op_sel_hi:[0, 1, 1]
	v_pk_mul_f32 v[64:65], v[18:19], v[2:3] op_sel_hi:[0,1]
	v_exp_f32_e32 v64, v64
	v_exp_f32_e32 v65, v65
	v_exp_f32_e32 v70, v70
	v_exp_f32_e32 v71, v71
	v_pk_fma_f32 v[62:63], s[80:81], v[112:113], v[62:63]
	v_pk_mul_f32 v[64:65], v[64:65], v[104:105]
	v_pk_fma_f32 v[62:63], s[82:83], v[102:103], v[62:63]
	v_pk_fma_f32 v[104:105], v[22:23], s[48:49], v[64:65] op_sel_hi:[0, 1, 1]
	v_pk_mul_f32 v[64:65], v[70:71], v[98:99]
	v_pk_fma_f32 v[62:63], s[84:85], v[104:105], v[62:63]
	v_pk_fma_f32 v[98:99], v[22:23], s[50:51], v[64:65] op_sel_hi:[0, 1, 1]
	v_pk_fma_f32 v[62:63], s[86:87], v[98:99], v[62:63]
	s_nop 0
	v_add_f32_e32 v18, v62, v63
	v_fma_mix_f32 v18, v1, v19, v18 op_sel_hi:[0,1,0]
	v_fma_mixlo_f16 v18, v18, v23, 0 op_sel_hi:[0,1,0]
	ds_write_b16 v68, v18 offset:31136
	s_waitcnt lgkmcnt(0)
	s_load_dwordx16 s[36:51], s[54:55], 0xe00
	s_load_dwordx16 s[72:87], s[54:55], 0xe40
	v_cvt_f32_f16_sdwa v18, v27 dst_sel:DWORD dst_unused:UNUSED_PAD src0_sel:WORD_1
	v_cvt_f32_f16_sdwa v22, v19 dst_sel:DWORD dst_unused:UNUSED_PAD src0_sel:WORD_1
	v_pk_mul_f32 v[26:27], v[18:19], v[14:15] op_sel_hi:[0,1]
	v_exp_f32_e32 v26, v26
	v_exp_f32_e32 v27, v27
	v_pk_mul_f32 v[114:115], v[18:19], v[16:17] op_sel_hi:[0,1]
	v_exp_f32_e32 v114, v114
	v_exp_f32_e32 v115, v115
	v_mul_f32_e32 v22, v18, v22
	v_pk_mul_f32 v[26:27], v[26:27], v[100:101]
	v_pk_fma_f32 v[26:27], v[22:23], s[56:57], v[26:27] op_sel_hi:[0, 1, 1]
	v_pk_fma_f32 v[30:31], s[88:89], v[26:27], 0 op_sel_hi:[1, 1, 0]
	v_pk_mul_f32 v[46:47], v[114:115], v[106:107]
	s_nop 0
	v_pk_fma_f32 v[100:101], v[22:23], s[58:59], v[46:47] op_sel_hi:[0, 1, 1]
	v_pk_mul_f32 v[32:33], v[18:19], v[10:11] op_sel_hi:[0,1]
	v_exp_f32_e32 v32, v32
	v_exp_f32_e32 v33, v33
	v_pk_mul_f32 v[46:47], v[18:19], v[12:13] op_sel_hi:[0,1]
	v_exp_f32_e32 v46, v46
	v_exp_f32_e32 v47, v47
	v_pk_mul_f32 v[32:33], v[32:33], v[108:109]
	v_pk_fma_f32 v[30:31], s[90:91], v[100:101], v[30:31]
	v_pk_fma_f32 v[106:107], v[22:23], s[60:61], v[32:33] op_sel_hi:[0, 1, 1]
	v_pk_mul_f32 v[32:33], v[46:47], v[110:111]
	v_pk_mul_f32 v[34:35], v[18:19], v[8:9] op_sel_hi:[0,1]
	v_pk_fma_f32 v[108:109], v[22:23], s[62:63], v[32:33] op_sel_hi:[0, 1, 1]
	v_pk_mul_f32 v[32:33], v[18:19], v[6:7] op_sel_hi:[0,1]
	v_exp_f32_e32 v32, v32
	v_exp_f32_e32 v33, v33
	v_exp_f32_e32 v34, v34
	v_exp_f32_e32 v35, v35
	v_pk_fma_f32 v[30:31], s[92:93], v[106:107], v[30:31]
	v_pk_mul_f32 v[32:33], v[32:33], v[112:113]
	v_pk_fma_f32 v[30:31], s[94:95], v[108:109], v[30:31]
	v_pk_fma_f32 v[110:111], v[22:23], s[64:65], v[32:33] op_sel_hi:[0, 1, 1]
	v_pk_mul_f32 v[32:33], v[34:35], v[102:103]
	v_pk_mul_f32 v[34:35], v[18:19], v[4:5] op_sel_hi:[0,1]
	v_pk_fma_f32 v[102:103], v[22:23], s[66:67], v[32:33] op_sel_hi:[0, 1, 1]
	v_pk_mul_f32 v[32:33], v[18:19], v[2:3] op_sel_hi:[0,1]
	v_exp_f32_e32 v32, v32
	v_exp_f32_e32 v33, v33
	v_exp_f32_e32 v34, v34
	v_exp_f32_e32 v35, v35
	v_pk_fma_f32 v[30:31], s[96:97], v[110:111], v[30:31]
	v_pk_mul_f32 v[32:33], v[32:33], v[104:105]
	v_pk_fma_f32 v[30:31], s[98:99], v[102:103], v[30:31]
	v_pk_fma_f32 v[104:105], v[22:23], s[68:69], v[32:33] op_sel_hi:[0, 1, 1]
	v_pk_mul_f32 v[32:33], v[34:35], v[98:99]
	v_pk_fma_f32 v[30:31], s[20:21], v[104:105], v[30:31]
	v_pk_fma_f32 v[98:99], v[22:23], s[70:71], v[32:33] op_sel_hi:[0, 1, 1]
	v_pk_fma_f32 v[30:31], s[22:23], v[98:99], v[30:31]
	s_nop 0
	v_add_f32_e32 v18, v30, v31
	v_fma_mix_f32 v18, v1, v19, v18 op_sel:[0,1,0] op_sel_hi:[0,1,0]
	v_fma_mixlo_f16 v18, v18, v23, 0 op_sel:[0,1,0] op_sel_hi:[0,1,0]
	ds_write_b16 v68, v18 offset:32176
	s_waitcnt lgkmcnt(0)
	s_load_dwordx16 s[56:71], s[54:55], 0xe80
	s_load_dwordx8 s[88:95], s[54:55], 0xec0
	s_load_dwordx4 s[96:99], s[54:55], 0xee0
	s_load_dwordx4 s[20:23], s[54:55], 0xef0
	v_cvt_f32_f16_e32 v18, v28
	v_cvt_f32_f16_e32 v19, v20
	v_pk_mul_f32 v[112:113], v[18:19], v[14:15] op_sel_hi:[0,1]
	v_exp_f32_e32 v112, v112
	v_exp_f32_e32 v113, v113
	v_pk_mul_f32 v[114:115], v[18:19], v[16:17] op_sel_hi:[0,1]
	v_exp_f32_e32 v114, v114
	v_exp_f32_e32 v115, v115
	v_mul_f32_e32 v22, v18, v19
	v_pk_mul_f32 v[26:27], v[112:113], v[26:27]
	v_pk_fma_f32 v[26:27], v[22:23], s[36:37], v[26:27] op_sel_hi:[0, 1, 1]
	v_pk_fma_f32 v[62:63], s[72:73], v[26:27], 0 op_sel_hi:[1, 1, 0]
	v_pk_mul_f32 v[82:83], v[114:115], v[100:101]
	s_nop 0
	v_pk_fma_f32 v[100:101], v[22:23], s[38:39], v[82:83] op_sel_hi:[0, 1, 1]
	v_pk_mul_f32 v[64:65], v[18:19], v[10:11] op_sel_hi:[0,1]
	v_exp_f32_e32 v64, v64
	v_exp_f32_e32 v65, v65
	v_pk_mul_f32 v[82:83], v[18:19], v[12:13] op_sel_hi:[0,1]
	v_exp_f32_e32 v82, v82
	v_exp_f32_e32 v83, v83
	v_pk_mul_f32 v[64:65], v[64:65], v[106:107]
	v_pk_fma_f32 v[62:63], s[74:75], v[100:101], v[62:63]
	v_pk_fma_f32 v[106:107], v[22:23], s[40:41], v[64:65] op_sel_hi:[0, 1, 1]
	v_pk_mul_f32 v[64:65], v[82:83], v[108:109]
	v_pk_mul_f32 v[70:71], v[18:19], v[8:9] op_sel_hi:[0,1]
	v_pk_fma_f32 v[108:109], v[22:23], s[42:43], v[64:65] op_sel_hi:[0, 1, 1]
	v_pk_mul_f32 v[64:65], v[18:19], v[6:7] op_sel_hi:[0,1]
	v_exp_f32_e32 v64, v64
	v_exp_f32_e32 v65, v65
	v_exp_f32_e32 v70, v70
	v_exp_f32_e32 v71, v71
	v_pk_fma_f32 v[62:63], s[76:77], v[106:107], v[62:63]
	v_pk_mul_f32 v[64:65], v[64:65], v[110:111]
	v_pk_fma_f32 v[62:63], s[78:79], v[108:109], v[62:63]
	v_pk_fma_f32 v[110:111], v[22:23], s[44:45], v[64:65] op_sel_hi:[0, 1, 1]
	v_pk_mul_f32 v[64:65], v[70:71], v[102:103]
	v_pk_fma_f32 v[62:63], s[80:81], v[110:111], v[62:63]
	v_pk_fma_f32 v[102:103], v[22:23], s[46:47], v[64:65] op_sel_hi:[0, 1, 1]
	v_pk_mul_f32 v[64:65], v[18:19], v[2:3] op_sel_hi:[0,1]
	v_exp_f32_e32 v64, v64
	v_exp_f32_e32 v65, v65
	v_pk_mul_f32 v[18:19], v[18:19], v[4:5] op_sel_hi:[0,1]
	v_exp_f32_e32 v18, v18
	v_exp_f32_e32 v19, v19
	v_pk_mul_f32 v[64:65], v[64:65], v[104:105]
	v_pk_fma_f32 v[62:63], s[82:83], v[102:103], v[62:63]
	v_pk_fma_f32 v[104:105], v[22:23], s[48:49], v[64:65] op_sel_hi:[0, 1, 1]
	v_pk_mul_f32 v[18:19], v[18:19], v[98:99]
	v_pk_fma_f32 v[62:63], s[84:85], v[104:105], v[62:63]
	v_pk_fma_f32 v[18:19], v[22:23], s[50:51], v[18:19] op_sel_hi:[0, 1, 1]
	v_pk_fma_f32 v[22:23], s[86:87], v[18:19], v[62:63]
	s_nop 0
	v_add_f32_e32 v22, v22, v23
	v_fma_mix_f32 v22, v1, v20, v22 op_sel_hi:[0,1,0]
	v_fma_mixlo_f16 v22, v22, v24, 0 op_sel_hi:[0,1,0]
	ds_write_b16 v68, v22 offset:33216
	s_waitcnt lgkmcnt(0)
	s_load_dwordx16 s[36:51], s[54:55], 0xf00
	s_load_dwordx16 s[72:87], s[54:55], 0xf40
	v_cvt_f32_f16_sdwa v22, v28 dst_sel:DWORD dst_unused:UNUSED_PAD src0_sel:WORD_1
	v_cvt_f32_f16_sdwa v23, v20 dst_sel:DWORD dst_unused:UNUSED_PAD src0_sel:WORD_1
	v_pk_mul_f32 v[98:99], v[22:23], v[14:15] op_sel_hi:[0,1]
	v_exp_f32_e32 v98, v98
	v_exp_f32_e32 v99, v99
	v_pk_mul_f32 v[112:113], v[22:23], v[16:17] op_sel_hi:[0,1]
	v_exp_f32_e32 v112, v112
	v_exp_f32_e32 v113, v113
	v_mul_f32_e32 v28, v22, v23
	v_pk_mul_f32 v[26:27], v[98:99], v[26:27]
	v_pk_fma_f32 v[26:27], v[28:29], s[56:57], v[26:27] op_sel_hi:[0, 1, 1]
	v_pk_fma_f32 v[30:31], s[88:89], v[26:27], 0 op_sel_hi:[1, 1, 0]
	v_pk_mul_f32 v[46:47], v[112:113], v[100:101]
	s_nop 0
	v_pk_fma_f32 v[98:99], v[28:29], s[58:59], v[46:47] op_sel_hi:[0, 1, 1]
	v_pk_mul_f32 v[32:33], v[22:23], v[10:11] op_sel_hi:[0,1]
	v_exp_f32_e32 v32, v32
	v_exp_f32_e32 v33, v33
	v_pk_mul_f32 v[46:47], v[22:23], v[12:13] op_sel_hi:[0,1]
	v_exp_f32_e32 v46, v46
	v_exp_f32_e32 v47, v47
	v_pk_mul_f32 v[32:33], v[32:33], v[106:107]
	v_pk_fma_f32 v[30:31], s[90:91], v[98:99], v[30:31]
	v_pk_fma_f32 v[100:101], v[28:29], s[60:61], v[32:33] op_sel_hi:[0, 1, 1]
	v_pk_mul_f32 v[32:33], v[46:47], v[108:109]
	v_pk_mul_f32 v[34:35], v[22:23], v[8:9] op_sel_hi:[0,1]
	v_pk_fma_f32 v[106:107], v[28:29], s[62:63], v[32:33] op_sel_hi:[0, 1, 1]
	v_pk_mul_f32 v[32:33], v[22:23], v[6:7] op_sel_hi:[0,1]
	v_exp_f32_e32 v32, v32
	v_exp_f32_e32 v33, v33
	v_exp_f32_e32 v34, v34
	v_exp_f32_e32 v35, v35
	v_pk_fma_f32 v[30:31], s[92:93], v[100:101], v[30:31]
	v_pk_mul_f32 v[32:33], v[32:33], v[110:111]
	v_pk_fma_f32 v[30:31], s[94:95], v[106:107], v[30:31]
	v_pk_fma_f32 v[108:109], v[28:29], s[64:65], v[32:33] op_sel_hi:[0, 1, 1]
	v_pk_mul_f32 v[32:33], v[34:35], v[102:103]
	v_pk_fma_f32 v[30:31], s[96:97], v[108:109], v[30:31]
	v_pk_fma_f32 v[102:103], v[28:29], s[66:67], v[32:33] op_sel_hi:[0, 1, 1]
	v_pk_mul_f32 v[32:33], v[22:23], v[2:3] op_sel_hi:[0,1]
	v_exp_f32_e32 v32, v32
	v_exp_f32_e32 v33, v33
	v_pk_mul_f32 v[22:23], v[22:23], v[4:5] op_sel_hi:[0,1]
	v_exp_f32_e32 v22, v22
	v_exp_f32_e32 v23, v23
	v_pk_mul_f32 v[32:33], v[32:33], v[104:105]
	v_pk_fma_f32 v[30:31], s[98:99], v[102:103], v[30:31]
	v_pk_fma_f32 v[104:105], v[28:29], s[68:69], v[32:33] op_sel_hi:[0, 1, 1]
	v_pk_mul_f32 v[18:19], v[22:23], v[18:19]
	v_pk_fma_f32 v[30:31], s[20:21], v[104:105], v[30:31]
	v_pk_fma_f32 v[18:19], v[28:29], s[70:71], v[18:19] op_sel_hi:[0, 1, 1]
	v_pk_fma_f32 v[22:23], s[22:23], v[18:19], v[30:31]
	s_nop 0
	v_add_f32_e32 v22, v22, v23
	v_fma_mix_f32 v20, v1, v20, v22 op_sel:[0,1,0] op_sel_hi:[0,1,0]
	v_fma_mixlo_f16 v20, v20, v24, 0 op_sel:[0,1,0] op_sel_hi:[0,1,0]
	ds_write_b16 v68, v20 offset:34256
	s_waitcnt lgkmcnt(0)
	s_load_dwordx16 s[56:71], s[54:55], 0xf80
	s_load_dwordx8 s[88:95], s[54:55], 0xfc0
	s_load_dwordx4 s[96:99], s[54:55], 0xfe0
	s_load_dwordx4 s[20:23], s[54:55], 0xff0
	v_cvt_f32_f16_e32 v20, v29
	v_cvt_f32_f16_e32 v22, v21
	v_pk_mul_f32 v[110:111], v[20:21], v[14:15] op_sel_hi:[0,1]
	v_exp_f32_e32 v110, v110
	v_exp_f32_e32 v111, v111
	v_pk_mul_f32 v[112:113], v[20:21], v[16:17] op_sel_hi:[0,1]
	v_exp_f32_e32 v112, v112
	v_exp_f32_e32 v113, v113
	v_mul_f32_e32 v22, v20, v22
	v_pk_mul_f32 v[26:27], v[110:111], v[26:27]
	v_pk_fma_f32 v[26:27], v[22:23], s[36:37], v[26:27] op_sel_hi:[0, 1, 1]
	v_pk_fma_f32 v[62:63], s[72:73], v[26:27], 0 op_sel_hi:[1, 1, 0]
	v_pk_mul_f32 v[82:83], v[112:113], v[98:99]
	s_nop 0
	v_pk_fma_f32 v[64:65], v[22:23], s[38:39], v[82:83] op_sel_hi:[0, 1, 1]
	v_pk_mul_f32 v[82:83], v[20:21], v[10:11] op_sel_hi:[0,1]
	v_pk_fma_f32 v[62:63], s[74:75], v[64:65], v[62:63]
	v_exp_f32_e32 v82, v82
	v_exp_f32_e32 v83, v83
	v_pk_mul_f32 v[84:85], v[20:21], v[12:13] op_sel_hi:[0,1]
	v_exp_f32_e32 v84, v84
	v_exp_f32_e32 v85, v85
	v_pk_mul_f32 v[82:83], v[82:83], v[100:101]
	s_nop 0
	v_pk_fma_f32 v[70:71], v[22:23], s[40:41], v[82:83] op_sel_hi:[0, 1, 1]
	v_pk_mul_f32 v[82:83], v[84:85], v[106:107]
	v_pk_mul_f32 v[84:85], v[20:21], v[8:9] op_sel_hi:[0,1]
	v_pk_fma_f32 v[72:73], v[22:23], s[42:43], v[82:83] op_sel_hi:[0, 1, 1]
	v_pk_mul_f32 v[82:83], v[20:21], v[6:7] op_sel_hi:[0,1]
	v_exp_f32_e32 v82, v82
	v_exp_f32_e32 v83, v83
	v_exp_f32_e32 v84, v84
	v_exp_f32_e32 v85, v85
	v_pk_fma_f32 v[62:63], s[76:77], v[70:71], v[62:63]
	v_pk_mul_f32 v[82:83], v[82:83], v[108:109]
	v_pk_fma_f32 v[62:63], s[78:79], v[72:73], v[62:63]
	v_pk_fma_f32 v[74:75], v[22:23], s[44:45], v[82:83] op_sel_hi:[0, 1, 1]
	v_pk_mul_f32 v[82:83], v[84:85], v[102:103]
	v_pk_mul_f32 v[84:85], v[20:21], v[4:5] op_sel_hi:[0,1]
	v_pk_fma_f32 v[76:77], v[22:23], s[46:47], v[82:83] op_sel_hi:[0, 1, 1]
	v_pk_mul_f32 v[82:83], v[20:21], v[2:3] op_sel_hi:[0,1]
	v_exp_f32_e32 v82, v82
	v_exp_f32_e32 v83, v83
	v_exp_f32_e32 v84, v84
	v_exp_f32_e32 v85, v85
	v_pk_fma_f32 v[62:63], s[80:81], v[74:75], v[62:63]
	v_pk_mul_f32 v[82:83], v[82:83], v[104:105]
	v_pk_fma_f32 v[62:63], s[82:83], v[76:77], v[62:63]
	v_pk_fma_f32 v[78:79], v[22:23], s[48:49], v[82:83] op_sel_hi:[0, 1, 1]
	v_pk_mul_f32 v[18:19], v[84:85], v[18:19]
	v_pk_fma_f32 v[62:63], s[84:85], v[78:79], v[62:63]
	v_pk_fma_f32 v[18:19], v[22:23], s[50:51], v[18:19] op_sel_hi:[0, 1, 1]
	v_pk_fma_f32 v[22:23], s[86:87], v[18:19], v[62:63]
	s_nop 0
	v_add_f32_e32 v20, v22, v23
	v_fma_mix_f32 v20, v1, v21, v20 op_sel_hi:[0,1,0]
	v_fma_mixlo_f16 v20, v20, v25, 0 op_sel_hi:[0,1,0]
	ds_write_b16 v68, v20 offset:35296
	v_cvt_f32_f16_sdwa v20, v29 dst_sel:DWORD dst_unused:UNUSED_PAD src0_sel:WORD_1
	v_cvt_f32_f16_sdwa v22, v21 dst_sel:DWORD dst_unused:UNUSED_PAD src0_sel:WORD_1
	v_pk_mul_f32 v[14:15], v[20:21], v[14:15] op_sel_hi:[0,1]
	v_exp_f32_e32 v14, v14
	v_exp_f32_e32 v15, v15
	v_pk_mul_f32 v[16:17], v[20:21], v[16:17] op_sel_hi:[0,1]
	v_exp_f32_e32 v16, v16
	v_exp_f32_e32 v17, v17
	v_pk_mul_f32 v[10:11], v[20:21], v[10:11] op_sel_hi:[0,1]
	v_exp_f32_e32 v10, v10
	v_exp_f32_e32 v11, v11
	v_pk_mul_f32 v[12:13], v[20:21], v[12:13] op_sel_hi:[0,1]
	v_exp_f32_e32 v12, v12
	v_exp_f32_e32 v13, v13
	v_pk_mul_f32 v[6:7], v[20:21], v[6:7] op_sel_hi:[0,1]
	v_mul_f32_e32 v22, v20, v22
	v_pk_mul_f32 v[14:15], v[14:15], v[26:27]
	v_exp_f32_e32 v6, v6
	v_exp_f32_e32 v7, v7
	v_pk_mul_f32 v[8:9], v[20:21], v[8:9] op_sel_hi:[0,1]
	v_pk_fma_f32 v[14:15], v[22:23], s[56:57], v[14:15] op_sel_hi:[0, 1, 1]
	v_pk_mul_f32 v[16:17], v[16:17], v[64:65]
	v_exp_f32_e32 v8, v8
	v_exp_f32_e32 v9, v9
	v_pk_mul_f32 v[2:3], v[20:21], v[2:3] op_sel_hi:[0,1]
	v_pk_fma_f32 v[14:15], s[88:89], v[14:15], 0 op_sel_hi:[1, 1, 0]
	v_pk_fma_f32 v[16:17], v[22:23], s[58:59], v[16:17] op_sel_hi:[0, 1, 1]
	v_pk_mul_f32 v[10:11], v[10:11], v[70:71]
	v_exp_f32_e32 v2, v2
	v_exp_f32_e32 v3, v3
	v_pk_mul_f32 v[4:5], v[20:21], v[4:5] op_sel_hi:[0,1]
	v_pk_fma_f32 v[14:15], s[90:91], v[16:17], v[14:15]
	v_pk_fma_f32 v[10:11], v[22:23], s[60:61], v[10:11] op_sel_hi:[0, 1, 1]
	v_pk_mul_f32 v[12:13], v[12:13], v[72:73]
	v_exp_f32_e32 v4, v4
	v_exp_f32_e32 v5, v5
	v_pk_fma_f32 v[10:11], s[92:93], v[10:11], v[14:15]
	v_pk_fma_f32 v[12:13], v[22:23], s[62:63], v[12:13] op_sel_hi:[0, 1, 1]
	v_pk_mul_f32 v[6:7], v[6:7], v[74:75]
	v_pk_fma_f32 v[10:11], s[94:95], v[12:13], v[10:11]
	v_pk_fma_f32 v[6:7], v[22:23], s[64:65], v[6:7] op_sel_hi:[0, 1, 1]
	v_pk_mul_f32 v[8:9], v[8:9], v[76:77]
	v_pk_fma_f32 v[6:7], s[96:97], v[6:7], v[10:11]
	v_pk_fma_f32 v[8:9], v[22:23], s[66:67], v[8:9] op_sel_hi:[0, 1, 1]
	v_pk_mul_f32 v[2:3], v[2:3], v[78:79]
	v_pk_fma_f32 v[6:7], s[98:99], v[8:9], v[6:7]
	v_pk_fma_f32 v[2:3], v[22:23], s[68:69], v[2:3] op_sel_hi:[0, 1, 1]
	v_pk_mul_f32 v[4:5], v[4:5], v[18:19]
	v_pk_fma_f32 v[2:3], s[20:21], v[2:3], v[6:7]
	v_pk_fma_f32 v[4:5], v[22:23], s[70:71], v[4:5] op_sel_hi:[0, 1, 1]
	v_pk_fma_f32 v[2:3], s[22:23], v[4:5], v[2:3]
	s_nop 0
	v_add_f32_e32 v2, v2, v3
	v_fma_mix_f32 v1, v1, v21, v2 op_sel:[0,1,0] op_sel_hi:[0,1,0]
	v_fma_mixlo_f16 v1, v1, v25, 0 op_sel:[0,1,0] op_sel_hi:[0,1,0]
	ds_write_b16 v68, v1 offset:36336
	v_lshlrev_b32_e32 v1, 9, v0
	v_and_b32_e32 v2, 0x38000, v1
	v_mov_b32_e32 v3, v67
	v_and_b32_e32 v1, 63, v0
	s_bfe_u32 s14, s2, 0x40003
	v_lshl_add_u64 v[2:3], s[18:19], 0, v[2:3]
	v_lshlrev_b32_e32 v58, 4, v1
	v_mov_b32_e32 v59, v67
	s_lshl_b32 s13, s14, 6
	v_lshl_add_u64 v[20:21], v[2:3], 0, v[58:59]
	s_lshl_b32 s26, s14, 10
	s_add_i32 s12, s13, 64
	v_lshl_add_u64 v[2:3], v[20:21], 0, s[26:27]
	s_and_b32 s15, s12, 0x3c0
	v_add_co_u32_e32 v4, vcc, s52, v2
	s_lshl_b32 s26, s15, 4
	s_lshl_b32 s12, s12, 4
	v_addc_co_u32_e32 v5, vcc, 0, v3, vcc
	global_load_dwordx4 v[28:31], v[2:3], off
	global_load_dwordx4 v[32:35], v[4:5], off
	v_lshl_add_u64 v[2:3], v[20:21], 0, s[26:27]
	s_or_b32 s26, s12, 0x4000
	s_add_i32 s12, s13, 0x80
	s_and_b32 s15, s12, 0x3c0
	v_lshl_add_u64 v[4:5], v[20:21], 0, s[26:27]
	s_lshl_b32 s26, s15, 4
	s_lshl_b32 s12, s12, 4
	global_load_dwordx4 v[36:39], v[2:3], off
	global_load_dwordx4 v[40:43], v[4:5], off
	v_lshl_add_u64 v[2:3], v[20:21], 0, s[26:27]
	s_or_b32 s26, s12, 0x4000
	s_add_i32 s12, s13, 0xc0
	s_and_b32 s15, s12, 0x3c0
	v_lshl_add_u64 v[4:5], v[20:21], 0, s[26:27]
	s_lshl_b32 s26, s15, 4
	s_lshl_b32 s12, s12, 4
	global_load_dwordx4 v[44:47], v[2:3], off
	global_load_dwordx4 v[48:51], v[4:5], off
	v_lshl_add_u64 v[2:3], v[20:21], 0, s[26:27]
	s_or_b32 s26, s12, 0x4000
	s_add_i32 s12, s13, 0x100
	s_and_b32 s15, s12, 0x3c0
	v_lshl_add_u64 v[4:5], v[20:21], 0, s[26:27]
	s_lshl_b32 s26, s15, 4
	s_lshl_b32 s12, s12, 4
	global_load_dwordx4 v[52:55], v[2:3], off
	global_load_dwordx4 v[60:63], v[4:5], off
	v_lshl_add_u64 v[2:3], v[20:21], 0, s[26:27]
	s_or_b32 s26, s12, 0x4000
	s_add_i32 s12, s13, 0x140
	s_and_b32 s15, s12, 0x3c0
	v_lshl_add_u64 v[4:5], v[20:21], 0, s[26:27]
	s_lshl_b32 s26, s15, 4
	s_lshl_b32 s12, s12, 4
	global_load_dwordx4 v[68:71], v[2:3], off
	global_load_dwordx4 v[72:75], v[4:5], off
	v_lshl_add_u64 v[2:3], v[20:21], 0, s[26:27]
	s_or_b32 s26, s12, 0x4000
	s_add_i32 s12, s13, 0x180
	s_and_b32 s15, s12, 0x3c0
	v_lshl_add_u64 v[4:5], v[20:21], 0, s[26:27]
	s_lshl_b32 s26, s15, 4
	s_lshl_b32 s12, s12, 4
	global_load_dwordx4 v[76:79], v[2:3], off
	global_load_dwordx4 v[82:85], v[4:5], off
	v_lshl_add_u64 v[2:3], v[20:21], 0, s[26:27]
	s_or_b32 s26, s12, 0x4000
	s_add_i32 s12, s13, 0x1c0
	s_and_b32 s15, s12, 0x3c0
	v_lshl_add_u64 v[4:5], v[20:21], 0, s[26:27]
	s_lshl_b32 s26, s15, 4
	s_lshl_b32 s12, s12, 4
	v_lshl_add_u64 v[18:19], v[20:21], 0, s[26:27]
	s_or_b32 s26, s12, 0x4000
	s_xor_b32 s15, s13, 0x200
	v_lshl_add_u64 v[22:23], v[20:21], 0, s[26:27]
	s_lshl_b32 s26, s15, 4
	global_load_dwordx4 v[14:17], v[2:3], off
	global_load_dwordx4 v[10:13], v[4:5], off
	global_load_dwordx4 v[6:9], v[18:19], off
	s_nop 0
	global_load_dwordx4 v[2:5], v[22:23], off
	v_lshl_add_u64 v[18:19], v[20:21], 0, s[26:27]
	v_add_co_u32_e32 v22, vcc, s52, v18
	s_waitcnt lgkmcnt(0)
	s_barrier
	v_addc_co_u32_e32 v23, vcc, 0, v19, vcc
	global_load_dwordx4 v[86:89], v[18:19], off
	global_load_dwordx4 v[90:93], v[22:23], off
	v_lshrrev_b32_e32 v118, 6, v0
	v_lshlrev_b32_e32 v22, 7, v118
	v_mov_b32_e32 v23, v67
	v_and_b32_e32 v81, 15, v0
	v_lshl_add_u64 v[24:25], s[4:5], 0, v[22:23]
	v_and_b32_e32 v18, 48, v0
	v_mov_b32_e32 v19, v67
	s_movk_i32 s12, 0x410
	v_lshl_add_u64 v[56:57], v[24:25], 0, v[18:19]
	v_mad_u32_u24 v19, v81, s12, v18
	v_add_u32_e32 v23, s13, v19
	ds_read_b128 v[94:97], v23 offset:4096
	ds_read_b128 v[98:101], v23 offset:20736
	v_or_b32_e32 v26, s28, v81
	v_mov_b32_e32 v27, v67
	v_lshlrev_b64 v[24:25], 10, v[26:27]
	v_or_b32_e32 v26, 16, v26
	v_lshlrev_b64 v[26:27], 10, v[26:27]
	v_lshrrev_b32_e32 v23, 1, v0
	v_lshl_add_u64 v[24:25], v[56:57], 0, v[24:25]
	v_lshl_add_u64 v[26:27], v[56:57], 0, v[26:27]
	v_and_b32_e32 v80, 24, v23
	s_lshl_b32 s14, s14, 5
	s_setprio 1
	s_waitcnt vmcnt(17) lgkmcnt(1)
	v_mfma_f32_16x16x32_f16 v[102:105], v[28:31], v[94:97], 0
	s_waitcnt lgkmcnt(0)
	v_mfma_f32_16x16x32_f16 v[28:31], v[28:31], v[98:101], 0
	s_waitcnt vmcnt(16)
	v_mfma_f32_16x16x32_f16 v[94:97], v[32:35], v[94:97], 0
	v_mfma_f32_16x16x32_f16 v[32:35], v[32:35], v[98:101], 0
	s_setprio 0
	s_add_i32 s16, s13, 0x240
	s_and_b32 s17, s16, 0x3c0
	s_lshl_b32 s26, s17, 4
	s_lshl_b32 s16, s16, 4
	v_lshl_add_u64 v[56:57], v[20:21], 0, s[26:27]
	s_or_b32 s26, s16, 0x4000
	v_lshl_add_u64 v[64:65], v[20:21], 0, s[26:27]
	global_load_dwordx4 v[98:101], v[56:57], off
	global_load_dwordx4 v[106:109], v[64:65], off
	s_add_i32 s16, s14, 32
	s_and_b32 s16, s16, 0x1e0
	v_lshl_add_u32 v23, s16, 1, v19
	ds_read_b128 v[110:113], v23 offset:4096
	ds_read_b128 v[114:117], v23 offset:20736
	s_setprio 1
	s_waitcnt vmcnt(17) lgkmcnt(1)
	v_mfma_f32_16x16x32_f16 v[102:105], v[36:39], v[110:113], v[102:105]
	s_waitcnt lgkmcnt(0)
	v_mfma_f32_16x16x32_f16 v[28:31], v[36:39], v[114:117], v[28:31]
	s_waitcnt vmcnt(16)
	v_mfma_f32_16x16x32_f16 v[36:39], v[40:43], v[110:113], v[94:97]
	v_mfma_f32_16x16x32_f16 v[32:35], v[40:43], v[114:117], v[32:35]
	s_setprio 0
	s_add_i32 s16, s13, 0x280
	s_and_b32 s17, s16, 0x3c0
	s_lshl_b32 s26, s17, 4
	s_lshl_b32 s16, s16, 4
	v_lshl_add_u64 v[56:57], v[20:21], 0, s[26:27]
	s_or_b32 s26, s16, 0x4000
	v_lshl_add_u64 v[64:65], v[20:21], 0, s[26:27]
	global_load_dwordx4 v[40:43], v[56:57], off
	global_load_dwordx4 v[94:97], v[64:65], off
	s_add_i32 s16, s14, 64
	s_and_b32 s16, s16, 0x1e0
	v_lshl_add_u32 v23, s16, 1, v19
	ds_read_b128 v[110:113], v23 offset:4096
	ds_read_b128 v[114:117], v23 offset:20736
	s_setprio 1
	s_waitcnt vmcnt(17) lgkmcnt(1)
	v_mfma_f32_16x16x32_f16 v[102:105], v[44:47], v[110:113], v[102:105]
	s_waitcnt lgkmcnt(0)
	v_mfma_f32_16x16x32_f16 v[28:31], v[44:47], v[114:117], v[28:31]
	s_waitcnt vmcnt(16)
	v_mfma_f32_16x16x32_f16 v[36:39], v[48:51], v[110:113], v[36:39]
	v_mfma_f32_16x16x32_f16 v[32:35], v[48:51], v[114:117], v[32:35]
	s_setprio 0
	s_add_i32 s16, s13, 0x2c0
	s_and_b32 s17, s16, 0x3c0
	s_lshl_b32 s26, s17, 4
	s_lshl_b32 s16, s16, 4
	v_lshl_add_u64 v[56:57], v[20:21], 0, s[26:27]
	s_or_b32 s26, s16, 0x4000
	v_lshl_add_u64 v[64:65], v[20:21], 0, s[26:27]
	global_load_dwordx4 v[44:47], v[56:57], off
	global_load_dwordx4 v[48:51], v[64:65], off
	s_add_i32 s16, s14, 0x60
	s_and_b32 s16, s16, 0x1e0
	v_lshl_add_u32 v23, s16, 1, v19
	ds_read_b128 v[110:113], v23 offset:4096
	ds_read_b128 v[114:117], v23 offset:20736
	s_setprio 1
	s_waitcnt vmcnt(17) lgkmcnt(1)
	v_mfma_f32_16x16x32_f16 v[102:105], v[52:55], v[110:113], v[102:105]
	s_waitcnt lgkmcnt(0)
	v_mfma_f32_16x16x32_f16 v[28:31], v[52:55], v[114:117], v[28:31]
	s_waitcnt vmcnt(16)
	v_mfma_f32_16x16x32_f16 v[36:39], v[60:63], v[110:113], v[36:39]
	v_mfma_f32_16x16x32_f16 v[32:35], v[60:63], v[114:117], v[32:35]
	s_setprio 0
	s_add_i32 s16, s13, 0x300
	s_and_b32 s17, s16, 0x3c0
	s_lshl_b32 s26, s17, 4
	s_lshl_b32 s16, s16, 4
	v_lshl_add_u64 v[56:57], v[20:21], 0, s[26:27]
	s_or_b32 s26, s16, 0x4000
	v_lshl_add_u64 v[64:65], v[20:21], 0, s[26:27]
	global_load_dwordx4 v[52:55], v[56:57], off
	global_load_dwordx4 v[60:63], v[64:65], off
	s_add_i32 s16, s14, 0x80
	s_and_b32 s16, s16, 0x1e0
	v_lshl_add_u32 v23, s16, 1, v19
	ds_read_b128 v[110:113], v23 offset:4096
	ds_read_b128 v[114:117], v23 offset:20736
	s_setprio 1
	s_waitcnt vmcnt(17) lgkmcnt(1)
	v_mfma_f32_16x16x32_f16 v[102:105], v[68:71], v[110:113], v[102:105]
	s_waitcnt lgkmcnt(0)
	v_mfma_f32_16x16x32_f16 v[28:31], v[68:71], v[114:117], v[28:31]
	s_waitcnt vmcnt(16)
	v_mfma_f32_16x16x32_f16 v[36:39], v[72:75], v[110:113], v[36:39]
	v_mfma_f32_16x16x32_f16 v[32:35], v[72:75], v[114:117], v[32:35]
	s_setprio 0
	s_add_i32 s16, s13, 0x340
	s_and_b32 s17, s16, 0x3c0
	s_lshl_b32 s26, s17, 4
	s_lshl_b32 s16, s16, 4
	v_lshl_add_u64 v[56:57], v[20:21], 0, s[26:27]
	s_or_b32 s26, s16, 0x4000
	v_lshl_add_u64 v[64:65], v[20:21], 0, s[26:27]
	global_load_dwordx4 v[68:71], v[56:57], off
	global_load_dwordx4 v[72:75], v[64:65], off
	s_add_i32 s16, s14, 0xa0
	s_and_b32 s16, s16, 0x1e0
	v_lshl_add_u32 v23, s16, 1, v19
	ds_read_b128 v[110:113], v23 offset:4096
	ds_read_b128 v[114:117], v23 offset:20736
	s_setprio 1
	s_waitcnt vmcnt(17) lgkmcnt(1)
	v_mfma_f32_16x16x32_f16 v[102:105], v[76:79], v[110:113], v[102:105]
	s_waitcnt lgkmcnt(0)
	v_mfma_f32_16x16x32_f16 v[28:31], v[76:79], v[114:117], v[28:31]
	s_waitcnt vmcnt(16)
	v_mfma_f32_16x16x32_f16 v[36:39], v[82:85], v[110:113], v[36:39]
	v_mfma_f32_16x16x32_f16 v[32:35], v[82:85], v[114:117], v[32:35]
	s_setprio 0
	s_add_i32 s16, s13, 0x380
	s_and_b32 s17, s16, 0x3c0
	s_lshl_b32 s26, s17, 4
	s_lshl_b32 s16, s16, 4
	v_lshl_add_u64 v[56:57], v[20:21], 0, s[26:27]
	s_or_b32 s26, s16, 0x4000
	v_lshl_add_u64 v[64:65], v[20:21], 0, s[26:27]
	global_load_dwordx4 v[76:79], v[56:57], off
	global_load_dwordx4 v[82:85], v[64:65], off
	s_add_i32 s16, s14, 0xc0
	s_and_b32 s16, s16, 0x1e0
	v_lshl_add_u32 v23, s16, 1, v19
	ds_read_b128 v[110:113], v23 offset:4096
	ds_read_b128 v[114:117], v23 offset:20736
	s_setprio 1
	s_waitcnt vmcnt(17) lgkmcnt(1)
	v_mfma_f32_16x16x32_f16 v[102:105], v[14:17], v[110:113], v[102:105]
	s_waitcnt lgkmcnt(0)
	v_mfma_f32_16x16x32_f16 v[14:17], v[14:17], v[114:117], v[28:31]
	s_waitcnt vmcnt(16)
	v_mfma_f32_16x16x32_f16 v[28:31], v[10:13], v[110:113], v[36:39]
	v_mfma_f32_16x16x32_f16 v[10:13], v[10:13], v[114:117], v[32:35]
	s_setprio 0
	s_addk_i32 s13, 0x3c0
	s_and_b32 s16, s13, 0x3c0
	s_lshl_b32 s26, s16, 4
	s_lshl_b32 s13, s13, 4
	v_lshl_add_u64 v[56:57], v[20:21], 0, s[26:27]
	s_or_b32 s26, s13, 0x4000
	v_lshl_add_u64 v[20:21], v[20:21], 0, s[26:27]
	global_load_dwordx4 v[32:35], v[56:57], off
	global_load_dwordx4 v[36:39], v[20:21], off
	s_add_i32 s13, s14, 0xe0
	s_and_b32 s13, s13, 0x1e0
	v_lshl_add_u32 v20, s13, 1, v19
	ds_read_b128 v[110:113], v20 offset:4096
	ds_read_b128 v[114:117], v20 offset:20736
	s_setprio 1
	s_waitcnt vmcnt(17) lgkmcnt(1)
	v_mfma_f32_16x16x32_f16 v[102:105], v[6:9], v[110:113], v[102:105]
	s_waitcnt lgkmcnt(0)
	v_mfma_f32_16x16x32_f16 v[6:9], v[6:9], v[114:117], v[14:17]
	s_waitcnt vmcnt(16)
	v_mfma_f32_16x16x32_f16 v[14:17], v[2:5], v[110:113], v[28:31]
	v_mfma_f32_16x16x32_f16 v[2:5], v[2:5], v[114:117], v[10:13]
	s_setprio 0
	v_add_u32_e32 v20, s15, v19
	s_nop 0
	ds_read_b128 v[10:13], v20 offset:4096
	ds_read_b128 v[28:31], v20 offset:20736
	s_setprio 1
	s_waitcnt vmcnt(15) lgkmcnt(1)
	v_mfma_f32_16x16x32_f16 v[102:105], v[86:89], v[10:13], v[102:105]
	s_waitcnt lgkmcnt(0)
	v_mfma_f32_16x16x32_f16 v[6:9], v[86:89], v[28:31], v[6:9]
	s_waitcnt vmcnt(14)
	v_mfma_f32_16x16x32_f16 v[10:13], v[90:93], v[10:13], v[14:17]
	v_mfma_f32_16x16x32_f16 v[2:5], v[90:93], v[28:31], v[2:5]
	s_setprio 0
	s_add_i32 s13, s14, 0x120
	s_and_b32 s13, s13, 0x1e0
	v_lshl_add_u32 v20, s13, 1, v19
	ds_read_b128 v[14:17], v20 offset:4096
	ds_read_b128 v[28:31], v20 offset:20736
	s_setprio 1
	s_waitcnt vmcnt(13) lgkmcnt(1)
	v_mfma_f32_16x16x32_f16 v[86:89], v[98:101], v[14:17], v[102:105]
	s_waitcnt lgkmcnt(0)
	v_mfma_f32_16x16x32_f16 v[6:9], v[98:101], v[28:31], v[6:9]
	s_waitcnt vmcnt(12)
	v_mfma_f32_16x16x32_f16 v[10:13], v[106:109], v[14:17], v[10:13]
	v_mfma_f32_16x16x32_f16 v[2:5], v[106:109], v[28:31], v[2:5]
	s_setprio 0
	s_add_i32 s13, s14, 0x140
	s_and_b32 s13, s13, 0x1e0
	v_lshl_add_u32 v20, s13, 1, v19
	ds_read_b128 v[14:17], v20 offset:4096
	ds_read_b128 v[28:31], v20 offset:20736
	s_setprio 1
	s_waitcnt vmcnt(11) lgkmcnt(1)
	v_mfma_f32_16x16x32_f16 v[86:89], v[40:43], v[14:17], v[86:89]
	s_waitcnt lgkmcnt(0)
	v_mfma_f32_16x16x32_f16 v[6:9], v[40:43], v[28:31], v[6:9]
	s_waitcnt vmcnt(10)
	v_mfma_f32_16x16x32_f16 v[10:13], v[94:97], v[14:17], v[10:13]
	v_mfma_f32_16x16x32_f16 v[2:5], v[94:97], v[28:31], v[2:5]
	s_setprio 0
	s_add_i32 s13, s14, 0x160
	s_and_b32 s13, s13, 0x1e0
	v_lshl_add_u32 v20, s13, 1, v19
	ds_read_b128 v[14:17], v20 offset:4096
	ds_read_b128 v[28:31], v20 offset:20736
	s_setprio 1
	s_waitcnt vmcnt(9) lgkmcnt(1)
	v_mfma_f32_16x16x32_f16 v[40:43], v[44:47], v[14:17], v[86:89]
	s_waitcnt lgkmcnt(0)
	v_mfma_f32_16x16x32_f16 v[6:9], v[44:47], v[28:31], v[6:9]
	s_waitcnt vmcnt(8)
	v_mfma_f32_16x16x32_f16 v[10:13], v[48:51], v[14:17], v[10:13]
	v_mfma_f32_16x16x32_f16 v[2:5], v[48:51], v[28:31], v[2:5]
	s_setprio 0
	s_add_i32 s13, s14, 0x180
	s_and_b32 s13, s13, 0x1e0
	v_lshl_add_u32 v20, s13, 1, v19
	ds_read_b128 v[14:17], v20 offset:4096
	ds_read_b128 v[28:31], v20 offset:20736
	s_setprio 1
	s_waitcnt vmcnt(7) lgkmcnt(1)
	v_mfma_f32_16x16x32_f16 v[40:43], v[52:55], v[14:17], v[40:43]
	s_waitcnt lgkmcnt(0)
	v_mfma_f32_16x16x32_f16 v[6:9], v[52:55], v[28:31], v[6:9]
	s_waitcnt vmcnt(6)
	v_mfma_f32_16x16x32_f16 v[10:13], v[60:63], v[14:17], v[10:13]
	v_mfma_f32_16x16x32_f16 v[2:5], v[60:63], v[28:31], v[2:5]
	s_setprio 0
	s_add_i32 s13, s14, 0x1a0
	s_and_b32 s13, s13, 0x1e0
	v_lshl_add_u32 v20, s13, 1, v19
	ds_read_b128 v[14:17], v20 offset:4096
	ds_read_b128 v[28:31], v20 offset:20736
	s_setprio 1
	s_waitcnt vmcnt(5) lgkmcnt(1)
	v_mfma_f32_16x16x32_f16 v[40:43], v[68:71], v[14:17], v[40:43]
	s_waitcnt lgkmcnt(0)
	v_mfma_f32_16x16x32_f16 v[6:9], v[68:71], v[28:31], v[6:9]
	s_waitcnt vmcnt(4)
	v_mfma_f32_16x16x32_f16 v[10:13], v[72:75], v[14:17], v[10:13]
	v_mfma_f32_16x16x32_f16 v[2:5], v[72:75], v[28:31], v[2:5]
	s_setprio 0
	s_add_i32 s13, s14, 0x1c0
	s_and_b32 s13, s13, 0x1e0
	v_lshl_add_u32 v20, s13, 1, v19
	ds_read_b128 v[14:17], v20 offset:4096
	ds_read_b128 v[28:31], v20 offset:20736
	s_setprio 1
	s_waitcnt vmcnt(3) lgkmcnt(1)
	v_mfma_f32_16x16x32_f16 v[40:43], v[76:79], v[14:17], v[40:43]
	s_waitcnt lgkmcnt(0)
	v_mfma_f32_16x16x32_f16 v[6:9], v[76:79], v[28:31], v[6:9]
	s_waitcnt vmcnt(2)
	v_mfma_f32_16x16x32_f16 v[10:13], v[82:85], v[14:17], v[10:13]
	v_mfma_f32_16x16x32_f16 v[2:5], v[82:85], v[28:31], v[2:5]
	s_setprio 0
	s_addk_i32 s14, 0x1e0
	s_and_b32 s13, s14, 0x1e0
	v_lshl_add_u32 v20, s13, 1, v19
	ds_read_b128 v[14:17], v20 offset:4096
	ds_read_b128 v[28:31], v20 offset:20736
	s_setprio 1
	s_waitcnt vmcnt(1) lgkmcnt(1)
	v_mfma_f32_16x16x32_f16 v[40:43], v[32:35], v[14:17], v[40:43]
	s_waitcnt lgkmcnt(0)
	v_mfma_f32_16x16x32_f16 v[6:9], v[32:35], v[28:31], v[6:9]
	s_waitcnt vmcnt(0)
	v_mfma_f32_16x16x32_f16 v[10:13], v[36:39], v[14:17], v[10:13]
	v_mfma_f32_16x16x32_f16 v[2:5], v[36:39], v[28:31], v[2:5]
	s_setprio 0
	v_add_u32_e32 v19, v19, v22
	v_lshlrev_b32_e32 v20, 15, v118
	v_mov_b32_e32 v21, v67
	s_bfe_u32 s22, s2, 0x30003
	v_lshl_add_u64 v[20:21], s[10:11], 0, v[20:21]
	s_lshl_b32 s26, s22, 10
	v_lshl_add_u64 v[64:65], v[20:21], 0, v[58:59]
	v_lshl_add_u64 v[52:53], v[64:65], 0, s[26:27]
	v_add_co_u32_e32 v76, vcc, s29, v52
	s_lshl_b32 s53, s22, 6
	s_nop 0
	v_addc_co_u32_e32 v77, vcc, 0, v53, vcc
	s_mov_b32 s14, 0x14000
	v_mov_b32_e32 v22, 0x14000
	v_mul_u32_u24_e32 v23, 0x210, v81
	s_add_i32 s38, s53, 64
	v_lshlrev_b32_e32 v83, 2, v118
	s_movk_i32 s16, 0x1040
	s_movk_i32 s18, 0x840
	v_lshl_or_b32 v1, v1, 3, v22
	v_add3_u32 v84, v23, v18, s14
	s_and_b32 s14, s38, 0x1c0
	s_movk_i32 s20, 0x210
	s_mov_b32 s19, s27
	v_mad_u32_u24 v56, v118, s16, v58
	v_or_b32_e32 v22, 1, v83
	v_mad_u32_u24 v98, v118, s18, v1
	s_lshl_b32 s18, s14, 4
	v_mad_u32_u24 v99, v22, s12, v58
	v_mad_u32_u24 v85, v22, s20, v1
	v_lshl_add_u64 v[54:55], v[64:65], 0, s[18:19]
	s_add_i32 s12, s53, 0xc0
	s_and_b32 s2, s3, 0x7ffffff
	s_lshl_b32 s3, s22, 5
	s_and_b32 s39, s12, 0x1c0
	s_lshl_b32 s14, s39, 4
	s_add_i32 s39, s3, 32
	s_and_b32 s39, s39, 0xe0
	v_lshl_add_u32 v82, s39, 1, v84
	s_add_i32 s11, s53, 0x80
	s_lshl_b32 s16, s38, 4
	s_mov_b32 s21, s27
	s_and_b32 s30, s11, 0x1c0
	s_lshl_b32 s11, s11, 4
	s_or_b32 s20, s16, 0x2000
	s_mov_b32 s23, s27
	s_mov_b32 s31, s27
	s_mov_b32 s35, s27
	s_or_b32 s22, s16, 0x6000
	s_lshl_b32 s30, s30, 4
	s_or_b32 s34, s11, 0x2000
	v_lshl_add_u64 v[26:27], v[64:65], 0, s[20:21]
	v_lshl_add_u64 v[28:29], v[64:65], 0, s[22:23]
	v_lshl_add_u64 v[30:31], v[64:65], 0, s[30:31]
	v_lshl_add_u64 v[32:33], v[64:65], 0, s[34:35]
	s_mov_b64 s[40:41], 0x40000
	v_lshl_add_u64 v[60:61], v[64:65], 0, s[40:41]
	s_mov_b32 s37, s27
	s_or_b32 s36, s11, 0x6000
	v_lshl_add_u64 v[74:75], v[64:65], 0, s[36:37]
	s_mov_b32 s15, s27
	s_lshl_b32 s12, s12, 4
	v_lshl_add_u64 v[70:71], v[64:65], 0, s[14:15]
	s_mov_b32 s17, s27
	s_or_b32 s16, s12, 0x2000
	s_mov_b32 s13, s27
	s_or_b32 s12, s12, 0x6000
	v_lshl_add_u64 v[72:73], v[64:65], 0, s[16:17]
	v_lshl_add_u64 v[68:69], v[64:65], 0, s[12:13]
	v_add_u32_e32 v1, s53, v84
	s_xor_b32 s10, s26, 0x1000
	s_mov_b32 s11, s27
	s_mov_b32 s49, s27
	s_mov_b32 s51, s27
	s_mov_b32 s47, s27
	v_pk_add_f32 v[14:15], v[180:181], v[40:41]
	v_pk_add_f32 v[16:17], v[182:183], v[42:43]
	v_pk_add_f32 v[10:11], v[184:185], v[10:11]
	v_pk_add_f32 v[12:13], v[186:187], v[12:13]
	v_pk_add_f32 v[6:7], v[188:189], v[6:7]
	v_pk_add_f32 v[8:9], v[190:191], v[8:9]
	v_pk_add_f32 v[2:3], v[192:193], v[2:3]
	v_pk_add_f32 v[4:5], v[194:195], v[4:5]
	ds_write_b128 v19, v[14:17] offset:37376
	ds_write_b128 v19, v[10:13] offset:37440
	ds_write_b128 v19, v[6:9] offset:54016
	ds_write_b128 v19, v[2:5] offset:54080
	v_mov_b64_e32 v[34:35], v[204:205]
	v_mov_b64_e32 v[36:37], v[206:207]
	v_mov_b64_e32 v[38:39], v[208:209]
	v_mov_b64_e32 v[40:41], v[210:211]
	v_add_co_u32_e32 v2, vcc, s52, v52
	s_waitcnt lgkmcnt(0)
	s_nop 0
	v_addc_co_u32_e32 v3, vcc, 0, v53, vcc
	v_add_co_u32_e32 v4, vcc, s33, v52
	s_barrier
	s_nop 0
	v_addc_co_u32_e32 v5, vcc, 0, v53, vcc
	global_load_dwordx4 v[14:17], v[2:3], off
	global_load_dwordx4 v[18:21], v[4:5], off
	global_load_dwordx4 v[22:25], v[52:53], off
	global_load_dwordx4 v[10:13], v[54:55], off
	ds_read_b128 v[2:5], v56 offset:37376
	ds_read_b128 v[6:9], v99 offset:37376
	v_add_co_u32_e32 v78, vcc, s52, v54
	s_mov_b32 s43, s27
	s_waitcnt lgkmcnt(1)
	v_add_f32_e32 v42, v2, v3
	v_add_f32_e32 v42, v42, v4
	v_add_f32_e32 v42, v42, v5
	v_addc_co_u32_e32 v79, vcc, 0, v55, vcc
	s_nop 0
	v_add_f32_dpp v42, v42, v42 quad_perm:[1,0,3,2] row_mask:0xf bank_mask:0xf bound_ctrl:1
	s_mov_b32 s45, s27
	s_mov_b32 s41, s27
	v_add_f32_dpp v42, v42, v42 quad_perm:[2,3,0,1] row_mask:0xf bank_mask:0xf bound_ctrl:1
	v_lshl_add_u64 v[62:63], v[64:65], 0, s[10:11]
	v_lshl_add_u64 v[58:59], s[4:5], 0, v[58:59]
	v_add_f32_dpp v42, v42, v42 row_half_mirror row_mask:0xf bank_mask:0xf bound_ctrl:1
	v_lshl_add_u64 v[152:153], v[60:61], 0, s[26:27]
	v_lshl_add_u64 v[154:155], v[60:61], 0, s[18:19]
	v_add_f32_dpp v42, v42, v42 row_mirror row_mask:0xf bank_mask:0xf bound_ctrl:1
	v_lshl_add_u64 v[156:157], v[60:61], 0, s[20:21]
	v_readlane_b32 s8, v42, 16
	v_readlane_b32 s9, v42, 48
	v_readlane_b32 s6, v42, 0
	v_readlane_b32 s7, v42, 32
	v_mov_b32_e32 v42, s8
	v_mov_b32_e32 v43, s9
	v_pk_add_f32 v[42:43], s[6:7], v[42:43]
	s_mov_b32 s6, 0x3b800000
	v_add_f32_e32 v42, v42, v43
	v_mul_f32_e32 v42, 0x3b800000, v42
	v_pk_add_f32 v[86:87], v[2:3], v[42:43] op_sel_hi:[1,0] neg_lo:[0,1] neg_hi:[0,1]
	v_pk_add_f32 v[88:89], v[4:5], v[42:43] op_sel_hi:[1,0] neg_lo:[0,1] neg_hi:[0,1]
	v_pk_mul_f32 v[42:43], v[86:87], v[86:87]
	v_pk_mul_f32 v[44:45], v[88:89], v[88:89]
	v_add_f32_e32 v42, v42, v43
	v_add_f32_e32 v42, v44, v42
	s_waitcnt lgkmcnt(0)
	v_add_f32_e32 v44, v6, v7
	v_add_f32_e32 v42, v45, v42
	v_add_f32_e32 v44, v44, v8
	v_add_f32_e32 v44, v44, v9
	v_add_f32_dpp v42, v42, v42 quad_perm:[1,0,3,2] row_mask:0xf bank_mask:0xf bound_ctrl:1
	v_lshl_add_u64 v[158:159], v[60:61], 0, s[22:23]
	v_add_f32_dpp v44, v44, v44 quad_perm:[1,0,3,2] row_mask:0xf bank_mask:0xf bound_ctrl:1
	v_add_f32_dpp v42, v42, v42 quad_perm:[2,3,0,1] row_mask:0xf bank_mask:0xf bound_ctrl:1
	v_lshl_add_u64 v[160:161], v[60:61], 0, s[30:31]
	v_add_f32_dpp v44, v44, v44 quad_perm:[2,3,0,1] row_mask:0xf bank_mask:0xf bound_ctrl:1
	v_add_f32_dpp v42, v42, v42 row_half_mirror row_mask:0xf bank_mask:0xf bound_ctrl:1
	v_lshl_add_u64 v[162:163], v[60:61], 0, s[34:35]
	v_add_f32_dpp v44, v44, v44 row_half_mirror row_mask:0xf bank_mask:0xf bound_ctrl:1
	v_add_f32_dpp v42, v42, v42 row_mirror row_mask:0xf bank_mask:0xf bound_ctrl:1
	v_lshl_add_u64 v[164:165], v[60:61], 0, s[36:37]
	v_readlane_b32 s7, v42, 16
	v_readlane_b32 s39, v42, 48
	v_add_f32_dpp v44, v44, v44 row_mirror row_mask:0xf bank_mask:0xf bound_ctrl:1
	v_readlane_b32 s8, v42, 0
	v_readlane_b32 s9, v42, 32
	v_mov_b32_e32 v42, s7
	v_mov_b32_e32 v43, s39
	v_readlane_b32 s7, v44, 16
	v_readlane_b32 s39, v44, 48
	v_pk_add_f32 v[42:43], s[8:9], v[42:43]
	v_readlane_b32 s8, v44, 0
	v_readlane_b32 s9, v44, 32
	v_mov_b32_e32 v44, s7
	v_mov_b32_e32 v45, s39
	v_pk_add_f32 v[44:45], s[8:9], v[44:45]
	s_nop 0
	v_add_f32_e32 v44, v44, v45
	v_mul_f32_e32 v44, 0x3b800000, v44
	v_pk_add_f32 v[90:91], v[6:7], v[44:45] op_sel_hi:[1,0] neg_lo:[0,1] neg_hi:[0,1]
	v_pk_add_f32 v[92:93], v[8:9], v[44:45] op_sel_hi:[1,0] neg_lo:[0,1] neg_hi:[0,1]
	v_pk_mul_f32 v[46:47], v[90:91], v[90:91]
	v_pk_mul_f32 v[44:45], v[92:93], v[92:93]
	v_add_f32_e32 v46, v46, v47
	v_add_f32_e32 v44, v44, v46
	v_add_f32_e32 v44, v45, v44
	v_mov_b32_e32 v47, v42
	s_nop 0
	v_add_f32_dpp v44, v44, v44 quad_perm:[1,0,3,2] row_mask:0xf bank_mask:0xf bound_ctrl:1
	s_nop 1
	v_add_f32_dpp v44, v44, v44 quad_perm:[2,3,0,1] row_mask:0xf bank_mask:0xf bound_ctrl:1
	s_nop 1
	v_add_f32_dpp v44, v44, v44 row_half_mirror row_mask:0xf bank_mask:0xf bound_ctrl:1
	s_nop 1
	v_add_f32_dpp v44, v44, v44 row_mirror row_mask:0xf bank_mask:0xf bound_ctrl:1
	s_nop 0
	v_readlane_b32 s7, v44, 16
	v_readlane_b32 s39, v44, 48
	v_readlane_b32 s8, v44, 0
	v_readlane_b32 s9, v44, 32
	v_mov_b32_e32 v44, s7
	v_mov_b32_e32 v45, s39
	v_pk_add_f32 v[44:45], s[8:9], v[44:45]
	s_mov_b32 s8, 0x3727c5ac
	v_mov_b32_e32 v46, v44
	v_mov_b32_e32 v42, v45
	v_pk_add_f32 v[42:43], v[46:47], v[42:43]
	v_mov_b64_e32 v[94:95], s[8:9]
	v_pk_fma_f32 v[96:97], v[42:43], s[6:7], v[94:95] op_sel_hi:[1,0,0]
	s_mov_b32 s7, 0x800000
	v_mul_f32_e32 v42, 0x4b800000, v97
	v_cmp_gt_f32_e32 vcc, s7, v97
	s_nop 1
	v_cndmask_b32_e32 v42, v97, v42, vcc
	v_rsq_f32_e32 v97, v42
	global_load_dwordx4 v[54:57], v[26:27], off
	global_load_dwordx4 v[50:53], v[28:29], off
	global_load_dwordx4 v[46:49], v[30:31], off
	global_load_dwordx4 v[42:45], v[32:33], off
	v_mul_f32_e32 v26, 0x45800000, v97
	v_cndmask_b32_e32 v26, v97, v26, vcc
	v_pk_mul_f32 v[28:29], v[86:87], v[26:27] op_sel_hi:[1,0]
	v_cmp_gt_f32_e32 vcc, s7, v96
	s_waitcnt vmcnt(8)
	v_pk_fma_f32 v[28:29], v[34:35], v[28:29], v[38:39]
	v_pk_mul_f32 v[26:27], v[88:89], v[26:27] op_sel_hi:[1,0]
	v_cvt_pk_f16_f32 v28, v28, v29
	v_mul_f32_e32 v29, 0x4b800000, v96
	v_cndmask_b32_e32 v29, v96, v29, vcc
	v_rsq_f32_e32 v32, v29
	v_pk_fma_f32 v[26:27], v[36:37], v[26:27], v[40:41]
	s_nop 0
	v_cvt_pk_f16_f32 v29, v26, v27
	v_mul_f32_e32 v26, 0x45800000, v32
	v_cndmask_b32_e32 v26, v32, v26, vcc
	ds_write_b64 v98, v[28:29]
	v_pk_mul_f32 v[28:29], v[90:91], v[26:27] op_sel_hi:[1,0]
	v_pk_mul_f32 v[26:27], v[92:93], v[26:27] op_sel_hi:[1,0]
	v_pk_fma_f32 v[28:29], v[34:35], v[28:29], v[38:39]
	v_pk_fma_f32 v[26:27], v[36:37], v[26:27], v[40:41]
	v_cvt_pk_f16_f32 v28, v28, v29
	v_cvt_pk_f16_f32 v29, v26, v27
	ds_write_b64 v85, v[28:29]
	ds_read_b128 v[26:29], v99 offset:38416
	v_add_co_u32_e32 v102, vcc, s52, v30
	s_nop 1
	v_addc_co_u32_e32 v103, vcc, 0, v31, vcc
	ds_read_b128 v[30:33], v99 offset:39456
	s_waitcnt lgkmcnt(1)
	v_add_f32_e32 v86, v26, v27
	v_add_f32_e32 v86, v86, v28
	v_add_f32_e32 v86, v86, v29
	s_nop 1
	v_add_f32_dpp v86, v86, v86 quad_perm:[1,0,3,2] row_mask:0xf bank_mask:0xf bound_ctrl:1
	s_nop 1
	v_add_f32_dpp v86, v86, v86 quad_perm:[2,3,0,1] row_mask:0xf bank_mask:0xf bound_ctrl:1
	s_nop 1
	v_add_f32_dpp v86, v86, v86 row_half_mirror row_mask:0xf bank_mask:0xf bound_ctrl:1
	s_nop 1
	v_add_f32_dpp v86, v86, v86 row_mirror row_mask:0xf bank_mask:0xf bound_ctrl:1
	s_nop 0
	v_readlane_b32 s39, v86, 16
	v_readlane_b32 s40, v86, 48
	v_readlane_b32 s8, v86, 0
	v_readlane_b32 s9, v86, 32
	v_mov_b32_e32 v86, s39
	v_mov_b32_e32 v87, s40
	v_pk_add_f32 v[86:87], s[8:9], v[86:87]
	s_nop 0
	v_add_f32_e32 v86, v86, v87
	v_mul_f32_e32 v86, 0x3b800000, v86
	v_pk_add_f32 v[104:105], v[26:27], v[86:87] op_sel_hi:[1,0] neg_lo:[0,1] neg_hi:[0,1]
	v_pk_add_f32 v[106:107], v[28:29], v[86:87] op_sel_hi:[1,0] neg_lo:[0,1] neg_hi:[0,1]
	v_pk_mul_f32 v[88:89], v[104:105], v[104:105]
	v_pk_mul_f32 v[86:87], v[106:107], v[106:107]
	v_add_f32_e32 v88, v88, v89
	v_add_f32_e32 v86, v86, v88
	s_waitcnt lgkmcnt(0)
	v_add_f32_e32 v88, v30, v31
	v_add_f32_e32 v86, v87, v86
	v_add_f32_e32 v88, v88, v32
	v_add_f32_e32 v88, v88, v33
	v_add_f32_dpp v86, v86, v86 quad_perm:[1,0,3,2] row_mask:0xf bank_mask:0xf bound_ctrl:1
	s_nop 0
	v_add_f32_dpp v88, v88, v88 quad_perm:[1,0,3,2] row_mask:0xf bank_mask:0xf bound_ctrl:1
	v_add_f32_dpp v86, v86, v86 quad_perm:[2,3,0,1] row_mask:0xf bank_mask:0xf bound_ctrl:1
	s_nop 0
	v_add_f32_dpp v88, v88, v88 quad_perm:[2,3,0,1] row_mask:0xf bank_mask:0xf bound_ctrl:1
	v_add_f32_dpp v86, v86, v86 row_half_mirror row_mask:0xf bank_mask:0xf bound_ctrl:1
	s_nop 0
	v_add_f32_dpp v88, v88, v88 row_half_mirror row_mask:0xf bank_mask:0xf bound_ctrl:1
	v_add_f32_dpp v86, v86, v86 row_mirror row_mask:0xf bank_mask:0xf bound_ctrl:1
	s_nop 0
	v_readlane_b32 s39, v86, 16
	v_readlane_b32 s40, v86, 48
	v_add_f32_dpp v88, v88, v88 row_mirror row_mask:0xf bank_mask:0xf bound_ctrl:1
	v_readlane_b32 s8, v86, 0
	v_readlane_b32 s9, v86, 32
	v_mov_b32_e32 v86, s39
	v_mov_b32_e32 v87, s40
	v_readlane_b32 s39, v88, 16
	v_readlane_b32 s40, v88, 48
	v_pk_add_f32 v[86:87], s[8:9], v[86:87]
	v_readlane_b32 s8, v88, 0
	v_readlane_b32 s9, v88, 32
	v_mov_b32_e32 v88, s39
	v_mov_b32_e32 v89, s40
	v_pk_add_f32 v[88:89], s[8:9], v[88:89]
	s_nop 0
	v_add_f32_e32 v88, v88, v89
	v_mul_f32_e32 v88, 0x3b800000, v88
	v_pk_add_f32 v[108:109], v[30:31], v[88:89] op_sel_hi:[1,0] neg_lo:[0,1] neg_hi:[0,1]
	v_pk_add_f32 v[110:111], v[32:33], v[88:89] op_sel_hi:[1,0] neg_lo:[0,1] neg_hi:[0,1]
	v_pk_mul_f32 v[90:91], v[108:109], v[108:109]
	v_pk_mul_f32 v[88:89], v[110:111], v[110:111]
	v_add_f32_e32 v90, v90, v91
	v_add_f32_e32 v88, v88, v90
	v_add_f32_e32 v88, v89, v88
	v_mov_b32_e32 v91, v86
	s_nop 0
	v_add_f32_dpp v88, v88, v88 quad_perm:[1,0,3,2] row_mask:0xf bank_mask:0xf bound_ctrl:1
	s_nop 1
	v_add_f32_dpp v88, v88, v88 quad_perm:[2,3,0,1] row_mask:0xf bank_mask:0xf bound_ctrl:1
	s_nop 1
	v_add_f32_dpp v88, v88, v88 row_half_mirror row_mask:0xf bank_mask:0xf bound_ctrl:1
	s_nop 1
	v_add_f32_dpp v88, v88, v88 row_mirror row_mask:0xf bank_mask:0xf bound_ctrl:1
	s_nop 0
	v_readlane_b32 s39, v88, 16
	v_readlane_b32 s40, v88, 48
	v_readlane_b32 s8, v88, 0
	v_readlane_b32 s9, v88, 32
	v_mov_b32_e32 v88, s39
	v_mov_b32_e32 v89, s40
	v_pk_add_f32 v[88:89], s[8:9], v[88:89]
	s_mov_b32 s9, s27
	v_mov_b32_e32 v90, v88
	v_mov_b32_e32 v86, v89
	v_pk_add_f32 v[86:87], v[90:91], v[86:87]
	s_mov_b32 s39, s27
	v_pk_fma_f32 v[112:113], v[86:87], s[6:7], v[94:95] op_sel_hi:[1,0,0]
	s_add_i32 s6, s53, 0x140
	v_mul_f32_e32 v86, 0x4b800000, v113
	v_cmp_gt_f32_e32 vcc, s7, v113
	s_nop 1
	v_cndmask_b32_e32 v86, v113, v86, vcc
	v_rsq_f32_e32 v113, v86
	global_load_dwordx4 v[86:89], v[78:79], off
	global_load_dwordx4 v[90:93], v[102:103], off
	global_load_dwordx4 v[94:97], v[76:77], off
	global_load_dwordx4 v[98:101], v[74:75], off
	v_mul_f32_e32 v74, 0x45800000, v113
	v_cndmask_b32_e32 v74, v113, v74, vcc
	v_pk_mul_f32 v[76:77], v[104:105], v[74:75] op_sel_hi:[1,0]
	v_mul_f32_e32 v75, 0x4b800000, v112
	v_cmp_gt_f32_e32 vcc, s7, v112
	v_pk_fma_f32 v[76:77], v[34:35], v[76:77], v[38:39]
	s_and_b32 s7, s6, 0x1c0
	v_cndmask_b32_e32 v75, v112, v75, vcc
	v_rsq_f32_e32 v78, v75
	v_pk_mul_f32 v[74:75], v[106:107], v[74:75] op_sel_hi:[1,0]
	v_cvt_pk_f16_f32 v76, v76, v77
	v_pk_fma_f32 v[74:75], v[36:37], v[74:75], v[40:41]
	s_lshl_b32 s6, s6, 4
	v_cvt_pk_f16_f32 v77, v74, v75
	v_mul_f32_e32 v74, 0x45800000, v78
	v_cndmask_b32_e32 v74, v78, v74, vcc
	v_pk_mul_f32 v[78:79], v[108:109], v[74:75] op_sel_hi:[1,0]
	s_or_b32 s50, s6, 0x2000
	v_pk_fma_f32 v[34:35], v[34:35], v[78:79], v[38:39]
	v_pk_mul_f32 v[38:39], v[110:111], v[74:75] op_sel_hi:[1,0]
	v_add_co_u32_e32 v78, vcc, s52, v70
	v_pk_fma_f32 v[36:37], v[36:37], v[38:39], v[40:41]
	v_cvt_pk_f16_f32 v34, v34, v35
	v_cvt_pk_f16_f32 v35, v36, v37
	v_addc_co_u32_e32 v79, vcc, 0, v71, vcc
	ds_write2_b64 v85, v[76:77], v[34:35] offset0:66 offset1:132
	s_waitcnt lgkmcnt(0)
	s_barrier
	global_load_dwordx4 v[34:37], v[70:71], off
	global_load_dwordx4 v[38:41], v[72:73], off
	s_nop 0
	global_load_dwordx4 v[70:73], v[78:79], off
	global_load_dwordx4 v[74:77], v[68:69], off
	s_or_b32 s46, s6, 0x6000
	s_sub_i32 s6, s38, s3
	s_and_b32 s6, s6, 0xe0
	v_lshl_add_u32 v172, s6, 1, v84
	s_add_i32 s6, s53, 0x180
	s_lshl_b32 s48, s7, 4
	s_and_b32 s7, s6, 0x1c0
	s_lshl_b32 s6, s6, 4
	s_or_b32 s44, s6, 0x2000
	s_or_b32 s40, s6, 0x6000
	s_add_i32 s6, s3, 0x60
	s_and_b32 s6, s6, 0xe0
	v_lshl_add_u32 v173, s6, 1, v84
	s_add_i32 s6, s53, 0x1c0
	s_xor_b32 s53, s53, 0x100
	v_add_u32_e32 v174, s53, v84
	s_add_i32 s53, s3, 0xa0
	s_lshl_b32 s42, s7, 4
	s_and_b32 s7, s6, 0x1c0
	s_lshl_b32 s6, s6, 4
	s_and_b32 s53, s53, 0xe0
	s_lshl_b32 s8, s7, 4
	s_or_b32 s38, s6, 0x2000
	s_or_b32 s6, s6, 0x6000
	s_mov_b32 s7, s27
	v_lshl_add_u32 v175, s53, 1, v84
	s_add_i32 s53, s3, 0xc0
	s_addk_i32 s3, 0xe0
	v_lshl_add_u64 v[68:69], v[64:65], 0, s[48:49]
	v_lshl_add_u64 v[78:79], v[64:65], 0, s[50:51]
	v_lshl_add_u64 v[138:139], v[64:65], 0, s[46:47]
	v_lshl_add_u64 v[140:141], v[64:65], 0, s[42:43]
	v_lshl_add_u64 v[142:143], v[64:65], 0, s[44:45]
	v_lshl_add_u64 v[144:145], v[64:65], 0, s[40:41]
	v_lshl_add_u64 v[146:147], v[64:65], 0, s[8:9]
	v_lshl_add_u64 v[148:149], v[64:65], 0, s[38:39]
	v_lshl_add_u64 v[150:151], v[64:65], 0, s[6:7]
	s_and_b32 s53, s53, 0xe0
	s_and_b32 s3, s3, 0xe0
	v_add_u32_e32 v64, s28, v83
	v_mov_b32_e32 v65, v67
	v_lshl_add_u32 v176, s53, 1, v84
	v_lshl_add_u32 v177, s3, 1, v84
	v_lshlrev_b64 v[84:85], 10, v[64:65]
	ds_read_b128 v[102:105], v1
	ds_read_b128 v[106:109], v1 offset:8448
	v_lshl_add_u64 v[166:167], v[58:59], 0, v[84:85]
	v_or_b32_e32 v84, 1, v64
	v_mov_b32_e32 v85, v67
	v_lshlrev_b64 v[84:85], 10, v[84:85]
	v_lshl_add_u64 v[168:169], v[58:59], 0, v[84:85]
	v_or_b32_e32 v84, 2, v64
	v_mov_b32_e32 v85, v67
	v_or_b32_e32 v64, 3, v64
	v_lshlrev_b64 v[84:85], 10, v[84:85]
	v_lshlrev_b64 v[64:65], 10, v[64:65]
	v_lshl_add_u64 v[170:171], v[58:59], 0, v[84:85]
	v_lshl_add_u64 v[58:59], v[58:59], 0, v[64:65]
	s_setprio 1
	s_waitcnt vmcnt(13) lgkmcnt(1)
	v_mfma_f32_16x16x32_f16 v[110:113], v[102:105], v[22:25], 0
	s_waitcnt lgkmcnt(0)
	v_mfma_f32_16x16x32_f16 v[22:25], v[106:109], v[22:25], 0
	s_waitcnt vmcnt(5)
	v_mfma_f32_16x16x32_f16 v[114:117], v[102:105], v[94:97], 0
	v_mfma_f32_16x16x32_f16 v[94:97], v[106:109], v[94:97], 0
	v_mfma_f32_16x16x32_f16 v[118:121], v[102:105], v[14:17], 0
	v_mfma_f32_16x16x32_f16 v[14:17], v[106:109], v[14:17], 0
	v_mfma_f32_16x16x32_f16 v[102:105], v[102:105], v[18:21], 0
	v_mfma_f32_16x16x32_f16 v[18:21], v[106:109], v[18:21], 0
	s_setprio 0
	v_add_co_u32_e32 v64, vcc, s29, v62
	global_load_dwordx4 v[106:109], v[62:63], off
	s_nop 0
	v_addc_co_u32_e32 v65, vcc, 0, v63, vcc
	v_add_co_u32_e32 v84, vcc, s52, v62
	s_nop 1
	v_addc_co_u32_e32 v85, vcc, 0, v63, vcc
	v_add_co_u32_e32 v62, vcc, s33, v62
	global_load_dwordx4 v[122:125], v[64:65], off
	global_load_dwordx4 v[126:129], v[84:85], off
	v_addc_co_u32_e32 v63, vcc, 0, v63, vcc
	global_load_dwordx4 v[62:65], v[62:63], off
	ds_read_b128 v[130:133], v82
	ds_read_b128 v[134:137], v82 offset:8448
	s_setprio 1
	s_waitcnt lgkmcnt(1)
	v_mfma_f32_16x16x32_f16 v[110:113], v[130:133], v[10:13], v[110:113]
	s_waitcnt lgkmcnt(0)
	v_mfma_f32_16x16x32_f16 v[10:13], v[134:137], v[10:13], v[22:25]
	v_mfma_f32_16x16x32_f16 v[22:25], v[130:133], v[54:57], v[114:117]
	v_mfma_f32_16x16x32_f16 v[54:57], v[134:137], v[54:57], v[94:97]
	v_mfma_f32_16x16x32_f16 v[94:97], v[130:133], v[86:89], v[118:121]
	v_mfma_f32_16x16x32_f16 v[14:17], v[134:137], v[86:89], v[14:17]
	v_mfma_f32_16x16x32_f16 v[84:87], v[130:133], v[50:53], v[102:105]
	v_mfma_f32_16x16x32_f16 v[18:21], v[134:137], v[50:53], v[18:21]
	s_setprio 0
	global_load_dwordx4 v[50:53], v[68:69], off
	global_load_dwordx4 v[102:105], v[78:79], off
	v_add_co_u32_e32 v68, vcc, s52, v68
	s_nop 1
	v_addc_co_u32_e32 v69, vcc, 0, v69, vcc
	global_load_dwordx4 v[114:117], v[68:69], off
	global_load_dwordx4 v[118:121], v[138:139], off
	ds_read_b128 v[130:133], v172
	ds_read_b128 v[134:137], v172 offset:8448
	s_setprio 1
	s_waitcnt lgkmcnt(1)
	v_mfma_f32_16x16x32_f16 v[110:113], v[130:133], v[46:49], v[110:113]
	s_waitcnt lgkmcnt(0)
	v_mfma_f32_16x16x32_f16 v[10:13], v[134:137], v[46:49], v[10:13]
	v_mfma_f32_16x16x32_f16 v[22:25], v[130:133], v[42:45], v[22:25]
	v_mfma_f32_16x16x32_f16 v[42:45], v[134:137], v[42:45], v[54:57]
	v_mfma_f32_16x16x32_f16 v[46:49], v[130:133], v[90:93], v[94:97]
	v_mfma_f32_16x16x32_f16 v[14:17], v[134:137], v[90:93], v[14:17]
	s_waitcnt vmcnt(12)
	v_mfma_f32_16x16x32_f16 v[54:57], v[130:133], v[98:101], v[84:87]
	v_mfma_f32_16x16x32_f16 v[18:21], v[134:137], v[98:101], v[18:21]
	s_setprio 0
	v_add_co_u32_e32 v68, vcc, s52, v140
	global_load_dwordx4 v[84:87], v[140:141], off
	global_load_dwordx4 v[88:91], v[142:143], off
	v_addc_co_u32_e32 v69, vcc, 0, v141, vcc
	global_load_dwordx4 v[92:95], v[68:69], off
	global_load_dwordx4 v[96:99], v[144:145], off
	ds_read_b128 v[130:133], v173
	ds_read_b128 v[134:137], v173 offset:8448
	s_setprio 1
	s_waitcnt vmcnt(15) lgkmcnt(1)
	v_mfma_f32_16x16x32_f16 v[110:113], v[130:133], v[34:37], v[110:113]
	s_waitcnt lgkmcnt(0)
	v_mfma_f32_16x16x32_f16 v[10:13], v[134:137], v[34:37], v[10:13]
	s_waitcnt vmcnt(14)
	v_mfma_f32_16x16x32_f16 v[22:25], v[130:133], v[38:41], v[22:25]
	v_mfma_f32_16x16x32_f16 v[34:37], v[134:137], v[38:41], v[42:45]
	s_waitcnt vmcnt(13)
	v_mfma_f32_16x16x32_f16 v[38:41], v[130:133], v[70:73], v[46:49]
	v_mfma_f32_16x16x32_f16 v[14:17], v[134:137], v[70:73], v[14:17]
	s_waitcnt vmcnt(12)
	v_mfma_f32_16x16x32_f16 v[42:45], v[130:133], v[74:77], v[54:57]
	v_mfma_f32_16x16x32_f16 v[18:21], v[134:137], v[74:77], v[18:21]
	s_setprio 0
	v_add_co_u32_e32 v68, vcc, s52, v146
	global_load_dwordx4 v[46:49], v[146:147], off
	global_load_dwordx4 v[54:57], v[148:149], off
	v_addc_co_u32_e32 v69, vcc, 0, v147, vcc
	global_load_dwordx4 v[68:71], v[68:69], off
	s_nop 0
	global_load_dwordx4 v[72:75], v[150:151], off
	ds_read_b128 v[76:79], v174
	ds_read_b128 v[130:133], v174 offset:8448
	s_setprio 1
	s_waitcnt vmcnt(15) lgkmcnt(1)
	v_mfma_f32_16x16x32_f16 v[110:113], v[76:79], v[106:109], v[110:113]
	s_waitcnt lgkmcnt(0)
	v_mfma_f32_16x16x32_f16 v[10:13], v[130:133], v[106:109], v[10:13]
	s_waitcnt vmcnt(14)
	v_mfma_f32_16x16x32_f16 v[22:25], v[76:79], v[122:125], v[22:25]
	v_mfma_f32_16x16x32_f16 v[34:37], v[130:133], v[122:125], v[34:37]
	s_waitcnt vmcnt(13)
	v_mfma_f32_16x16x32_f16 v[38:41], v[76:79], v[126:129], v[38:41]
	v_mfma_f32_16x16x32_f16 v[14:17], v[130:133], v[126:129], v[14:17]
	s_waitcnt vmcnt(12)
	v_mfma_f32_16x16x32_f16 v[42:45], v[76:79], v[62:65], v[42:45]
	v_mfma_f32_16x16x32_f16 v[18:21], v[130:133], v[62:65], v[18:21]
	s_setprio 0
	ds_read_b128 v[62:65], v175
	ds_read_b128 v[76:79], v175 offset:8448
	s_setprio 1
	s_waitcnt vmcnt(11) lgkmcnt(1)
	v_mfma_f32_16x16x32_f16 v[106:109], v[62:65], v[50:53], v[110:113]
	s_waitcnt lgkmcnt(0)
	v_mfma_f32_16x16x32_f16 v[10:13], v[76:79], v[50:53], v[10:13]
	s_waitcnt vmcnt(10)
	v_mfma_f32_16x16x32_f16 v[22:25], v[62:65], v[102:105], v[22:25]
	v_mfma_f32_16x16x32_f16 v[34:37], v[76:79], v[102:105], v[34:37]
	s_waitcnt vmcnt(9)
	v_mfma_f32_16x16x32_f16 v[38:41], v[62:65], v[114:117], v[38:41]
	v_mfma_f32_16x16x32_f16 v[14:17], v[76:79], v[114:117], v[14:17]
	s_waitcnt vmcnt(8)
	v_mfma_f32_16x16x32_f16 v[42:45], v[62:65], v[118:121], v[42:45]
	v_mfma_f32_16x16x32_f16 v[18:21], v[76:79], v[118:121], v[18:21]
	s_setprio 0
	ds_read_b128 v[50:53], v176
	ds_read_b128 v[62:65], v176 offset:8448
	s_setprio 1
	s_waitcnt vmcnt(7) lgkmcnt(1)
	v_mfma_f32_16x16x32_f16 v[76:79], v[50:53], v[84:87], v[106:109]
	s_waitcnt lgkmcnt(0)
	v_mfma_f32_16x16x32_f16 v[10:13], v[62:65], v[84:87], v[10:13]
	s_waitcnt vmcnt(6)
	v_mfma_f32_16x16x32_f16 v[22:25], v[50:53], v[88:91], v[22:25]
	v_mfma_f32_16x16x32_f16 v[34:37], v[62:65], v[88:91], v[34:37]
	s_waitcnt vmcnt(5)
	v_mfma_f32_16x16x32_f16 v[38:41], v[50:53], v[92:95], v[38:41]
	v_mfma_f32_16x16x32_f16 v[14:17], v[62:65], v[92:95], v[14:17]
	s_waitcnt vmcnt(4)
	v_mfma_f32_16x16x32_f16 v[42:45], v[50:53], v[96:99], v[42:45]
	v_mfma_f32_16x16x32_f16 v[18:21], v[62:65], v[96:99], v[18:21]
	s_setprio 0
	ds_read_b128 v[50:53], v177
	ds_read_b128 v[62:65], v177 offset:8448
	s_setprio 1
	s_waitcnt vmcnt(3) lgkmcnt(1)
	v_mfma_f32_16x16x32_f16 v[76:79], v[50:53], v[46:49], v[76:79]
	s_waitcnt lgkmcnt(0)
	v_mfma_f32_16x16x32_f16 v[10:13], v[62:65], v[46:49], v[10:13]
	s_waitcnt vmcnt(2)
	v_mfma_f32_16x16x32_f16 v[22:25], v[50:53], v[54:57], v[22:25]
	v_mfma_f32_16x16x32_f16 v[34:37], v[62:65], v[54:57], v[34:37]
	s_waitcnt vmcnt(1)
	v_mfma_f32_16x16x32_f16 v[38:41], v[50:53], v[68:71], v[38:41]
	v_mfma_f32_16x16x32_f16 v[14:17], v[62:65], v[68:71], v[14:17]
	s_waitcnt vmcnt(0)
	v_mfma_f32_16x16x32_f16 v[42:45], v[50:53], v[72:75], v[42:45]
	v_mfma_f32_16x16x32_f16 v[18:21], v[62:65], v[72:75], v[18:21]
	s_setprio 0
	v_add_co_u32_e32 v108, vcc, s29, v152
	v_and_b32_e32 v67, 0x1c0, v0
	s_nop 0
	v_addc_co_u32_e32 v109, vcc, 0, v153, vcc
	v_add_co_u32_e32 v46, vcc, s52, v152
	s_movk_i32 s4, 0x50
	s_nop 0
	v_addc_co_u32_e32 v47, vcc, 0, v153, vcc
	v_add_co_u32_e32 v68, vcc, s33, v152
	v_or_b32_e32 v116, 16, v67
	s_nop 0
	v_addc_co_u32_e32 v69, vcc, 0, v153, vcc
	v_add_co_u32_e32 v110, vcc, s52, v154
	global_load_dwordx4 v[46:49], v[46:47], off
	s_nop 0
	global_load_dwordx4 v[50:53], v[68:69], off
	global_load_dwordx4 v[54:57], v[152:153], off
	global_load_dwordx4 v[62:65], v[154:155], off
	v_addc_co_u32_e32 v111, vcc, 0, v155, vcc
	v_add_co_u32_e32 v112, vcc, s52, v160
	global_load_dwordx4 v[68:71], v[156:157], off
	global_load_dwordx4 v[72:75], v[158:159], off
	global_load_dwordx4 v[84:87], v[160:161], off
	global_load_dwordx4 v[88:91], v[162:163], off
	v_addc_co_u32_e32 v113, vcc, 0, v161, vcc
	global_load_dwordx4 v[92:95], v[110:111], off
	global_load_dwordx4 v[96:99], v[112:113], off
	global_load_dwordx4 v[100:103], v[108:109], off
	global_load_dwordx4 v[104:107], v[164:165], off
	s_nop 0
	global_store_dwordx4 v[166:167], v[2:5], off sc0 sc1
	global_store_dwordx4 v[168:169], v[6:9], off sc0 sc1
	global_store_dwordx4 v[170:171], v[26:29], off sc0 sc1
	global_store_dwordx4 v[58:59], v[30:33], off sc0 sc1
	v_and_b32_e32 v4, 0x1cf, v0
	v_cvt_pk_f16_f32 v3, v78, v79
	v_cvt_pk_f16_f32 v2, v76, v77
	v_mad_u32_u24 v4, v4, s4, v80
	v_or_b32_e32 v5, v116, v81
	v_or_b32_e32 v117, 32, v67
	ds_write_b64 v4, v[2:3]
	v_cvt_pk_f16_f32 v3, v24, v25
	v_cvt_pk_f16_f32 v2, v22, v23
	v_mad_u32_u24 v5, v5, s4, v80
	v_or_b32_e32 v6, v117, v81
	v_or_b32_e32 v118, 48, v67
	ds_write_b64 v5, v[2:3]
	v_cvt_pk_f16_f32 v3, v40, v41
	v_cvt_pk_f16_f32 v2, v38, v39
	v_mad_u32_u24 v6, v6, s4, v80
	v_or_b32_e32 v7, v118, v81
	ds_write_b64 v6, v[2:3]
	v_cvt_pk_f16_f32 v3, v44, v45
	v_cvt_pk_f16_f32 v2, v42, v43
	v_mad_u32_u24 v7, v7, s4, v80
	ds_write_b64 v7, v[2:3]
	v_cvt_pk_f16_f32 v3, v12, v13
	v_cvt_pk_f16_f32 v2, v10, v11
	ds_write_b64 v4, v[2:3] offset:32
	v_cvt_pk_f16_f32 v3, v36, v37
	v_cvt_pk_f16_f32 v2, v34, v35
	ds_write_b64 v5, v[2:3] offset:32
	v_cvt_pk_f16_f32 v3, v16, v17
	v_cvt_pk_f16_f32 v2, v14, v15
	v_lshl_add_u64 v[10:11], v[60:61], 0, s[14:15]
	ds_write_b64 v6, v[2:3] offset:32
	v_cvt_pk_f16_f32 v2, v18, v19
	v_add_co_u32_e32 v18, vcc, s52, v10
	v_cvt_pk_f16_f32 v3, v20, v21
	v_lshl_add_u64 v[12:13], v[60:61], 0, s[16:17]
	v_addc_co_u32_e32 v19, vcc, 0, v11, vcc
	ds_write_b64 v7, v[2:3] offset:32
	s_waitcnt lgkmcnt(0)
	s_barrier
	global_load_dwordx4 v[2:5], v[10:11], off
	global_load_dwordx4 v[6:9], v[12:13], off
	v_lshl_add_u64 v[20:21], v[60:61], 0, s[12:13]
	global_load_dwordx4 v[10:13], v[18:19], off
	global_load_dwordx4 v[14:17], v[20:21], off
	ds_read_b128 v[18:21], v1
	ds_read_b128 v[22:25], v1 offset:8448
	s_mov_b32 s3, s27
	s_setprio 1
	s_waitcnt vmcnt(17) lgkmcnt(1)
	v_mfma_f32_16x16x32_f16 v[26:29], v[18:21], v[54:57], 0
	s_waitcnt lgkmcnt(0)
	v_mfma_f32_16x16x32_f16 v[30:33], v[22:25], v[54:57], 0
	s_waitcnt vmcnt(9)
	v_mfma_f32_16x16x32_f16 v[34:37], v[18:21], v[100:103], 0
	v_mfma_f32_16x16x32_f16 v[38:41], v[22:25], v[100:103], 0
	v_mfma_f32_16x16x32_f16 v[42:45], v[18:21], v[46:49], 0
	v_mfma_f32_16x16x32_f16 v[46:49], v[22:25], v[46:49], 0
	v_mfma_f32_16x16x32_f16 v[18:21], v[18:21], v[50:53], 0
	v_mfma_f32_16x16x32_f16 v[22:25], v[22:25], v[50:53], 0
	s_setprio 0
	v_lshl_add_u64 v[58:59], v[60:61], 0, s[10:11]
	v_add_co_u32_e32 v76, vcc, s29, v58
	s_nop 1
	v_addc_co_u32_e32 v77, vcc, 0, v59, vcc
	v_add_co_u32_e32 v108, vcc, s52, v58
	global_load_dwordx4 v[50:53], v[58:59], off
	global_load_dwordx4 v[54:57], v[76:77], off
	v_addc_co_u32_e32 v109, vcc, 0, v59, vcc
	v_add_co_u32_e32 v58, vcc, s33, v58
	s_nop 1
	v_addc_co_u32_e32 v59, vcc, 0, v59, vcc
	global_load_dwordx4 v[76:79], v[108:109], off
	global_load_dwordx4 v[100:103], v[58:59], off
	ds_read_b128 v[108:111], v82
	ds_read_b128 v[112:115], v82 offset:8448
	s_setprio 1
	s_waitcnt lgkmcnt(1)
	v_mfma_f32_16x16x32_f16 v[26:29], v[108:111], v[62:65], v[26:29]
	s_waitcnt lgkmcnt(0)
	v_mfma_f32_16x16x32_f16 v[30:33], v[112:115], v[62:65], v[30:33]
	v_mfma_f32_16x16x32_f16 v[34:37], v[108:111], v[68:71], v[34:37]
	v_mfma_f32_16x16x32_f16 v[38:41], v[112:115], v[68:71], v[38:41]
	v_mfma_f32_16x16x32_f16 v[42:45], v[108:111], v[92:95], v[42:45]
	v_mfma_f32_16x16x32_f16 v[46:49], v[112:115], v[92:95], v[46:49]
	v_mfma_f32_16x16x32_f16 v[18:21], v[108:111], v[72:75], v[18:21]
	v_mfma_f32_16x16x32_f16 v[22:25], v[112:115], v[72:75], v[22:25]
	s_setprio 0
	v_lshl_add_u64 v[58:59], v[60:61], 0, s[48:49]
	v_lshl_add_u64 v[72:73], v[60:61], 0, s[50:51]
	global_load_dwordx4 v[62:65], v[58:59], off
	global_load_dwordx4 v[68:71], v[72:73], off
	v_add_co_u32_e32 v58, vcc, s52, v58
	v_lshl_add_u64 v[82:83], v[60:61], 0, s[46:47]
	s_nop 0
	v_addc_co_u32_e32 v59, vcc, 0, v59, vcc
	global_load_dwordx4 v[72:75], v[58:59], off
	global_load_dwordx4 v[92:95], v[82:83], off
	ds_read_b128 v[108:111], v172
	ds_read_b128 v[112:115], v172 offset:8448
	s_setprio 1
	s_waitcnt lgkmcnt(1)
	v_mfma_f32_16x16x32_f16 v[26:29], v[108:111], v[84:87], v[26:29]
	s_waitcnt lgkmcnt(0)
	v_mfma_f32_16x16x32_f16 v[30:33], v[112:115], v[84:87], v[30:33]
	v_mfma_f32_16x16x32_f16 v[34:37], v[108:111], v[88:91], v[34:37]
	v_mfma_f32_16x16x32_f16 v[38:41], v[112:115], v[88:91], v[38:41]
	v_mfma_f32_16x16x32_f16 v[42:45], v[108:111], v[96:99], v[42:45]
	v_mfma_f32_16x16x32_f16 v[46:49], v[112:115], v[96:99], v[46:49]
	s_waitcnt vmcnt(16)
	v_mfma_f32_16x16x32_f16 v[18:21], v[108:111], v[104:107], v[18:21]
	v_mfma_f32_16x16x32_f16 v[22:25], v[112:115], v[104:107], v[22:25]
	s_setprio 0
	v_lshl_add_u64 v[58:59], v[60:61], 0, s[42:43]
	v_lshl_add_u64 v[90:91], v[60:61], 0, s[44:45]
	global_load_dwordx4 v[82:85], v[58:59], off
	global_load_dwordx4 v[86:89], v[90:91], off
	v_add_co_u32_e32 v58, vcc, s52, v58
	v_lshl_add_u64 v[90:91], v[60:61], 0, s[40:41]
	s_nop 0
	v_addc_co_u32_e32 v59, vcc, 0, v59, vcc
	global_load_dwordx4 v[96:99], v[58:59], off
	global_load_dwordx4 v[104:107], v[90:91], off
	ds_read_b128 v[108:111], v173
	ds_read_b128 v[112:115], v173 offset:8448
	s_setprio 1
	s_waitcnt vmcnt(15) lgkmcnt(1)
	v_mfma_f32_16x16x32_f16 v[26:29], v[108:111], v[2:5], v[26:29]
	s_waitcnt lgkmcnt(0)
	v_mfma_f32_16x16x32_f16 v[2:5], v[112:115], v[2:5], v[30:33]
	s_waitcnt vmcnt(14)
	v_mfma_f32_16x16x32_f16 v[30:33], v[108:111], v[6:9], v[34:37]
	v_mfma_f32_16x16x32_f16 v[6:9], v[112:115], v[6:9], v[38:41]
	s_waitcnt vmcnt(13)
	v_mfma_f32_16x16x32_f16 v[34:37], v[108:111], v[10:13], v[42:45]
	v_mfma_f32_16x16x32_f16 v[10:13], v[112:115], v[10:13], v[46:49]
	s_waitcnt vmcnt(12)
	v_mfma_f32_16x16x32_f16 v[18:21], v[108:111], v[14:17], v[18:21]
	v_mfma_f32_16x16x32_f16 v[14:17], v[112:115], v[14:17], v[22:25]
	s_setprio 0
	v_lshl_add_u64 v[42:43], v[60:61], 0, s[8:9]
	v_add_co_u32_e32 v58, vcc, s52, v42
	v_lshl_add_u64 v[44:45], v[60:61], 0, s[38:39]
	s_nop 0
	v_addc_co_u32_e32 v59, vcc, 0, v43, vcc
	global_load_dwordx4 v[22:25], v[42:43], off
	global_load_dwordx4 v[38:41], v[44:45], off
	v_lshl_add_u64 v[60:61], v[60:61], 0, s[6:7]
	global_load_dwordx4 v[42:45], v[58:59], off
	global_load_dwordx4 v[46:49], v[60:61], off
	ds_read_b128 v[58:61], v174
	ds_read_b128 v[108:111], v174 offset:8448
	s_setprio 1
	s_waitcnt vmcnt(15) lgkmcnt(1)
	v_mfma_f32_16x16x32_f16 v[26:29], v[58:61], v[50:53], v[26:29]
	s_waitcnt lgkmcnt(0)
	v_mfma_f32_16x16x32_f16 v[2:5], v[108:111], v[50:53], v[2:5]
	s_waitcnt vmcnt(14)
	v_mfma_f32_16x16x32_f16 v[30:33], v[58:61], v[54:57], v[30:33]
	v_mfma_f32_16x16x32_f16 v[6:9], v[108:111], v[54:57], v[6:9]
	s_waitcnt vmcnt(13)
	v_mfma_f32_16x16x32_f16 v[34:37], v[58:61], v[76:79], v[34:37]
	v_mfma_f32_16x16x32_f16 v[10:13], v[108:111], v[76:79], v[10:13]
	s_waitcnt vmcnt(12)
	v_mfma_f32_16x16x32_f16 v[18:21], v[58:61], v[100:103], v[18:21]
	v_mfma_f32_16x16x32_f16 v[14:17], v[108:111], v[100:103], v[14:17]
	s_setprio 0
	ds_read_b128 v[50:53], v175
	ds_read_b128 v[54:57], v175 offset:8448
	s_setprio 1
	s_waitcnt vmcnt(11) lgkmcnt(1)
	v_mfma_f32_16x16x32_f16 v[26:29], v[50:53], v[62:65], v[26:29]
	s_waitcnt lgkmcnt(0)
	v_mfma_f32_16x16x32_f16 v[2:5], v[54:57], v[62:65], v[2:5]
	s_waitcnt vmcnt(10)
	v_mfma_f32_16x16x32_f16 v[30:33], v[50:53], v[68:71], v[30:33]
	v_mfma_f32_16x16x32_f16 v[6:9], v[54:57], v[68:71], v[6:9]
	s_waitcnt vmcnt(9)
	v_mfma_f32_16x16x32_f16 v[34:37], v[50:53], v[72:75], v[34:37]
	v_mfma_f32_16x16x32_f16 v[10:13], v[54:57], v[72:75], v[10:13]
	s_waitcnt vmcnt(8)
	v_mfma_f32_16x16x32_f16 v[18:21], v[50:53], v[92:95], v[18:21]
	v_mfma_f32_16x16x32_f16 v[14:17], v[54:57], v[92:95], v[14:17]
	s_setprio 0
	ds_read_b128 v[50:53], v176
	ds_read_b128 v[54:57], v176 offset:8448
	s_setprio 1
	s_waitcnt vmcnt(7) lgkmcnt(1)
	v_mfma_f32_16x16x32_f16 v[26:29], v[50:53], v[82:85], v[26:29]
	s_waitcnt lgkmcnt(0)
	v_mfma_f32_16x16x32_f16 v[2:5], v[54:57], v[82:85], v[2:5]
	s_waitcnt vmcnt(6)
	v_mfma_f32_16x16x32_f16 v[30:33], v[50:53], v[86:89], v[30:33]
	v_mfma_f32_16x16x32_f16 v[6:9], v[54:57], v[86:89], v[6:9]
	s_waitcnt vmcnt(5)
	v_mfma_f32_16x16x32_f16 v[34:37], v[50:53], v[96:99], v[34:37]
	v_mfma_f32_16x16x32_f16 v[58:61], v[54:57], v[96:99], v[10:13]
	s_waitcnt vmcnt(4)
	v_mfma_f32_16x16x32_f16 v[18:21], v[50:53], v[104:107], v[18:21]
	v_mfma_f32_16x16x32_f16 v[50:53], v[54:57], v[104:107], v[14:17]
	s_setprio 0
	ds_read_b128 v[54:57], v177
	ds_read_b128 v[62:65], v177 offset:8448
	s_setprio 1
	s_waitcnt vmcnt(3) lgkmcnt(1)
	v_mfma_f32_16x16x32_f16 v[26:29], v[54:57], v[22:25], v[26:29]
	s_waitcnt lgkmcnt(0)
	v_mfma_f32_16x16x32_f16 v[14:17], v[62:65], v[22:25], v[2:5]
	s_waitcnt vmcnt(2)
	v_mfma_f32_16x16x32_f16 v[22:25], v[54:57], v[38:41], v[30:33]
	v_mfma_f32_16x16x32_f16 v[10:13], v[62:65], v[38:41], v[6:9]
	s_waitcnt vmcnt(1)
	v_mfma_f32_16x16x32_f16 v[30:33], v[54:57], v[42:45], v[34:37]
	v_mfma_f32_16x16x32_f16 v[6:9], v[62:65], v[42:45], v[58:61]
	s_waitcnt vmcnt(0)
	v_mfma_f32_16x16x32_f16 v[34:37], v[54:57], v[46:49], v[18:21]
	v_mfma_f32_16x16x32_f16 v[2:5], v[62:65], v[46:49], v[50:53]
	s_setprio 0
	s_nop 1
	v_mul_u32_u24_e32 v52, 0x50, v0
	ds_read_b128 v[18:21], v52
	s_lshl_b64 s[2:3], s[2:3], 15
	v_or_b32_e32 v0, s2, v66
	v_mov_b32_e32 v1, s3
	v_lshl_add_u64 v[50:51], s[24:25], 0, v[0:1]
	ds_read_b128 v[38:41], v52 offset:16
	ds_read_b128 v[42:45], v52 offset:32
	ds_read_b128 v[46:49], v52 offset:48
	s_waitcnt lgkmcnt(3)
	global_store_dwordx4 v[50:51], v[18:21], off sc0 sc1
	s_nop 1
	v_add_co_u32_e32 v18, vcc, s29, v50
	s_nop 1
	v_addc_co_u32_e32 v19, vcc, 0, v51, vcc
	s_waitcnt lgkmcnt(2)
	global_store_dwordx4 v[18:19], v[38:41], off sc0 sc1
	v_or_b32_e32 v18, 0x4000, v0
	v_mov_b32_e32 v19, s3
	v_lshl_add_u64 v[20:21], s[24:25], 0, v[18:19]
	s_waitcnt lgkmcnt(1)
	global_store_dwordx4 v[20:21], v[42:45], off sc0 sc1
	v_mul_f32_e32 v20, 0xbfb8aa3b, v26
	v_exp_f32_e32 v38, v20
	v_add_co_u32_e32 v20, vcc, s33, v50
	v_or_b32_e32 v39, 0x200, v81
	s_nop 0
	v_addc_co_u32_e32 v21, vcc, 0, v51, vcc
	s_waitcnt lgkmcnt(0)
	global_store_dwordx4 v[20:21], v[46:49], off sc0 sc1
	v_add_f32_e32 v20, 1.0, v38
	v_rcp_f32_e32 v20, v20
	v_mul_f32_e32 v21, 0xbfb8aa3b, v27
	v_mul_f32_e32 v38, 0xbfb8aa3b, v28
	v_exp_f32_e32 v21, v21
	v_exp_f32_e32 v38, v38
	v_fma_mixlo_f16 v40, v26, v20, 0
	v_mul_f32_e32 v26, 0xbfb8aa3b, v29
	v_add_f32_e32 v20, 1.0, v21
	v_add_f32_e32 v21, 1.0, v38
	v_exp_f32_e32 v38, v26
	v_rcp_f32_e32 v20, v20
	v_rcp_f32_e32 v21, v21
	v_mov_b32_e32 v26, v27
	v_mov_b32_e32 v27, v28
	v_add_f32_e32 v28, 1.0, v38
	v_rcp_f32_e32 v28, v28
	v_pk_mul_f32 v[20:21], v[26:27], v[20:21]
	v_or_b32_e32 v27, v39, v67
	v_cvt_pk_f16_f32 v21, v20, v21
	v_fma_mixlo_f16 v26, v29, v28, 0
	v_pack_b32_f16 v20, v40, v21
	v_alignbit_b32 v21, v26, v21, 16
	v_mul_f32_e32 v26, 0xbfb8aa3b, v22
	v_exp_f32_e32 v26, v26
	v_mad_u32_u24 v27, v27, s4, v80
	ds_write_b64 v27, v[20:21]
	v_mul_f32_e32 v21, 0xbfb8aa3b, v23
	v_add_f32_e32 v20, 1.0, v26
	v_rcp_f32_e32 v20, v20
	v_mul_f32_e32 v26, 0xbfb8aa3b, v24
	v_exp_f32_e32 v21, v21
	v_exp_f32_e32 v26, v26
	v_fma_mixlo_f16 v28, v22, v20, 0
	v_mul_f32_e32 v22, 0xbfb8aa3b, v25
	v_add_f32_e32 v20, 1.0, v21
	v_add_f32_e32 v21, 1.0, v26
	v_exp_f32_e32 v26, v22
	v_rcp_f32_e32 v20, v20
	v_rcp_f32_e32 v21, v21
	v_mov_b32_e32 v22, v23
	v_mov_b32_e32 v23, v24
	v_add_f32_e32 v24, 1.0, v26
	v_rcp_f32_e32 v24, v24
	v_pk_mul_f32 v[20:21], v[22:23], v[20:21]
	v_or_b32_e32 v23, v116, v39
	v_cvt_pk_f16_f32 v21, v20, v21
	v_fma_mixlo_f16 v22, v25, v24, 0
	v_pack_b32_f16 v20, v28, v21
	v_alignbit_b32 v21, v22, v21, 16
	v_mul_f32_e32 v22, 0xbfb8aa3b, v30
	v_exp_f32_e32 v22, v22
	v_mad_u32_u24 v24, v23, s4, v80
	ds_write_b64 v24, v[20:21]
	v_mul_f32_e32 v21, 0xbfb8aa3b, v31
	v_add_f32_e32 v20, 1.0, v22
	v_mul_f32_e32 v22, 0xbfb8aa3b, v32
	v_rcp_f32_e32 v20, v20
	v_exp_f32_e32 v21, v21
	v_exp_f32_e32 v22, v22
	v_mov_b32_e32 v23, v32
	v_fma_mixlo_f16 v25, v30, v20, 0
	v_add_f32_e32 v20, 1.0, v21
	v_add_f32_e32 v21, 1.0, v22
	v_mul_f32_e32 v22, 0xbfb8aa3b, v33
	v_exp_f32_e32 v26, v22
	v_rcp_f32_e32 v20, v20
	v_rcp_f32_e32 v21, v21
	v_mov_b32_e32 v22, v31
	v_add_f32_e32 v26, 1.0, v26
	v_rcp_f32_e32 v26, v26
	v_pk_mul_f32 v[20:21], v[22:23], v[20:21]
	v_or_b32_e32 v23, v117, v39
	v_cvt_pk_f16_f32 v21, v20, v21
	v_fma_mixlo_f16 v22, v33, v26, 0
	v_pack_b32_f16 v20, v25, v21
	v_alignbit_b32 v21, v22, v21, 16
	v_mul_f32_e32 v22, 0xbfb8aa3b, v34
	v_exp_f32_e32 v22, v22
	v_mad_u32_u24 v25, v23, s4, v80
	ds_write_b64 v25, v[20:21]
	v_mul_f32_e32 v21, 0xbfb8aa3b, v35
	v_add_f32_e32 v20, 1.0, v22
	v_mul_f32_e32 v22, 0xbfb8aa3b, v36
	v_rcp_f32_e32 v20, v20
	v_exp_f32_e32 v21, v21
	v_exp_f32_e32 v22, v22
	v_mov_b32_e32 v23, v36
	v_fma_mixlo_f16 v26, v34, v20, 0
	v_add_f32_e32 v20, 1.0, v21
	v_add_f32_e32 v21, 1.0, v22
	v_mul_f32_e32 v22, 0xbfb8aa3b, v37
	v_exp_f32_e32 v28, v22
	v_rcp_f32_e32 v20, v20
	v_rcp_f32_e32 v21, v21
	v_mov_b32_e32 v22, v35
	v_add_f32_e32 v28, 1.0, v28
	v_rcp_f32_e32 v28, v28
	v_pk_mul_f32 v[20:21], v[22:23], v[20:21]
	v_or_b32_e32 v23, v118, v39
	v_cvt_pk_f16_f32 v21, v20, v21
	v_fma_mixlo_f16 v22, v37, v28, 0
	v_pack_b32_f16 v20, v26, v21
	v_alignbit_b32 v21, v22, v21, 16
	v_mul_f32_e32 v22, 0xbfb8aa3b, v14
	v_exp_f32_e32 v22, v22
	v_mad_u32_u24 v23, v23, s4, v80
	ds_write_b64 v23, v[20:21]
	v_mul_f32_e32 v21, 0xbfb8aa3b, v15
	v_add_f32_e32 v20, 1.0, v22
	v_rcp_f32_e32 v20, v20
	v_exp_f32_e32 v21, v21
	v_mul_f32_e32 v22, 0xbfb8aa3b, v16
	v_exp_f32_e32 v22, v22
	v_fma_mixlo_f16 v26, v14, v20, 0
	v_add_f32_e32 v14, 1.0, v21
	v_rcp_f32_e32 v20, v14
	v_add_f32_e32 v14, 1.0, v22
	v_rcp_f32_e32 v21, v14
	v_mov_b32_e32 v14, v15
	v_mul_f32_e32 v15, 0xbfb8aa3b, v17
	v_exp_f32_e32 v22, v15
	v_mov_b32_e32 v15, v16
	v_pk_mul_f32 v[14:15], v[14:15], v[20:21]
	v_mul_f32_e32 v20, 0xbfb8aa3b, v10
	v_cvt_pk_f16_f32 v15, v14, v15
	v_add_f32_e32 v14, 1.0, v22
	v_rcp_f32_e32 v16, v14
	v_exp_f32_e32 v20, v20
	v_pack_b32_f16 v14, v26, v15
	v_lshl_add_u64 v[0:1], s[0:1], 0, v[0:1]
	v_fma_mixlo_f16 v16, v17, v16, 0
	v_alignbit_b32 v15, v16, v15, 16
	ds_write_b64 v27, v[14:15] offset:32
	v_add_f32_e32 v14, 1.0, v20
	v_mul_f32_e32 v15, 0xbfb8aa3b, v11
	v_rcp_f32_e32 v14, v14
	v_exp_f32_e32 v15, v15
	v_mul_f32_e32 v16, 0xbfb8aa3b, v12
	v_exp_f32_e32 v16, v16
	v_fma_mixlo_f16 v17, v10, v14, 0
	v_add_f32_e32 v10, 1.0, v15
	v_rcp_f32_e32 v14, v10
	v_add_f32_e32 v10, 1.0, v16
	v_rcp_f32_e32 v15, v10
	v_mov_b32_e32 v10, v11
	v_mul_f32_e32 v11, 0xbfb8aa3b, v13
	v_exp_f32_e32 v16, v11
	v_mov_b32_e32 v11, v12
	v_pk_mul_f32 v[10:11], v[10:11], v[14:15]
	v_mul_f32_e32 v14, 0xbfb8aa3b, v6
	v_cvt_pk_f16_f32 v11, v10, v11
	v_add_f32_e32 v10, 1.0, v16
	v_rcp_f32_e32 v12, v10
	v_exp_f32_e32 v14, v14
	v_pack_b32_f16 v10, v17, v11
	v_fma_mixlo_f16 v12, v13, v12, 0
	v_alignbit_b32 v11, v12, v11, 16
	ds_write_b64 v24, v[10:11] offset:32
	v_add_f32_e32 v10, 1.0, v14
	v_mul_f32_e32 v11, 0xbfb8aa3b, v7
	v_rcp_f32_e32 v10, v10
	v_exp_f32_e32 v11, v11
	v_mul_f32_e32 v12, 0xbfb8aa3b, v8
	v_exp_f32_e32 v12, v12
	v_fma_mixlo_f16 v13, v6, v10, 0
	v_add_f32_e32 v6, 1.0, v11
	v_rcp_f32_e32 v10, v6
	v_add_f32_e32 v6, 1.0, v12
	v_rcp_f32_e32 v11, v6
	v_mov_b32_e32 v6, v7
	v_mul_f32_e32 v7, 0xbfb8aa3b, v9
	v_exp_f32_e32 v12, v7
	v_mov_b32_e32 v7, v8
	v_pk_mul_f32 v[6:7], v[6:7], v[10:11]
	v_mul_f32_e32 v10, 0xbfb8aa3b, v2
	v_cvt_pk_f16_f32 v7, v6, v7
	v_add_f32_e32 v6, 1.0, v12
	v_rcp_f32_e32 v8, v6
	v_exp_f32_e32 v10, v10
	v_pack_b32_f16 v6, v13, v7
	v_fma_mixlo_f16 v8, v9, v8, 0
	v_alignbit_b32 v7, v8, v7, 16
	ds_write_b64 v25, v[6:7] offset:32
	v_add_f32_e32 v6, 1.0, v10
	v_mul_f32_e32 v7, 0xbfb8aa3b, v3
	v_rcp_f32_e32 v6, v6
	v_exp_f32_e32 v7, v7
	v_mul_f32_e32 v8, 0xbfb8aa3b, v4
	v_exp_f32_e32 v8, v8
	v_fma_mixlo_f16 v9, v2, v6, 0
	v_add_f32_e32 v2, 1.0, v7
	v_mul_f32_e32 v7, 0xbfb8aa3b, v5
	v_rcp_f32_e32 v6, v2
	v_add_f32_e32 v2, 1.0, v8
	v_exp_f32_e32 v8, v7
	v_rcp_f32_e32 v7, v2
	v_mov_b32_e32 v2, v3
	v_mov_b32_e32 v3, v4
	v_add_f32_e32 v4, 1.0, v8
	v_rcp_f32_e32 v4, v4
	v_pk_mul_f32 v[2:3], v[2:3], v[6:7]
	v_fma_mixlo_f16 v4, v5, v4, 0
	v_cvt_pk_f16_f32 v3, v2, v3
	v_pack_b32_f16 v2, v9, v3
	v_alignbit_b32 v3, v4, v3, 16
	ds_write_b64 v23, v[2:3] offset:32
	s_waitcnt lgkmcnt(0)
	s_barrier
	ds_read_b128 v[2:5], v52 offset:40960
	ds_read_b128 v[6:9], v52 offset:40976
	ds_read_b128 v[10:13], v52 offset:40992
	ds_read_b128 v[14:17], v52 offset:41008
	s_waitcnt lgkmcnt(3)
	global_store_dwordx4 v[0:1], v[2:5], off sc0 sc1
	s_nop 1
	v_add_co_u32_e32 v2, vcc, 0x2000, v0
	s_nop 1
	v_addc_co_u32_e32 v3, vcc, 0, v1, vcc
	v_add_co_u32_e32 v0, vcc, 0x6000, v0
	s_waitcnt lgkmcnt(2)
	global_store_dwordx4 v[2:3], v[6:9], off sc0 sc1
	v_lshl_add_u64 v[2:3], s[0:1], 0, v[18:19]
	v_addc_co_u32_e32 v1, vcc, 0, v1, vcc
	s_waitcnt lgkmcnt(1)
	global_store_dwordx4 v[2:3], v[10:13], off sc0 sc1
	s_waitcnt lgkmcnt(0)
	global_store_dwordx4 v[0:1], v[14:17], off sc0 sc1
	s_endpgm
	.p2align	8

	.amdhsa_kernel _Z4k_k2ILb0EEvPKDF16_S1_PKfS3_S3_S1_S1_PfS3_S3_S1_PDF16_PKiS4_S4_
		.amdhsa_group_segment_fixed_size 98816
		.amdhsa_private_segment_fixed_size 0
		.amdhsa_kernarg_size 120
		.amdhsa_user_sgpr_count 2
		.amdhsa_user_sgpr_dispatch_ptr 0
		.amdhsa_user_sgpr_queue_ptr 0
		.amdhsa_user_sgpr_kernarg_segment_ptr 1
		.amdhsa_user_sgpr_dispatch_id 0
		.amdhsa_user_sgpr_kernarg_preload_length 0
		.amdhsa_user_sgpr_kernarg_preload_offset 0
		.amdhsa_user_sgpr_private_segment_size 0
		.amdhsa_uses_dynamic_stack 0
		.amdhsa_enable_private_segment 0
		.amdhsa_system_sgpr_workgroup_id_x 1
		.amdhsa_system_sgpr_workgroup_id_y 0
		.amdhsa_system_sgpr_workgroup_id_z 0
		.amdhsa_system_sgpr_workgroup_info 0
		.amdhsa_system_vgpr_workitem_id 0
		.amdhsa_next_free_vgpr 232
		.amdhsa_next_free_sgpr 100
		.amdhsa_accum_offset 232
		.amdhsa_reserve_vcc 1
		.amdhsa_float_round_mode_32 0
		.amdhsa_float_round_mode_16_64 0
		.amdhsa_float_denorm_mode_32 3
		.amdhsa_float_denorm_mode_16_64 3
		.amdhsa_dx10_clamp 1
		.amdhsa_ieee_mode 1
		.amdhsa_fp16_overflow 0
		.amdhsa_tg_split 0
		.amdhsa_exception_fp_ieee_invalid_op 0
		.amdhsa_exception_fp_denorm_src 0
		.amdhsa_exception_fp_ieee_div_zero 0
		.amdhsa_exception_fp_ieee_overflow 0
		.amdhsa_exception_fp_ieee_underflow 0
		.amdhsa_exception_fp_ieee_inexact 0
		.amdhsa_exception_int_div_zero 0
	.end_amdhsa_kernel

amdhsa.kernels:
  - .agpr_count:     0
    .args:
      - .actual_access:  read_only
        .address_space:  global
        .offset:         0
        .size:           8
        .value_kind:     global_buffer
      - .actual_access:  write_only
        .address_space:  global
        .offset:         8
        .size:           8
        .value_kind:     global_buffer
      - .offset:         16
        .size:           4
        .value_kind:     by_value
      - .offset:         20
        .size:           4
        .value_kind:     by_value
      - .actual_access:  read_only
        .address_space:  global
        .offset:         24
        .size:           8
        .value_kind:     global_buffer
      - .actual_access:  write_only
        .address_space:  global
        .offset:         32
        .size:           8
        .value_kind:     global_buffer
      - .offset:         40
        .size:           4
        .value_kind:     by_value
      - .offset:         44
        .size:           4
        .value_kind:     by_value
      - .actual_access:  read_only
        .address_space:  global
        .offset:         48
        .size:           8
        .value_kind:     global_buffer
      - .actual_access:  write_only
        .address_space:  global
        .offset:         56
        .size:           8
        .value_kind:     global_buffer
      - .offset:         64
        .size:           4
        .value_kind:     by_value
      - .offset:         68
        .size:           4
        .value_kind:     by_value
      - .actual_access:  read_only
        .address_space:  global
        .offset:         72
        .size:           8
        .value_kind:     global_buffer
      - .actual_access:  write_only
        .address_space:  global
        .offset:         80
        .size:           8
        .value_kind:     global_buffer
      - .offset:         88
        .size:           4
        .value_kind:     by_value
      - .actual_access:  read_only
        .address_space:  global
        .offset:         96
        .size:           8
        .value_kind:     global_buffer
      - .actual_access:  write_only
        .address_space:  global
        .offset:         104
        .size:           8
        .value_kind:     global_buffer
      - .offset:         112
        .size:           4
        .value_kind:     by_value
      - .offset:         120
        .size:           4
        .value_kind:     hidden_block_count_x
      - .offset:         124
        .size:           4
        .value_kind:     hidden_block_count_y
      - .offset:         128
        .size:           4
        .value_kind:     hidden_block_count_z
      - .offset:         132
        .size:           2
        .value_kind:     hidden_group_size_x
      - .offset:         134
        .size:           2
        .value_kind:     hidden_group_size_y
      - .offset:         136
        .size:           2
        .value_kind:     hidden_group_size_z
      - .offset:         138
        .size:           2
        .value_kind:     hidden_remainder_x
      - .offset:         140
        .size:           2
        .value_kind:     hidden_remainder_y
      - .offset:         142
        .size:           2
        .value_kind:     hidden_remainder_z
      - .offset:         160
        .size:           8
        .value_kind:     hidden_global_offset_x
      - .offset:         168
        .size:           8
        .value_kind:     hidden_global_offset_y
      - .offset:         176
        .size:           8
        .value_kind:     hidden_global_offset_z
      - .offset:         184
        .size:           2
        .value_kind:     hidden_grid_dims
    .group_segment_fixed_size: 0
    .kernarg_segment_align: 8
    .kernarg_segment_size: 376
    .language:       OpenCL C
    .language_version:
      - 2
      - 0
    .max_flat_workgroup_size: 1024
    .name:           _Z5k_swzPKfPDF16_iiS0_S1_iiS0_S1_iiS0_PfiS0_S1_i
    .private_segment_fixed_size: 0
    .sgpr_count:     32
    .sgpr_spill_count: 0
    .symbol:         _Z5k_swzPKfPDF16_iiS0_S1_iiS0_S1_iiS0_PfiS0_S1_i.kd
    .uniform_work_group_size: 1
    .uses_dynamic_stack: false
    .vgpr_count:     14
    .vgpr_spill_count: 0
    .wavefront_size: 64
  - .agpr_count:     0
    .args:
      - .actual_access:  read_only
        .address_space:  global
        .offset:         0
        .size:           8
        .value_kind:     global_buffer
      - .actual_access:  read_only
        .address_space:  global
        .offset:         8
        .size:           8
        .value_kind:     global_buffer
      - .actual_access:  write_only
        .address_space:  global
        .offset:         16
        .size:           8
        .value_kind:     global_buffer
      - .actual_access:  read_only
        .address_space:  global
        .offset:         24
        .size:           8
        .value_kind:     global_buffer
      - .actual_access:  read_only
        .address_space:  global
        .offset:         32
        .size:           8
        .value_kind:     global_buffer
      - .actual_access:  read_only
        .address_space:  global
        .offset:         40
        .size:           8
        .value_kind:     global_buffer
      - .actual_access:  write_only
        .address_space:  global
        .offset:         48
        .size:           8
        .value_kind:     global_buffer
    .group_segment_fixed_size: 98816
    .kernarg_segment_align: 8
    .kernarg_segment_size: 56
    .language:       OpenCL C
    .language_version:
      - 2
      - 0
    .max_flat_workgroup_size: 512
    .name:           _Z10k_ka_firstPKfPKiPfS0_S0_PKDF16_PDF16_
    .private_segment_fixed_size: 0
    .sgpr_count:     59
    .sgpr_spill_count: 0
    .symbol:         _Z10k_ka_firstPKfPKiPfS0_S0_PKDF16_PDF16_.kd
    .uniform_work_group_size: 1
    .uses_dynamic_stack: false
    .vgpr_count:     174
    .vgpr_spill_count: 0
    .wavefront_size: 64
  - .agpr_count:     0
    .args:
      - .actual_access:  read_only
        .address_space:  global
        .offset:         0
        .size:           8
        .value_kind:     global_buffer
      - .actual_access:  read_only
        .address_space:  global
        .offset:         8
        .size:           8
        .value_kind:     global_buffer
      - .actual_access:  read_only
        .address_space:  global
        .offset:         16
        .size:           8
        .value_kind:     global_buffer
      - .actual_access:  read_only
        .address_space:  global
        .offset:         24
        .size:           8
        .value_kind:     global_buffer
      - .actual_access:  read_only
        .address_space:  global
        .offset:         32
        .size:           8
        .value_kind:     global_buffer
      - .actual_access:  read_only
        .address_space:  global
        .offset:         40
        .size:           8
        .value_kind:     global_buffer
      - .actual_access:  write_only
        .address_space:  global
        .offset:         48
        .size:           8
        .value_kind:     global_buffer
      - .actual_access:  write_only
        .address_space:  global
        .offset:         56
        .size:           8
        .value_kind:     global_buffer
      - .actual_access:  write_only
        .address_space:  global
        .offset:         64
        .size:           8
        .value_kind:     global_buffer
      - .actual_access:  read_only
        .address_space:  global
        .offset:         72
        .size:           8
        .value_kind:     global_buffer
      - .actual_access:  write_only
        .address_space:  global
        .offset:         80
        .size:           8
        .value_kind:     global_buffer
      - .actual_access:  write_only
        .address_space:  global
        .offset:         88
        .size:           8
        .value_kind:     global_buffer
    .group_segment_fixed_size: 47616
    .kernarg_segment_align: 8
    .kernarg_segment_size: 96
    .language:       OpenCL C
    .language_version:
      - 2
      - 0
    .max_flat_workgroup_size: 512
    .name:           _Z12k_conv_xprojPKDF16_PKfS2_S0_S0_S2_PDF16_S3_PfS2_S3_S4_
    .private_segment_fixed_size: 0
    .sgpr_count:     32
    .sgpr_spill_count: 0
    .symbol:         _Z12k_conv_xprojPKDF16_PKfS2_S0_S0_S2_PDF16_S3_PfS2_S3_S4_.kd
    .uniform_work_group_size: 1
    .uses_dynamic_stack: false
    .vgpr_count:     160
    .vgpr_spill_count: 0
    .wavefront_size: 64
  - .agpr_count:     0
    .args:
      - .actual_access:  read_only
        .address_space:  global
        .offset:         0
        .size:           8
        .value_kind:     global_buffer
      - .actual_access:  read_only
        .address_space:  global
        .offset:         8
        .size:           8
        .value_kind:     global_buffer
      - .actual_access:  read_only
        .address_space:  global
        .offset:         16
        .size:           8
        .value_kind:     global_buffer
      - .actual_access:  write_only
        .address_space:  global
        .offset:         24
        .size:           8
        .value_kind:     global_buffer
    .group_segment_fixed_size: 16384
    .kernarg_segment_align: 8
    .kernarg_segment_size: 32
    .language:       OpenCL C
    .language_version:
      - 2
      - 0
    .max_flat_workgroup_size: 512
    .name:           _Z11k_scan_combPKDF16_PKfS2_PDF16_
    .private_segment_fixed_size: 0
    .sgpr_count:     18
    .sgpr_spill_count: 0
    .symbol:         _Z11k_scan_combPKDF16_PKfS2_PDF16_.kd
    .uniform_work_group_size: 1
    .uses_dynamic_stack: false
    .vgpr_count:     120
    .vgpr_spill_count: 0
    .wavefront_size: 64
  - .agpr_count:     0
    .args:
      - .actual_access:  read_only
        .address_space:  global
        .offset:         0
        .size:           8
        .value_kind:     global_buffer
      - .actual_access:  read_only
        .address_space:  global
        .offset:         8
        .size:           8
        .value_kind:     global_buffer
      - .actual_access:  read_only
        .address_space:  global
        .offset:         16
        .size:           8
        .value_kind:     global_buffer
      - .actual_access:  read_only
        .address_space:  global
        .offset:         24
        .size:           8
        .value_kind:     global_buffer
      - .actual_access:  write_only
        .address_space:  global
        .offset:         32
        .size:           8
        .value_kind:     global_buffer
    .group_segment_fixed_size: 32
    .kernarg_segment_align: 8
    .kernarg_segment_size: 40
    .language:       OpenCL C
    .language_version:
      - 2
      - 0
    .max_flat_workgroup_size: 256
    .name:           _Z6k_headPKfS0_S0_S0_Pf
    .private_segment_fixed_size: 0
    .sgpr_count:     86
    .sgpr_spill_count: 0
    .symbol:         _Z6k_headPKfS0_S0_S0_Pf.kd
    .uniform_work_group_size: 1
    .uses_dynamic_stack: false
    .vgpr_count:     92
    .vgpr_spill_count: 0
    .wavefront_size: 64
  - .agpr_count:     0
    .args:
      - .actual_access:  read_only
        .address_space:  global
        .offset:         0
        .size:           8
        .value_kind:     global_buffer
      - .actual_access:  read_only
        .address_space:  global
        .offset:         8
        .size:           8
        .value_kind:     global_buffer
      - .actual_access:  read_only
        .address_space:  global
        .offset:         16
        .size:           8
        .value_kind:     global_buffer
      - .actual_access:  read_only
        .address_space:  global
        .offset:         24
        .size:           8
        .value_kind:     global_buffer
      - .actual_access:  read_only
        .address_space:  global
        .offset:         32
        .size:           8
        .value_kind:     global_buffer
      - .actual_access:  read_only
        .address_space:  global
        .offset:         40
        .size:           8
        .value_kind:     global_buffer
      - .actual_access:  read_only
        .address_space:  global
        .offset:         48
        .size:           8
        .value_kind:     global_buffer
      - .address_space:  global
        .offset:         56
        .size:           8
        .value_kind:     global_buffer
      - .actual_access:  read_only
        .address_space:  global
        .offset:         64
        .size:           8
        .value_kind:     global_buffer
      - .actual_access:  read_only
        .address_space:  global
        .offset:         72
        .size:           8
        .value_kind:     global_buffer
      - .actual_access:  read_only
        .address_space:  global
        .offset:         80
        .size:           8
        .value_kind:     global_buffer
      - .address_space:  global
        .offset:         88
        .size:           8
        .value_kind:     global_buffer
      - .actual_access:  read_only
        .address_space:  global
        .offset:         96
        .size:           8
        .value_kind:     global_buffer
      - .actual_access:  read_only
        .address_space:  global
        .offset:         104
        .size:           8
        .value_kind:     global_buffer
      - .actual_access:  read_only
        .address_space:  global
        .offset:         112
        .size:           8
        .value_kind:     global_buffer
    .group_segment_fixed_size: 98816
    .kernarg_segment_align: 8
    .kernarg_segment_size: 120
    .language:       OpenCL C
    .language_version:
      - 2
      - 0
    .max_flat_workgroup_size: 512
    .name:           _Z4k_k2ILb0EEvPKDF16_S1_PKfS3_S3_S1_S1_PfS3_S3_S1_PDF16_PKiS4_S4_
    .private_segment_fixed_size: 0
    .sgpr_count:     106
    .sgpr_spill_count: 0
    .symbol:         _Z4k_k2ILb0EEvPKDF16_S1_PKfS3_S3_S1_S1_PfS3_S3_S1_PDF16_PKiS4_S4_.kd
    .uniform_work_group_size: 1
    .uses_dynamic_stack: false
    .vgpr_count:     232
    .vgpr_spill_count: 0
    .wavefront_size: 64
  - .agpr_count:     0
    .args:
      - .actual_access:  read_only
        .address_space:  global
        .offset:         0
        .size:           8
        .value_kind:     global_buffer
      - .actual_access:  read_only
        .address_space:  global
        .offset:         8
        .size:           8
        .value_kind:     global_buffer
      - .actual_access:  read_only
        .address_space:  global
        .offset:         16
        .size:           8
        .value_kind:     global_buffer
      - .actual_access:  read_only
        .address_space:  global
        .offset:         24
        .size:           8
        .value_kind:     global_buffer
      - .actual_access:  read_only
        .address_space:  global
        .offset:         32
        .size:           8
        .value_kind:     global_buffer
      - .actual_access:  read_only
        .address_space:  global
        .offset:         40
        .size:           8
        .value_kind:     global_buffer
      - .actual_access:  read_only
        .address_space:  global
        .offset:         48
        .size:           8
        .value_kind:     global_buffer
      - .actual_access:  read_only
        .address_space:  global
        .offset:         56
        .size:           8
        .value_kind:     global_buffer
      - .actual_access:  read_only
        .address_space:  global
        .offset:         64
        .size:           8
        .value_kind:     global_buffer
      - .actual_access:  read_only
        .address_space:  global
        .offset:         72
        .size:           8
        .value_kind:     global_buffer
      - .actual_access:  read_only
        .address_space:  global
        .offset:         80
        .size:           8
        .value_kind:     global_buffer
      - .actual_access:  read_only
        .address_space:  global
        .offset:         88
        .size:           8
        .value_kind:     global_buffer
      - .actual_access:  read_only
        .address_space:  global
        .offset:         96
        .size:           8
        .value_kind:     global_buffer
      - .actual_access:  write_only
        .address_space:  global
        .offset:         104
        .size:           8
        .value_kind:     global_buffer
      - .actual_access:  write_only
        .address_space:  global
        .offset:         112
        .size:           8
        .value_kind:     global_buffer
    .group_segment_fixed_size: 98816
    .kernarg_segment_align: 8
    .kernarg_segment_size: 120
    .language:       OpenCL C
    .language_version:
      - 2
      - 0
    .max_flat_workgroup_size: 512
    .name:           _Z4k_k2ILb1EEvPKDF16_S1_PKfS3_S3_S1_S1_PfS3_S3_S1_PDF16_PKiS4_S4_
    .private_segment_fixed_size: 0
    .sgpr_count:     44
    .sgpr_spill_count: 0
    .symbol:         _Z4k_k2ILb1EEvPKDF16_S1_PKfS3_S3_S1_S1_PfS3_S3_S1_PDF16_PKiS4_S4_.kd
    .uniform_work_group_size: 1
    .uses_dynamic_stack: false
    .vgpr_count:     160
    .vgpr_spill_count: 0
    .wavefront_size: 64
